# GEMM K-loops: all per-segment s_setprio toggles removed (equal priority, age arbitration)
# baseline (speedup 1.0000x reference)
.LBB0_378:
	s_add_u32 s28, s36, 0xfff80080
	s_addc_u32 s29, s37, -1
	s_add_i32 s42, 0, 0x10000
	s_cmp_eq_u32 vcc_hi, 28
	s_cselect_b32 s53, s11, s29
	s_cselect_b32 s52, s21, s28
	s_cselect_b32 s51, s41, s79
	s_cselect_b32 s50, vcc_lo, s78
	s_add_i32 s43, 0, 0x14000
	v_add_u32_e32 v140, s42, v169
	v_add_u32_e32 v173, s43, v169
	ds_read_b128 v[128:131], v140
	ds_read_b128 v[132:135], v140 offset:1024
	ds_read_b128 v[136:139], v140 offset:2048
	ds_read_b128 v[140:143], v140 offset:3072
	ds_read_b128 v[156:159], v173
	ds_read_b128 v[160:163], v173 offset:1024
	ds_read_b128 v[164:167], v173 offset:2048
	ds_read_b128 v[174:177], v173 offset:3072
	v_lshl_add_u64 v[182:183], s[36:37], 0, v[152:153]
	s_add_i32 m0, s88, 0xc000
	ds_read_b128 v[178:181], v172
	ds_read_b128 v[194:197], v172 offset:1024
	ds_read_b128 v[198:201], v172 offset:2048
	ds_read_b128 v[202:205], v172 offset:3072
	ds_read_b128 v[206:209], v172 offset:4096
	ds_read_b128 v[224:227], v172 offset:5120
	ds_read_b128 v[228:231], v172 offset:6144
	ds_read_b128 v[232:235], v172 offset:7168
	global_load_lds_dwordx4 v[182:183], off
	v_lshl_add_u64 v[182:183], s[36:37], 0, v[154:155]
	s_add_i32 m0, s88, 0xe000
	s_nop 0
	global_load_lds_dwordx4 v[182:183], off
	s_waitcnt vmcnt(8)
	s_waitcnt lgkmcnt(0)
	s_barrier
	s_waitcnt lgkmcnt(0)
	v_mfma_f32_16x16x32_bf16 v[124:127], v[128:131], v[178:181], v[124:127]
	v_mfma_f32_16x16x32_bf16 v[120:123], v[136:139], v[178:181], v[120:123]
	v_mfma_f32_16x16x32_bf16 v[116:119], v[128:131], v[198:201], v[116:119]
	v_mfma_f32_16x16x32_bf16 v[108:111], v[136:139], v[198:201], v[108:111]
	v_mfma_f32_16x16x32_bf16 v[100:103], v[128:131], v[206:209], v[100:103]
	v_mfma_f32_16x16x32_bf16 v[92:95], v[136:139], v[206:209], v[92:95]
	v_mfma_f32_16x16x32_bf16 v[84:87], v[128:131], v[228:231], v[84:87]
	v_mfma_f32_16x16x32_bf16 v[76:79], v[136:139], v[228:231], v[76:79]
	v_mfma_f32_16x16x32_bf16 v[124:127], v[132:135], v[194:197], v[124:127]
	v_mfma_f32_16x16x32_bf16 v[120:123], v[140:143], v[194:197], v[120:123]
	v_mfma_f32_16x16x32_bf16 v[116:119], v[132:135], v[202:205], v[116:119]
	v_mfma_f32_16x16x32_bf16 v[108:111], v[140:143], v[202:205], v[108:111]
	v_mfma_f32_16x16x32_bf16 v[100:103], v[132:135], v[224:227], v[100:103]
	v_mfma_f32_16x16x32_bf16 v[92:95], v[140:143], v[224:227], v[92:95]
	v_mfma_f32_16x16x32_bf16 v[84:87], v[132:135], v[232:235], v[84:87]
	v_mfma_f32_16x16x32_bf16 v[76:79], v[140:143], v[232:235], v[76:79]
	v_mfma_f32_16x16x32_bf16 v[112:115], v[156:159], v[178:181], v[112:115]
	v_mfma_f32_16x16x32_bf16 v[104:107], v[164:167], v[178:181], v[104:107]
	v_mfma_f32_16x16x32_bf16 v[96:99], v[156:159], v[198:201], v[96:99]
	v_mfma_f32_16x16x32_bf16 v[88:91], v[164:167], v[198:201], v[88:91]
	v_mfma_f32_16x16x32_bf16 v[80:83], v[156:159], v[206:209], v[80:83]
	v_mfma_f32_16x16x32_bf16 v[72:75], v[164:167], v[206:209], v[72:75]
	v_mfma_f32_16x16x32_bf16 v[68:71], v[156:159], v[228:231], v[68:71]
	v_mfma_f32_16x16x32_bf16 v[64:67], v[164:167], v[228:231], v[64:67]
	v_mfma_f32_16x16x32_bf16 v[112:115], v[160:163], v[194:197], v[112:115]
	v_mfma_f32_16x16x32_bf16 v[104:107], v[174:177], v[194:197], v[104:107]
	v_mfma_f32_16x16x32_bf16 v[96:99], v[160:163], v[202:205], v[96:99]
	v_mfma_f32_16x16x32_bf16 v[88:91], v[174:177], v[202:205], v[88:91]
	v_mfma_f32_16x16x32_bf16 v[80:83], v[160:163], v[224:227], v[80:83]
	v_mfma_f32_16x16x32_bf16 v[72:75], v[174:177], v[224:227], v[72:75]
	v_mfma_f32_16x16x32_bf16 v[68:71], v[160:163], v[232:235], v[68:71]
	v_mfma_f32_16x16x32_bf16 v[64:67], v[174:177], v[232:235], v[64:67]
	s_barrier
	s_add_i32 s28, s42, s62
	v_lshl_add_u64 v[182:183], s[50:51], 0, v[146:147]
	s_mov_b32 m0, s28
	ds_read_b128 v[178:181], v172 offset:16384
	ds_read_b128 v[194:197], v172 offset:17408
	ds_read_b128 v[198:201], v172 offset:18432
	ds_read_b128 v[202:205], v172 offset:19456
	ds_read_b128 v[206:209], v172 offset:20480
	ds_read_b128 v[224:227], v172 offset:21504
	ds_read_b128 v[228:231], v172 offset:22528
	ds_read_b128 v[232:235], v172 offset:23552
	global_load_lds_dwordx4 v[182:183], off
	s_add_i32 m0, s28, 0x2000
	s_add_u32 s28, s50, 0x80000
	v_lshl_add_u64 v[210:211], s[50:51], 0, v[150:151]
	s_addc_u32 s29, s51, 0
	s_add_i32 s42, s43, s62
	global_load_lds_dwordx4 v[210:211], off
	v_lshl_add_u64 v[236:237], s[28:29], 0, v[146:147]
	s_mov_b32 m0, s42
	v_lshl_add_u64 v[238:239], s[52:53], 0, v[148:149]
	global_load_lds_dwordx4 v[236:237], off
	v_lshl_add_u64 v[236:237], s[28:29], 0, v[150:151]
	s_add_i32 m0, s42, 0x2000
	s_nop 0
	global_load_lds_dwordx4 v[236:237], off
	v_lshl_add_u64 v[236:237], s[52:53], 0, v[144:145]
	s_mov_b32 m0, s88
	s_nop 0
	global_load_lds_dwordx4 v[236:237], off
	s_mov_b32 m0, s89
	s_nop 0
	global_load_lds_dwordx4 v[238:239], off
	s_waitcnt vmcnt(8)
	s_waitcnt lgkmcnt(0)
	s_barrier
	s_waitcnt lgkmcnt(0)
	v_mfma_f32_16x16x32_bf16 v[60:63], v[128:131], v[178:181], v[60:63]
	v_mfma_f32_16x16x32_bf16 v[56:59], v[136:139], v[178:181], v[56:59]
	v_mfma_f32_16x16x32_bf16 v[52:55], v[128:131], v[198:201], v[52:55]
	v_mfma_f32_16x16x32_bf16 v[44:47], v[136:139], v[198:201], v[44:47]
	v_mfma_f32_16x16x32_bf16 v[36:39], v[128:131], v[206:209], v[36:39]
	v_mfma_f32_16x16x32_bf16 v[28:31], v[136:139], v[206:209], v[28:31]
	v_mfma_f32_16x16x32_bf16 v[20:23], v[128:131], v[228:231], v[20:23]
	v_mfma_f32_16x16x32_bf16 v[12:15], v[136:139], v[228:231], v[12:15]
	v_mfma_f32_16x16x32_bf16 v[60:63], v[132:135], v[194:197], v[60:63]
	v_mfma_f32_16x16x32_bf16 v[56:59], v[140:143], v[194:197], v[56:59]
	v_mfma_f32_16x16x32_bf16 v[52:55], v[132:135], v[202:205], v[52:55]
	v_mfma_f32_16x16x32_bf16 v[44:47], v[140:143], v[202:205], v[44:47]
	v_mfma_f32_16x16x32_bf16 v[36:39], v[132:135], v[224:227], v[36:39]
	v_mfma_f32_16x16x32_bf16 v[28:31], v[140:143], v[224:227], v[28:31]
	v_mfma_f32_16x16x32_bf16 v[20:23], v[132:135], v[232:235], v[20:23]
	v_mfma_f32_16x16x32_bf16 v[12:15], v[140:143], v[232:235], v[12:15]
	v_mfma_f32_16x16x32_bf16 v[48:51], v[156:159], v[178:181], v[48:51]
	v_mfma_f32_16x16x32_bf16 v[40:43], v[164:167], v[178:181], v[40:43]
	v_mfma_f32_16x16x32_bf16 v[32:35], v[156:159], v[198:201], v[32:35]
	v_mfma_f32_16x16x32_bf16 v[24:27], v[164:167], v[198:201], v[24:27]
	v_mfma_f32_16x16x32_bf16 v[16:19], v[156:159], v[206:209], v[16:19]
	v_mfma_f32_16x16x32_bf16 v[8:11], v[164:167], v[206:209], v[8:11]
	v_mfma_f32_16x16x32_bf16 v[4:7], v[156:159], v[228:231], v[4:7]
	v_mfma_f32_16x16x32_bf16 v[0:3], v[164:167], v[228:231], v[0:3]
	v_mfma_f32_16x16x32_bf16 v[48:51], v[160:163], v[194:197], v[48:51]
	v_mfma_f32_16x16x32_bf16 v[40:43], v[174:177], v[194:197], v[40:43]
	v_mfma_f32_16x16x32_bf16 v[32:35], v[160:163], v[202:205], v[32:35]
	v_mfma_f32_16x16x32_bf16 v[24:27], v[174:177], v[202:205], v[24:27]
	v_mfma_f32_16x16x32_bf16 v[16:19], v[160:163], v[224:227], v[16:19]
	v_mfma_f32_16x16x32_bf16 v[8:11], v[174:177], v[224:227], v[8:11]
	v_mfma_f32_16x16x32_bf16 v[4:7], v[160:163], v[232:235], v[4:7]
	v_mfma_f32_16x16x32_bf16 v[0:3], v[174:177], v[232:235], v[0:3]
	s_barrier
	s_add_i32 s42, 0, 0x18000
	s_add_i32 s43, 0, 0x1c000
	v_add_u32_e32 v140, s42, v169
	v_add_u32_e32 v173, s43, v169
	ds_read_b128 v[128:131], v140
	ds_read_b128 v[132:135], v140 offset:1024
	ds_read_b128 v[136:139], v140 offset:2048
	ds_read_b128 v[140:143], v140 offset:3072
	ds_read_b128 v[156:159], v173
	ds_read_b128 v[160:163], v173 offset:1024
	ds_read_b128 v[164:167], v173 offset:2048
	ds_read_b128 v[174:177], v173 offset:3072
	s_add_u32 s28, s52, 0x80000
	s_addc_u32 s29, s53, 0
	s_mov_b32 m0, s26
	v_lshl_add_u64 v[240:241], s[28:29], 0, v[144:145]
	ds_read_b128 v[178:181], v172 offset:32768
	ds_read_b128 v[194:197], v172 offset:33792
	ds_read_b128 v[198:201], v172 offset:34816
	ds_read_b128 v[202:205], v172 offset:35840
	ds_read_b128 v[206:209], v172 offset:36864
	ds_read_b128 v[224:227], v172 offset:37888
	ds_read_b128 v[228:231], v172 offset:38912
	ds_read_b128 v[232:235], v172 offset:39936
	global_load_lds_dwordx4 v[240:241], off
	v_lshl_add_u64 v[240:241], s[28:29], 0, v[148:149]
	s_mov_b32 m0, s27
	s_nop 0
	global_load_lds_dwordx4 v[240:241], off
	s_waitcnt vmcnt(8)
	s_waitcnt lgkmcnt(0)
	s_barrier
	s_waitcnt lgkmcnt(0)
	v_mfma_f32_16x16x32_bf16 v[124:127], v[128:131], v[178:181], v[124:127]
	v_mfma_f32_16x16x32_bf16 v[120:123], v[136:139], v[178:181], v[120:123]
	v_mfma_f32_16x16x32_bf16 v[116:119], v[128:131], v[198:201], v[116:119]
	v_mfma_f32_16x16x32_bf16 v[108:111], v[136:139], v[198:201], v[108:111]
	v_mfma_f32_16x16x32_bf16 v[100:103], v[128:131], v[206:209], v[100:103]
	v_mfma_f32_16x16x32_bf16 v[92:95], v[136:139], v[206:209], v[92:95]
	v_mfma_f32_16x16x32_bf16 v[84:87], v[128:131], v[228:231], v[84:87]
	v_mfma_f32_16x16x32_bf16 v[76:79], v[136:139], v[228:231], v[76:79]
	v_mfma_f32_16x16x32_bf16 v[124:127], v[132:135], v[194:197], v[124:127]
	v_mfma_f32_16x16x32_bf16 v[120:123], v[140:143], v[194:197], v[120:123]
	v_mfma_f32_16x16x32_bf16 v[116:119], v[132:135], v[202:205], v[116:119]
	v_mfma_f32_16x16x32_bf16 v[108:111], v[140:143], v[202:205], v[108:111]
	v_mfma_f32_16x16x32_bf16 v[100:103], v[132:135], v[224:227], v[100:103]
	v_mfma_f32_16x16x32_bf16 v[92:95], v[140:143], v[224:227], v[92:95]
	v_mfma_f32_16x16x32_bf16 v[84:87], v[132:135], v[232:235], v[84:87]
	v_mfma_f32_16x16x32_bf16 v[76:79], v[140:143], v[232:235], v[76:79]
	v_mfma_f32_16x16x32_bf16 v[112:115], v[156:159], v[178:181], v[112:115]
	v_mfma_f32_16x16x32_bf16 v[104:107], v[164:167], v[178:181], v[104:107]
	v_mfma_f32_16x16x32_bf16 v[96:99], v[156:159], v[198:201], v[96:99]
	v_mfma_f32_16x16x32_bf16 v[88:91], v[164:167], v[198:201], v[88:91]
	v_mfma_f32_16x16x32_bf16 v[80:83], v[156:159], v[206:209], v[80:83]
	v_mfma_f32_16x16x32_bf16 v[72:75], v[164:167], v[206:209], v[72:75]
	v_mfma_f32_16x16x32_bf16 v[68:71], v[156:159], v[228:231], v[68:71]
	v_mfma_f32_16x16x32_bf16 v[64:67], v[164:167], v[228:231], v[64:67]
	v_mfma_f32_16x16x32_bf16 v[112:115], v[160:163], v[194:197], v[112:115]
	v_mfma_f32_16x16x32_bf16 v[104:107], v[174:177], v[194:197], v[104:107]
	v_mfma_f32_16x16x32_bf16 v[96:99], v[160:163], v[202:205], v[96:99]
	v_mfma_f32_16x16x32_bf16 v[88:91], v[174:177], v[202:205], v[88:91]
	v_mfma_f32_16x16x32_bf16 v[80:83], v[160:163], v[224:227], v[80:83]
	v_mfma_f32_16x16x32_bf16 v[72:75], v[174:177], v[224:227], v[72:75]
	v_mfma_f32_16x16x32_bf16 v[68:71], v[160:163], v[232:235], v[68:71]
	v_mfma_f32_16x16x32_bf16 v[64:67], v[174:177], v[232:235], v[64:67]
	s_barrier
	s_add_i32 s28, s42, s62
	v_lshl_add_u64 v[182:183], v[182:183], 0, s[68:69]
	s_mov_b32 m0, s28
	ds_read_b128 v[178:181], v172 offset:49152
	ds_read_b128 v[194:197], v172 offset:50176
	ds_read_b128 v[198:201], v172 offset:51200
	ds_read_b128 v[202:205], v172 offset:52224
	ds_read_b128 v[206:209], v172 offset:53248
	ds_read_b128 v[224:227], v172 offset:54272
	ds_read_b128 v[228:231], v172 offset:55296
	ds_read_b128 v[232:235], v172 offset:56320
	global_load_lds_dwordx4 v[182:183], off
	s_add_i32 m0, s28, 0x2000
	s_add_u32 s28, s50, 0x80080
	v_lshl_add_u64 v[182:183], v[210:211], 0, s[68:69]
	s_addc_u32 s29, s51, 0
	s_add_i32 s42, s43, s62
	global_load_lds_dwordx4 v[182:183], off
	v_lshl_add_u64 v[182:183], s[28:29], 0, v[146:147]
	s_mov_b32 m0, s42
	s_nop 0
	global_load_lds_dwordx4 v[182:183], off
	v_lshl_add_u64 v[182:183], s[28:29], 0, v[150:151]
	s_add_i32 m0, s42, 0x2000
	s_nop 0
	global_load_lds_dwordx4 v[182:183], off
	v_lshl_add_u64 v[182:183], v[236:237], 0, s[68:69]
	s_mov_b32 m0, s94
	s_nop 0
	global_load_lds_dwordx4 v[182:183], off
	v_lshl_add_u64 v[182:183], v[238:239], 0, s[68:69]
	s_mov_b32 m0, s95
	s_nop 0
	global_load_lds_dwordx4 v[182:183], off
	s_waitcnt vmcnt(8)
	s_waitcnt lgkmcnt(0)
	s_barrier
	s_waitcnt lgkmcnt(0)
	v_mfma_f32_16x16x32_bf16 v[60:63], v[128:131], v[178:181], v[60:63]
	v_mfma_f32_16x16x32_bf16 v[56:59], v[136:139], v[178:181], v[56:59]
	v_mfma_f32_16x16x32_bf16 v[52:55], v[128:131], v[198:201], v[52:55]
	v_mfma_f32_16x16x32_bf16 v[44:47], v[136:139], v[198:201], v[44:47]
	v_mfma_f32_16x16x32_bf16 v[36:39], v[128:131], v[206:209], v[36:39]
	v_mfma_f32_16x16x32_bf16 v[28:31], v[136:139], v[206:209], v[28:31]
	v_mfma_f32_16x16x32_bf16 v[20:23], v[128:131], v[228:231], v[20:23]
	v_mfma_f32_16x16x32_bf16 v[12:15], v[136:139], v[228:231], v[12:15]
	v_mfma_f32_16x16x32_bf16 v[60:63], v[132:135], v[194:197], v[60:63]
	v_mfma_f32_16x16x32_bf16 v[56:59], v[140:143], v[194:197], v[56:59]
	v_mfma_f32_16x16x32_bf16 v[52:55], v[132:135], v[202:205], v[52:55]
	v_mfma_f32_16x16x32_bf16 v[44:47], v[140:143], v[202:205], v[44:47]
	v_mfma_f32_16x16x32_bf16 v[36:39], v[132:135], v[224:227], v[36:39]
	v_mfma_f32_16x16x32_bf16 v[28:31], v[140:143], v[224:227], v[28:31]
	v_mfma_f32_16x16x32_bf16 v[20:23], v[132:135], v[232:235], v[20:23]
	v_mfma_f32_16x16x32_bf16 v[12:15], v[140:143], v[232:235], v[12:15]
	v_mfma_f32_16x16x32_bf16 v[48:51], v[156:159], v[178:181], v[48:51]
	v_mfma_f32_16x16x32_bf16 v[40:43], v[164:167], v[178:181], v[40:43]
	v_mfma_f32_16x16x32_bf16 v[32:35], v[156:159], v[198:201], v[32:35]
	v_mfma_f32_16x16x32_bf16 v[24:27], v[164:167], v[198:201], v[24:27]
	v_mfma_f32_16x16x32_bf16 v[16:19], v[156:159], v[206:209], v[16:19]
	v_mfma_f32_16x16x32_bf16 v[8:11], v[164:167], v[206:209], v[8:11]
	v_mfma_f32_16x16x32_bf16 v[4:7], v[156:159], v[228:231], v[4:7]
	v_mfma_f32_16x16x32_bf16 v[0:3], v[164:167], v[228:231], v[0:3]
	v_mfma_f32_16x16x32_bf16 v[48:51], v[160:163], v[194:197], v[48:51]
	v_mfma_f32_16x16x32_bf16 v[40:43], v[174:177], v[194:197], v[40:43]
	v_mfma_f32_16x16x32_bf16 v[32:35], v[160:163], v[202:205], v[32:35]
	v_mfma_f32_16x16x32_bf16 v[24:27], v[174:177], v[202:205], v[24:27]
	v_mfma_f32_16x16x32_bf16 v[16:19], v[160:163], v[224:227], v[16:19]
	v_mfma_f32_16x16x32_bf16 v[8:11], v[174:177], v[224:227], v[8:11]
	v_mfma_f32_16x16x32_bf16 v[4:7], v[160:163], v[232:235], v[4:7]
	v_mfma_f32_16x16x32_bf16 v[0:3], v[174:177], v[232:235], v[0:3]
	s_barrier
	s_add_i32 vcc_hi, vcc_hi, 2
	s_add_u32 s36, s36, 0x100
	s_addc_u32 s37, s37, 0
	s_add_u32 s78, s78, 0x100
	s_addc_u32 s79, s79, 0
	s_cmp_gt_u32 vcc_hi, 29
	s_cbranch_scc0 .LBB0_378
	s_and_b64 vcc, exec, s[14:15]
	s_cbranch_vccz .LBB0_381
	s_barrier

.LBB0_514:
	s_add_u32 s42, s30, s44
	s_addc_u32 s43, s31, 0
	s_add_u32 s40, s42, 0x100
	s_addc_u32 s41, s43, 0
	s_and_b64 s[28:29], s[38:39], exec
	s_cselect_b32 s41, s9, s41
	s_cselect_b32 s40, s63, s40
	s_add_u32 s28, s18, s44
	s_addc_u32 s29, s19, 0
	s_add_u32 s44, s28, 0x100
	s_addc_u32 s45, s29, 0
	s_add_i32 s76, 0, 0x10000
	s_and_b64 s[28:29], s[38:39], exec
	s_cselect_b32 s44, s79, s44
	s_cselect_b32 s45, s78, s45
	s_add_i32 s85, 0, 0x14000
	v_add_u32_e32 v158, s76, v136
	v_add_u32_e32 v174, s85, v136
	ds_read_b128 v[146:149], v158
	ds_read_b128 v[150:153], v158 offset:1024
	ds_read_b128 v[154:157], v158 offset:2048
	ds_read_b128 v[158:161], v158 offset:3072
	ds_read_b128 v[162:165], v174
	ds_read_b128 v[166:169], v174 offset:1024
	ds_read_b128 v[170:173], v174 offset:2048
	ds_read_b128 v[174:177], v174 offset:3072
	s_add_u32 s46, s42, 0x10080
	s_addc_u32 s47, s43, 0
	s_add_i32 s29, s76, s4
	s_add_i32 s43, s85, s4
	s_add_i32 m0, s20, 0xc000
	s_add_i32 s90, s20, 0xe000
	s_add_i32 s49, s29, 0x2000
	s_add_i32 s42, s43, 0x2000
	s_add_i32 s48, 0, 0x18000
	s_add_i32 s28, 0, 0x1c000
	s_add_u32 s38, s40, 0x10000
	s_addc_u32 s39, s41, 0
	s_add_i32 s88, s48, s4
	s_add_i32 s76, s28, s4
	s_add_i32 s89, s88, 0x2000
	s_add_i32 s85, s76, 0x2000
	v_lshl_add_u64 v[182:183], s[46:47], 0, v[134:135]
	ds_read_b128 v[178:181], v145
	ds_read_b128 v[194:197], v145 offset:1024
	ds_read_b128 v[198:201], v145 offset:2048
	ds_read_b128 v[202:205], v145 offset:3072
	ds_read_b128 v[206:209], v145 offset:4096
	ds_read_b128 v[224:227], v145 offset:5120
	ds_read_b128 v[228:231], v145 offset:6144
	ds_read_b128 v[232:235], v145 offset:7168
	global_load_lds_dwordx4 v[182:183], off
	v_lshl_add_u64 v[182:183], s[46:47], 0, v[130:131]
	s_mov_b32 m0, s90
	s_nop 0
	global_load_lds_dwordx4 v[182:183], off
	s_waitcnt vmcnt(8)
	s_waitcnt lgkmcnt(0)
	s_barrier
	s_waitcnt lgkmcnt(0)
	v_mfma_f32_16x16x32_bf16 v[124:127], v[146:149], v[178:181], v[124:127]
	v_mfma_f32_16x16x32_bf16 v[120:123], v[154:157], v[178:181], v[120:123]
	v_mfma_f32_16x16x32_bf16 v[112:115], v[146:149], v[198:201], v[112:115]
	v_mfma_f32_16x16x32_bf16 v[104:107], v[154:157], v[198:201], v[104:107]
	v_mfma_f32_16x16x32_bf16 v[96:99], v[146:149], v[206:209], v[96:99]
	v_mfma_f32_16x16x32_bf16 v[88:91], v[154:157], v[206:209], v[88:91]
	v_mfma_f32_16x16x32_bf16 v[80:83], v[146:149], v[228:231], v[80:83]
	v_mfma_f32_16x16x32_bf16 v[72:75], v[154:157], v[228:231], v[72:75]
	v_mfma_f32_16x16x32_bf16 v[124:127], v[150:153], v[194:197], v[124:127]
	v_mfma_f32_16x16x32_bf16 v[120:123], v[158:161], v[194:197], v[120:123]
	v_mfma_f32_16x16x32_bf16 v[112:115], v[150:153], v[202:205], v[112:115]
	v_mfma_f32_16x16x32_bf16 v[104:107], v[158:161], v[202:205], v[104:107]
	v_mfma_f32_16x16x32_bf16 v[96:99], v[150:153], v[224:227], v[96:99]
	v_mfma_f32_16x16x32_bf16 v[88:91], v[158:161], v[224:227], v[88:91]
	v_mfma_f32_16x16x32_bf16 v[80:83], v[150:153], v[232:235], v[80:83]
	v_mfma_f32_16x16x32_bf16 v[72:75], v[158:161], v[232:235], v[72:75]
	v_mfma_f32_16x16x32_bf16 v[116:119], v[162:165], v[178:181], v[116:119]
	v_mfma_f32_16x16x32_bf16 v[108:111], v[170:173], v[178:181], v[108:111]
	v_mfma_f32_16x16x32_bf16 v[100:103], v[162:165], v[198:201], v[100:103]
	v_mfma_f32_16x16x32_bf16 v[92:95], v[170:173], v[198:201], v[92:95]
	v_mfma_f32_16x16x32_bf16 v[84:87], v[162:165], v[206:209], v[84:87]
	v_mfma_f32_16x16x32_bf16 v[76:79], v[170:173], v[206:209], v[76:79]
	v_mfma_f32_16x16x32_bf16 v[68:71], v[162:165], v[228:231], v[68:71]
	v_mfma_f32_16x16x32_bf16 v[64:67], v[170:173], v[228:231], v[64:67]
	v_mfma_f32_16x16x32_bf16 v[116:119], v[166:169], v[194:197], v[116:119]
	v_mfma_f32_16x16x32_bf16 v[108:111], v[174:177], v[194:197], v[108:111]
	v_mfma_f32_16x16x32_bf16 v[100:103], v[166:169], v[202:205], v[100:103]
	v_mfma_f32_16x16x32_bf16 v[92:95], v[174:177], v[202:205], v[92:95]
	v_mfma_f32_16x16x32_bf16 v[84:87], v[166:169], v[224:227], v[84:87]
	v_mfma_f32_16x16x32_bf16 v[76:79], v[174:177], v[224:227], v[76:79]
	v_mfma_f32_16x16x32_bf16 v[68:71], v[166:169], v[232:235], v[68:71]
	v_mfma_f32_16x16x32_bf16 v[64:67], v[174:177], v[232:235], v[64:67]
	s_barrier
	s_mov_b32 m0, s29
	v_lshl_add_u64 v[182:183], s[44:45], 0, v[132:133]
	ds_read_b128 v[178:181], v145 offset:16384
	ds_read_b128 v[194:197], v145 offset:17408
	ds_read_b128 v[198:201], v145 offset:18432
	ds_read_b128 v[202:205], v145 offset:19456
	ds_read_b128 v[206:209], v145 offset:20480
	ds_read_b128 v[224:227], v145 offset:21504
	ds_read_b128 v[228:231], v145 offset:22528
	ds_read_b128 v[232:235], v145 offset:23552
	global_load_lds_dwordx4 v[182:183], off
	v_lshl_add_u64 v[210:211], s[44:45], 0, v[128:129]
	s_mov_b32 m0, s49
	v_lshl_add_u64 v[236:237], v[182:183], 0, s[70:71]
	global_load_lds_dwordx4 v[210:211], off
	s_mov_b32 m0, s43
	v_lshl_add_u64 v[238:239], s[40:41], 0, v[130:131]
	global_load_lds_dwordx4 v[236:237], off
	v_lshl_add_u64 v[236:237], v[210:211], 0, s[70:71]
	s_mov_b32 m0, s42
	s_nop 0
	global_load_lds_dwordx4 v[236:237], off
	v_lshl_add_u64 v[236:237], s[40:41], 0, v[134:135]
	s_mov_b32 m0, s20
	s_nop 0
	global_load_lds_dwordx4 v[236:237], off
	s_mov_b32 m0, s21
	s_nop 0
	global_load_lds_dwordx4 v[238:239], off
	s_waitcnt vmcnt(8)
	s_waitcnt lgkmcnt(0)
	s_barrier
	s_waitcnt lgkmcnt(0)
	v_mfma_f32_16x16x32_bf16 v[60:63], v[146:149], v[178:181], v[60:63]
	v_mfma_f32_16x16x32_bf16 v[56:59], v[154:157], v[178:181], v[56:59]
	v_mfma_f32_16x16x32_bf16 v[48:51], v[146:149], v[198:201], v[48:51]
	v_mfma_f32_16x16x32_bf16 v[40:43], v[154:157], v[198:201], v[40:43]
	v_mfma_f32_16x16x32_bf16 v[32:35], v[146:149], v[206:209], v[32:35]
	v_mfma_f32_16x16x32_bf16 v[24:27], v[154:157], v[206:209], v[24:27]
	v_mfma_f32_16x16x32_bf16 v[16:19], v[146:149], v[228:231], v[16:19]
	v_mfma_f32_16x16x32_bf16 v[8:11], v[154:157], v[228:231], v[8:11]
	v_mfma_f32_16x16x32_bf16 v[60:63], v[150:153], v[194:197], v[60:63]
	v_mfma_f32_16x16x32_bf16 v[56:59], v[158:161], v[194:197], v[56:59]
	v_mfma_f32_16x16x32_bf16 v[48:51], v[150:153], v[202:205], v[48:51]
	v_mfma_f32_16x16x32_bf16 v[40:43], v[158:161], v[202:205], v[40:43]
	v_mfma_f32_16x16x32_bf16 v[32:35], v[150:153], v[224:227], v[32:35]
	v_mfma_f32_16x16x32_bf16 v[24:27], v[158:161], v[224:227], v[24:27]
	v_mfma_f32_16x16x32_bf16 v[16:19], v[150:153], v[232:235], v[16:19]
	v_mfma_f32_16x16x32_bf16 v[8:11], v[158:161], v[232:235], v[8:11]
	v_mfma_f32_16x16x32_bf16 v[52:55], v[162:165], v[178:181], v[52:55]
	v_mfma_f32_16x16x32_bf16 v[44:47], v[170:173], v[178:181], v[44:47]
	v_mfma_f32_16x16x32_bf16 v[36:39], v[162:165], v[198:201], v[36:39]
	v_mfma_f32_16x16x32_bf16 v[28:31], v[170:173], v[198:201], v[28:31]
	v_mfma_f32_16x16x32_bf16 v[20:23], v[162:165], v[206:209], v[20:23]
	v_mfma_f32_16x16x32_bf16 v[12:15], v[170:173], v[206:209], v[12:15]
	v_mfma_f32_16x16x32_bf16 v[4:7], v[162:165], v[228:231], v[4:7]
	v_mfma_f32_16x16x32_bf16 v[0:3], v[170:173], v[228:231], v[0:3]
	v_mfma_f32_16x16x32_bf16 v[52:55], v[166:169], v[194:197], v[52:55]
	v_mfma_f32_16x16x32_bf16 v[44:47], v[174:177], v[194:197], v[44:47]
	v_mfma_f32_16x16x32_bf16 v[36:39], v[166:169], v[202:205], v[36:39]
	v_mfma_f32_16x16x32_bf16 v[28:31], v[174:177], v[202:205], v[28:31]
	v_mfma_f32_16x16x32_bf16 v[20:23], v[166:169], v[224:227], v[20:23]
	v_mfma_f32_16x16x32_bf16 v[12:15], v[174:177], v[224:227], v[12:15]
	v_mfma_f32_16x16x32_bf16 v[4:7], v[166:169], v[232:235], v[4:7]
	v_mfma_f32_16x16x32_bf16 v[0:3], v[174:177], v[232:235], v[0:3]
	s_barrier
	v_add_u32_e32 v158, s48, v136
	v_add_u32_e32 v174, s28, v136
	ds_read_b128 v[146:149], v158
	ds_read_b128 v[150:153], v158 offset:1024
	ds_read_b128 v[154:157], v158 offset:2048
	ds_read_b128 v[158:161], v158 offset:3072
	ds_read_b128 v[162:165], v174
	ds_read_b128 v[166:169], v174 offset:1024
	ds_read_b128 v[170:173], v174 offset:2048
	ds_read_b128 v[174:177], v174 offset:3072
	s_mov_b32 m0, s26
	v_lshl_add_u64 v[240:241], s[38:39], 0, v[134:135]
	ds_read_b128 v[178:181], v145 offset:32768
	ds_read_b128 v[194:197], v145 offset:33792
	ds_read_b128 v[198:201], v145 offset:34816
	ds_read_b128 v[202:205], v145 offset:35840
	ds_read_b128 v[206:209], v145 offset:36864
	ds_read_b128 v[224:227], v145 offset:37888
	ds_read_b128 v[228:231], v145 offset:38912
	ds_read_b128 v[232:235], v145 offset:39936
	global_load_lds_dwordx4 v[240:241], off
	v_lshl_add_u64 v[240:241], s[38:39], 0, v[130:131]
	s_mov_b32 m0, s27
	s_nop 0
	global_load_lds_dwordx4 v[240:241], off
	s_waitcnt vmcnt(8)
	s_waitcnt lgkmcnt(0)
	s_barrier
	s_waitcnt lgkmcnt(0)
	v_mfma_f32_16x16x32_bf16 v[124:127], v[146:149], v[178:181], v[124:127]
	v_mfma_f32_16x16x32_bf16 v[120:123], v[154:157], v[178:181], v[120:123]
	v_mfma_f32_16x16x32_bf16 v[112:115], v[146:149], v[198:201], v[112:115]
	v_mfma_f32_16x16x32_bf16 v[104:107], v[154:157], v[198:201], v[104:107]
	v_mfma_f32_16x16x32_bf16 v[96:99], v[146:149], v[206:209], v[96:99]
	v_mfma_f32_16x16x32_bf16 v[88:91], v[154:157], v[206:209], v[88:91]
	v_mfma_f32_16x16x32_bf16 v[80:83], v[146:149], v[228:231], v[80:83]
	v_mfma_f32_16x16x32_bf16 v[72:75], v[154:157], v[228:231], v[72:75]
	v_mfma_f32_16x16x32_bf16 v[124:127], v[150:153], v[194:197], v[124:127]
	v_mfma_f32_16x16x32_bf16 v[120:123], v[158:161], v[194:197], v[120:123]
	v_mfma_f32_16x16x32_bf16 v[112:115], v[150:153], v[202:205], v[112:115]
	v_mfma_f32_16x16x32_bf16 v[104:107], v[158:161], v[202:205], v[104:107]
	v_mfma_f32_16x16x32_bf16 v[96:99], v[150:153], v[224:227], v[96:99]
	v_mfma_f32_16x16x32_bf16 v[88:91], v[158:161], v[224:227], v[88:91]
	v_mfma_f32_16x16x32_bf16 v[80:83], v[150:153], v[232:235], v[80:83]
	v_mfma_f32_16x16x32_bf16 v[72:75], v[158:161], v[232:235], v[72:75]
	v_mfma_f32_16x16x32_bf16 v[116:119], v[162:165], v[178:181], v[116:119]
	v_mfma_f32_16x16x32_bf16 v[108:111], v[170:173], v[178:181], v[108:111]
	v_mfma_f32_16x16x32_bf16 v[100:103], v[162:165], v[198:201], v[100:103]
	v_mfma_f32_16x16x32_bf16 v[92:95], v[170:173], v[198:201], v[92:95]
	v_mfma_f32_16x16x32_bf16 v[84:87], v[162:165], v[206:209], v[84:87]
	v_mfma_f32_16x16x32_bf16 v[76:79], v[170:173], v[206:209], v[76:79]
	v_mfma_f32_16x16x32_bf16 v[68:71], v[162:165], v[228:231], v[68:71]
	v_mfma_f32_16x16x32_bf16 v[64:67], v[170:173], v[228:231], v[64:67]
	v_mfma_f32_16x16x32_bf16 v[116:119], v[166:169], v[194:197], v[116:119]
	v_mfma_f32_16x16x32_bf16 v[108:111], v[174:177], v[194:197], v[108:111]
	v_mfma_f32_16x16x32_bf16 v[100:103], v[166:169], v[202:205], v[100:103]
	v_mfma_f32_16x16x32_bf16 v[92:95], v[174:177], v[202:205], v[92:95]
	v_mfma_f32_16x16x32_bf16 v[84:87], v[166:169], v[224:227], v[84:87]
	v_mfma_f32_16x16x32_bf16 v[76:79], v[174:177], v[224:227], v[76:79]
	v_mfma_f32_16x16x32_bf16 v[68:71], v[166:169], v[232:235], v[68:71]
	v_mfma_f32_16x16x32_bf16 v[64:67], v[174:177], v[232:235], v[64:67]
	s_barrier
	s_mov_b32 m0, s88
	v_lshl_add_u64 v[240:241], v[182:183], 0, s[68:69]
	ds_read_b128 v[178:181], v145 offset:49152
	ds_read_b128 v[194:197], v145 offset:50176
	ds_read_b128 v[198:201], v145 offset:51200
	ds_read_b128 v[202:205], v145 offset:52224
	ds_read_b128 v[206:209], v145 offset:53248
	ds_read_b128 v[224:227], v145 offset:54272
	ds_read_b128 v[228:231], v145 offset:55296
	ds_read_b128 v[232:235], v145 offset:56320
	global_load_lds_dwordx4 v[240:241], off
	v_lshl_add_u64 v[240:241], v[210:211], 0, s[68:69]
	s_mov_b32 m0, s89
	v_lshl_add_u64 v[182:183], v[182:183], 0, s[54:55]
	global_load_lds_dwordx4 v[240:241], off
	s_mov_b32 m0, s76
	s_nop 0
	global_load_lds_dwordx4 v[182:183], off
	v_lshl_add_u64 v[182:183], v[210:211], 0, s[54:55]
	s_mov_b32 m0, s85
	s_nop 0
	global_load_lds_dwordx4 v[182:183], off
	v_lshl_add_u64 v[182:183], v[236:237], 0, s[68:69]
	s_mov_b32 m0, s50
	s_nop 0
	global_load_lds_dwordx4 v[182:183], off
	v_lshl_add_u64 v[182:183], v[238:239], 0, s[68:69]
	s_mov_b32 m0, s51
	s_nop 0
	global_load_lds_dwordx4 v[182:183], off
	s_waitcnt vmcnt(8)
	s_waitcnt lgkmcnt(0)
	s_barrier
	s_waitcnt lgkmcnt(0)
	v_mfma_f32_16x16x32_bf16 v[60:63], v[146:149], v[178:181], v[60:63]
	v_mfma_f32_16x16x32_bf16 v[56:59], v[154:157], v[178:181], v[56:59]
	v_mfma_f32_16x16x32_bf16 v[48:51], v[146:149], v[198:201], v[48:51]
	v_mfma_f32_16x16x32_bf16 v[40:43], v[154:157], v[198:201], v[40:43]
	v_mfma_f32_16x16x32_bf16 v[32:35], v[146:149], v[206:209], v[32:35]
	v_mfma_f32_16x16x32_bf16 v[24:27], v[154:157], v[206:209], v[24:27]
	v_mfma_f32_16x16x32_bf16 v[16:19], v[146:149], v[228:231], v[16:19]
	v_mfma_f32_16x16x32_bf16 v[8:11], v[154:157], v[228:231], v[8:11]
	v_mfma_f32_16x16x32_bf16 v[60:63], v[150:153], v[194:197], v[60:63]
	v_mfma_f32_16x16x32_bf16 v[56:59], v[158:161], v[194:197], v[56:59]
	v_mfma_f32_16x16x32_bf16 v[48:51], v[150:153], v[202:205], v[48:51]
	v_mfma_f32_16x16x32_bf16 v[40:43], v[158:161], v[202:205], v[40:43]
	v_mfma_f32_16x16x32_bf16 v[32:35], v[150:153], v[224:227], v[32:35]
	v_mfma_f32_16x16x32_bf16 v[24:27], v[158:161], v[224:227], v[24:27]
	v_mfma_f32_16x16x32_bf16 v[16:19], v[150:153], v[232:235], v[16:19]
	v_mfma_f32_16x16x32_bf16 v[8:11], v[158:161], v[232:235], v[8:11]
	v_mfma_f32_16x16x32_bf16 v[52:55], v[162:165], v[178:181], v[52:55]
	v_mfma_f32_16x16x32_bf16 v[44:47], v[170:173], v[178:181], v[44:47]
	v_mfma_f32_16x16x32_bf16 v[36:39], v[162:165], v[198:201], v[36:39]
	v_mfma_f32_16x16x32_bf16 v[28:31], v[170:173], v[198:201], v[28:31]
	v_mfma_f32_16x16x32_bf16 v[20:23], v[162:165], v[206:209], v[20:23]
	v_mfma_f32_16x16x32_bf16 v[12:15], v[170:173], v[206:209], v[12:15]
	v_mfma_f32_16x16x32_bf16 v[4:7], v[162:165], v[228:231], v[4:7]
	v_mfma_f32_16x16x32_bf16 v[0:3], v[170:173], v[228:231], v[0:3]
	v_mfma_f32_16x16x32_bf16 v[52:55], v[166:169], v[194:197], v[52:55]
	v_mfma_f32_16x16x32_bf16 v[44:47], v[174:177], v[194:197], v[44:47]
	v_mfma_f32_16x16x32_bf16 v[36:39], v[166:169], v[202:205], v[36:39]
	v_mfma_f32_16x16x32_bf16 v[28:31], v[174:177], v[202:205], v[28:31]
	v_mfma_f32_16x16x32_bf16 v[20:23], v[166:169], v[224:227], v[20:23]
	v_mfma_f32_16x16x32_bf16 v[12:15], v[174:177], v[224:227], v[12:15]
	v_mfma_f32_16x16x32_bf16 v[4:7], v[166:169], v[232:235], v[4:7]
	v_mfma_f32_16x16x32_bf16 v[0:3], v[174:177], v[232:235], v[0:3]
	s_barrier
	s_movk_i32 s44, 0x100
	s_andn2_b64 vcc, exec, s[36:37]
	s_mov_b64 s[38:39], -1
	s_mov_b64 s[36:37], 0
	s_cbranch_vccz .LBB0_514
	s_and_b64 vcc, exec, s[6:7]
	s_cbranch_vccz .LBB0_517
	s_barrier

.LBB0_531:
	s_add_u32 s39, s18, s38
	s_addc_u32 s42, s19, 0
	s_add_u32 s40, s39, 0x100
	s_addc_u32 s41, s42, 0
	s_and_b64 s[28:29], s[36:37], exec
	s_cselect_b32 s41, s78, s41
	s_cselect_b32 s40, s79, s40
	s_add_u32 s28, s16, s38
	s_addc_u32 s29, s17, 0
	s_add_u32 s38, s28, 0x100
	s_addc_u32 s43, s29, 0
	s_add_i32 s76, 0, 0x10000
	s_and_b64 s[28:29], s[36:37], exec
	s_cselect_b32 s45, s88, s43
	s_cselect_b32 s44, s89, s38
	s_add_i32 s29, 0, 0x14000
	s_add_u32 s50, s39, 0x10080
	s_addc_u32 s51, s42, 0
	s_add_i32 s43, s76, s4
	s_add_i32 m0, s20, 0xc000
	s_add_i32 s85, s20, 0xe000
	s_add_i32 s48, s43, 0x2000
	v_add_u32_e32 v136, s76, v139
	s_add_u32 s46, s44, 0x40000
	ds_read_b128 v[142:145], v136
	ds_read_b128 v[146:149], v136 offset:1024
	ds_read_b128 v[150:153], v136 offset:2048
	ds_read_b128 v[154:157], v136 offset:3072
	v_add_u32_e32 v136, s29, v139
	s_addc_u32 s47, s45, 0
	s_add_i32 s42, s29, s4
	ds_read_b128 v[158:161], v136
	ds_read_b128 v[162:165], v136 offset:1024
	ds_read_b128 v[166:169], v136 offset:2048
	ds_read_b128 v[170:173], v136 offset:3072
	s_add_i32 s49, s42, 0x2000
	s_add_i32 s28, 0, 0x18000
	s_add_i32 s94, 0, 0x1c000
	s_add_u32 s38, s40, 0x10000
	s_addc_u32 s39, s41, 0
	s_add_i32 s93, s28, s4
	s_add_i32 s92, s93, 0x2000
	s_add_u32 s36, s44, 0x40080
	s_addc_u32 s37, s45, 0
	s_add_i32 s76, s94, s4
	s_add_i32 s29, s76, 0x2000
	v_lshl_add_u64 v[136:137], s[50:51], 0, v[134:135]
	ds_read_b128 v[174:177], v140
	ds_read_b128 v[178:181], v140 offset:1024
	ds_read_b128 v[194:197], v140 offset:2048
	ds_read_b128 v[198:201], v140 offset:3072
	ds_read_b128 v[202:205], v140 offset:4096
	ds_read_b128 v[206:209], v140 offset:5120
	ds_read_b128 v[224:227], v140 offset:6144
	ds_read_b128 v[228:231], v140 offset:7168
	global_load_lds_dwordx4 v[136:137], off
	v_lshl_add_u64 v[136:137], s[50:51], 0, v[130:131]
	s_mov_b32 m0, s85
	s_nop 0
	global_load_lds_dwordx4 v[136:137], off
	s_waitcnt vmcnt(8)
	s_waitcnt lgkmcnt(0)
	s_barrier
	s_waitcnt lgkmcnt(0)
	v_mfma_f32_16x16x32_bf16 v[124:127], v[142:145], v[174:177], v[124:127]
	v_mfma_f32_16x16x32_bf16 v[120:123], v[150:153], v[174:177], v[120:123]
	v_mfma_f32_16x16x32_bf16 v[116:119], v[142:145], v[194:197], v[116:119]
	v_mfma_f32_16x16x32_bf16 v[108:111], v[150:153], v[194:197], v[108:111]
	v_mfma_f32_16x16x32_bf16 v[100:103], v[142:145], v[202:205], v[100:103]
	v_mfma_f32_16x16x32_bf16 v[92:95], v[150:153], v[202:205], v[92:95]
	v_mfma_f32_16x16x32_bf16 v[84:87], v[142:145], v[224:227], v[84:87]
	v_mfma_f32_16x16x32_bf16 v[76:79], v[150:153], v[224:227], v[76:79]
	v_mfma_f32_16x16x32_bf16 v[124:127], v[146:149], v[178:181], v[124:127]
	v_mfma_f32_16x16x32_bf16 v[120:123], v[154:157], v[178:181], v[120:123]
	v_mfma_f32_16x16x32_bf16 v[116:119], v[146:149], v[198:201], v[116:119]
	v_mfma_f32_16x16x32_bf16 v[108:111], v[154:157], v[198:201], v[108:111]
	v_mfma_f32_16x16x32_bf16 v[100:103], v[146:149], v[206:209], v[100:103]
	v_mfma_f32_16x16x32_bf16 v[92:95], v[154:157], v[206:209], v[92:95]
	v_mfma_f32_16x16x32_bf16 v[84:87], v[146:149], v[228:231], v[84:87]
	v_mfma_f32_16x16x32_bf16 v[76:79], v[154:157], v[228:231], v[76:79]
	v_mfma_f32_16x16x32_bf16 v[112:115], v[158:161], v[174:177], v[112:115]
	v_mfma_f32_16x16x32_bf16 v[104:107], v[166:169], v[174:177], v[104:107]
	v_mfma_f32_16x16x32_bf16 v[96:99], v[158:161], v[194:197], v[96:99]
	v_mfma_f32_16x16x32_bf16 v[88:91], v[166:169], v[194:197], v[88:91]
	v_mfma_f32_16x16x32_bf16 v[80:83], v[158:161], v[202:205], v[80:83]
	v_mfma_f32_16x16x32_bf16 v[72:75], v[166:169], v[202:205], v[72:75]
	v_mfma_f32_16x16x32_bf16 v[68:71], v[158:161], v[224:227], v[68:71]
	v_mfma_f32_16x16x32_bf16 v[64:67], v[166:169], v[224:227], v[64:67]
	v_mfma_f32_16x16x32_bf16 v[112:115], v[162:165], v[178:181], v[112:115]
	v_mfma_f32_16x16x32_bf16 v[104:107], v[170:173], v[178:181], v[104:107]
	v_mfma_f32_16x16x32_bf16 v[96:99], v[162:165], v[198:201], v[96:99]
	v_mfma_f32_16x16x32_bf16 v[88:91], v[170:173], v[198:201], v[88:91]
	v_mfma_f32_16x16x32_bf16 v[80:83], v[162:165], v[206:209], v[80:83]
	v_mfma_f32_16x16x32_bf16 v[72:75], v[170:173], v[206:209], v[72:75]
	v_mfma_f32_16x16x32_bf16 v[68:71], v[162:165], v[228:231], v[68:71]
	v_mfma_f32_16x16x32_bf16 v[64:67], v[170:173], v[228:231], v[64:67]
	s_barrier
	s_mov_b32 m0, s43
	v_lshl_add_u64 v[136:137], s[44:45], 0, v[132:133]
	ds_read_b128 v[174:177], v140 offset:16384
	ds_read_b128 v[178:181], v140 offset:17408
	ds_read_b128 v[194:197], v140 offset:18432
	ds_read_b128 v[198:201], v140 offset:19456
	ds_read_b128 v[202:205], v140 offset:20480
	ds_read_b128 v[206:209], v140 offset:21504
	ds_read_b128 v[224:227], v140 offset:22528
	ds_read_b128 v[228:231], v140 offset:23552
	global_load_lds_dwordx4 v[136:137], off
	v_lshl_add_u64 v[182:183], s[44:45], 0, v[128:129]
	s_mov_b32 m0, s48
	v_lshl_add_u64 v[210:211], s[46:47], 0, v[132:133]
	global_load_lds_dwordx4 v[182:183], off
	s_mov_b32 m0, s42
	v_lshl_add_u64 v[232:233], s[40:41], 0, v[130:131]
	global_load_lds_dwordx4 v[210:211], off
	v_lshl_add_u64 v[210:211], s[46:47], 0, v[128:129]
	s_mov_b32 m0, s49
	s_nop 0
	global_load_lds_dwordx4 v[210:211], off
	v_lshl_add_u64 v[210:211], s[40:41], 0, v[134:135]
	s_mov_b32 m0, s20
	s_nop 0
	global_load_lds_dwordx4 v[210:211], off
	s_mov_b32 m0, s21
	s_nop 0
	global_load_lds_dwordx4 v[232:233], off
	s_waitcnt vmcnt(8)
	s_waitcnt lgkmcnt(0)
	s_barrier
	s_waitcnt lgkmcnt(0)
	v_mfma_f32_16x16x32_bf16 v[60:63], v[142:145], v[174:177], v[60:63]
	v_mfma_f32_16x16x32_bf16 v[56:59], v[150:153], v[174:177], v[56:59]
	v_mfma_f32_16x16x32_bf16 v[52:55], v[142:145], v[194:197], v[52:55]
	v_mfma_f32_16x16x32_bf16 v[44:47], v[150:153], v[194:197], v[44:47]
	v_mfma_f32_16x16x32_bf16 v[36:39], v[142:145], v[202:205], v[36:39]
	v_mfma_f32_16x16x32_bf16 v[28:31], v[150:153], v[202:205], v[28:31]
	v_mfma_f32_16x16x32_bf16 v[20:23], v[142:145], v[224:227], v[20:23]
	v_mfma_f32_16x16x32_bf16 v[12:15], v[150:153], v[224:227], v[12:15]
	v_mfma_f32_16x16x32_bf16 v[60:63], v[146:149], v[178:181], v[60:63]
	v_mfma_f32_16x16x32_bf16 v[56:59], v[154:157], v[178:181], v[56:59]
	v_mfma_f32_16x16x32_bf16 v[52:55], v[146:149], v[198:201], v[52:55]
	v_mfma_f32_16x16x32_bf16 v[44:47], v[154:157], v[198:201], v[44:47]
	v_mfma_f32_16x16x32_bf16 v[36:39], v[146:149], v[206:209], v[36:39]
	v_mfma_f32_16x16x32_bf16 v[28:31], v[154:157], v[206:209], v[28:31]
	v_mfma_f32_16x16x32_bf16 v[20:23], v[146:149], v[228:231], v[20:23]
	v_mfma_f32_16x16x32_bf16 v[12:15], v[154:157], v[228:231], v[12:15]
	v_mfma_f32_16x16x32_bf16 v[48:51], v[158:161], v[174:177], v[48:51]
	v_mfma_f32_16x16x32_bf16 v[40:43], v[166:169], v[174:177], v[40:43]
	v_mfma_f32_16x16x32_bf16 v[32:35], v[158:161], v[194:197], v[32:35]
	v_mfma_f32_16x16x32_bf16 v[24:27], v[166:169], v[194:197], v[24:27]
	v_mfma_f32_16x16x32_bf16 v[16:19], v[158:161], v[202:205], v[16:19]
	v_mfma_f32_16x16x32_bf16 v[8:11], v[166:169], v[202:205], v[8:11]
	v_mfma_f32_16x16x32_bf16 v[4:7], v[158:161], v[224:227], v[4:7]
	v_mfma_f32_16x16x32_bf16 v[0:3], v[166:169], v[224:227], v[0:3]
	v_mfma_f32_16x16x32_bf16 v[48:51], v[162:165], v[178:181], v[48:51]
	v_mfma_f32_16x16x32_bf16 v[40:43], v[170:173], v[178:181], v[40:43]
	v_mfma_f32_16x16x32_bf16 v[32:35], v[162:165], v[198:201], v[32:35]
	v_mfma_f32_16x16x32_bf16 v[24:27], v[170:173], v[198:201], v[24:27]
	v_mfma_f32_16x16x32_bf16 v[16:19], v[162:165], v[206:209], v[16:19]
	v_mfma_f32_16x16x32_bf16 v[8:11], v[170:173], v[206:209], v[8:11]
	v_mfma_f32_16x16x32_bf16 v[4:7], v[162:165], v[228:231], v[4:7]
	v_mfma_f32_16x16x32_bf16 v[0:3], v[170:173], v[228:231], v[0:3]
	s_barrier
	v_add_u32_e32 v141, s28, v139
	ds_read_b128 v[142:145], v141
	ds_read_b128 v[146:149], v141 offset:1024
	ds_read_b128 v[150:153], v141 offset:2048
	ds_read_b128 v[154:157], v141 offset:3072
	v_add_u32_e32 v141, s94, v139
	ds_read_b128 v[158:161], v141
	ds_read_b128 v[162:165], v141 offset:1024
	ds_read_b128 v[166:169], v141 offset:2048
	ds_read_b128 v[170:173], v141 offset:3072
	s_mov_b32 m0, s26
	v_lshl_add_u64 v[234:235], s[38:39], 0, v[134:135]
	ds_read_b128 v[174:177], v140 offset:32768
	ds_read_b128 v[178:181], v140 offset:33792
	ds_read_b128 v[194:197], v140 offset:34816
	ds_read_b128 v[198:201], v140 offset:35840
	ds_read_b128 v[202:205], v140 offset:36864
	ds_read_b128 v[206:209], v140 offset:37888
	ds_read_b128 v[224:227], v140 offset:38912
	ds_read_b128 v[228:231], v140 offset:39936
	global_load_lds_dwordx4 v[234:235], off
	v_lshl_add_u64 v[234:235], s[38:39], 0, v[130:131]
	s_mov_b32 m0, s27
	s_nop 0
	global_load_lds_dwordx4 v[234:235], off
	s_waitcnt vmcnt(8)
	s_waitcnt lgkmcnt(0)
	s_barrier
	s_waitcnt lgkmcnt(0)
	v_mfma_f32_16x16x32_bf16 v[124:127], v[142:145], v[174:177], v[124:127]
	v_mfma_f32_16x16x32_bf16 v[120:123], v[150:153], v[174:177], v[120:123]
	v_mfma_f32_16x16x32_bf16 v[116:119], v[142:145], v[194:197], v[116:119]
	v_mfma_f32_16x16x32_bf16 v[108:111], v[150:153], v[194:197], v[108:111]
	v_mfma_f32_16x16x32_bf16 v[100:103], v[142:145], v[202:205], v[100:103]
	v_mfma_f32_16x16x32_bf16 v[92:95], v[150:153], v[202:205], v[92:95]
	v_mfma_f32_16x16x32_bf16 v[84:87], v[142:145], v[224:227], v[84:87]
	v_mfma_f32_16x16x32_bf16 v[76:79], v[150:153], v[224:227], v[76:79]
	v_mfma_f32_16x16x32_bf16 v[124:127], v[146:149], v[178:181], v[124:127]
	v_mfma_f32_16x16x32_bf16 v[120:123], v[154:157], v[178:181], v[120:123]
	v_mfma_f32_16x16x32_bf16 v[116:119], v[146:149], v[198:201], v[116:119]
	v_mfma_f32_16x16x32_bf16 v[108:111], v[154:157], v[198:201], v[108:111]
	v_mfma_f32_16x16x32_bf16 v[100:103], v[146:149], v[206:209], v[100:103]
	v_mfma_f32_16x16x32_bf16 v[92:95], v[154:157], v[206:209], v[92:95]
	v_mfma_f32_16x16x32_bf16 v[84:87], v[146:149], v[228:231], v[84:87]
	v_mfma_f32_16x16x32_bf16 v[76:79], v[154:157], v[228:231], v[76:79]
	v_mfma_f32_16x16x32_bf16 v[112:115], v[158:161], v[174:177], v[112:115]
	v_mfma_f32_16x16x32_bf16 v[104:107], v[166:169], v[174:177], v[104:107]
	v_mfma_f32_16x16x32_bf16 v[96:99], v[158:161], v[194:197], v[96:99]
	v_mfma_f32_16x16x32_bf16 v[88:91], v[166:169], v[194:197], v[88:91]
	v_mfma_f32_16x16x32_bf16 v[80:83], v[158:161], v[202:205], v[80:83]
	v_mfma_f32_16x16x32_bf16 v[72:75], v[166:169], v[202:205], v[72:75]
	v_mfma_f32_16x16x32_bf16 v[68:71], v[158:161], v[224:227], v[68:71]
	v_mfma_f32_16x16x32_bf16 v[64:67], v[166:169], v[224:227], v[64:67]
	v_mfma_f32_16x16x32_bf16 v[112:115], v[162:165], v[178:181], v[112:115]
	v_mfma_f32_16x16x32_bf16 v[104:107], v[170:173], v[178:181], v[104:107]
	v_mfma_f32_16x16x32_bf16 v[96:99], v[162:165], v[198:201], v[96:99]
	v_mfma_f32_16x16x32_bf16 v[88:91], v[170:173], v[198:201], v[88:91]
	v_mfma_f32_16x16x32_bf16 v[80:83], v[162:165], v[206:209], v[80:83]
	v_mfma_f32_16x16x32_bf16 v[72:75], v[170:173], v[206:209], v[72:75]
	v_mfma_f32_16x16x32_bf16 v[68:71], v[162:165], v[228:231], v[68:71]
	v_mfma_f32_16x16x32_bf16 v[64:67], v[170:173], v[228:231], v[64:67]
	s_barrier
	s_mov_b32 m0, s93
	v_lshl_add_u64 v[136:137], v[136:137], 0, s[68:69]
	ds_read_b128 v[174:177], v140 offset:49152
	ds_read_b128 v[178:181], v140 offset:50176
	ds_read_b128 v[194:197], v140 offset:51200
	ds_read_b128 v[198:201], v140 offset:52224
	ds_read_b128 v[202:205], v140 offset:53248
	ds_read_b128 v[206:209], v140 offset:54272
	ds_read_b128 v[224:227], v140 offset:55296
	ds_read_b128 v[228:231], v140 offset:56320
	global_load_lds_dwordx4 v[136:137], off
	v_lshl_add_u64 v[136:137], v[182:183], 0, s[68:69]
	s_mov_b32 m0, s92
	s_nop 0
	global_load_lds_dwordx4 v[136:137], off
	v_lshl_add_u64 v[136:137], s[36:37], 0, v[132:133]
	s_mov_b32 m0, s76
	s_nop 0
	global_load_lds_dwordx4 v[136:137], off
	v_lshl_add_u64 v[136:137], s[36:37], 0, v[128:129]
	s_mov_b32 m0, s29
	s_nop 0
	global_load_lds_dwordx4 v[136:137], off
	v_lshl_add_u64 v[136:137], v[210:211], 0, s[68:69]
	s_mov_b32 m0, s52
	s_nop 0
	global_load_lds_dwordx4 v[136:137], off
	v_lshl_add_u64 v[136:137], v[232:233], 0, s[68:69]
	s_mov_b32 m0, s53
	s_nop 0
	global_load_lds_dwordx4 v[136:137], off
	s_waitcnt vmcnt(8)
	s_waitcnt lgkmcnt(0)
	s_barrier
	s_waitcnt lgkmcnt(0)
	v_mfma_f32_16x16x32_bf16 v[60:63], v[142:145], v[174:177], v[60:63]
	v_mfma_f32_16x16x32_bf16 v[56:59], v[150:153], v[174:177], v[56:59]
	v_mfma_f32_16x16x32_bf16 v[52:55], v[142:145], v[194:197], v[52:55]
	v_mfma_f32_16x16x32_bf16 v[44:47], v[150:153], v[194:197], v[44:47]
	v_mfma_f32_16x16x32_bf16 v[36:39], v[142:145], v[202:205], v[36:39]
	v_mfma_f32_16x16x32_bf16 v[28:31], v[150:153], v[202:205], v[28:31]
	v_mfma_f32_16x16x32_bf16 v[20:23], v[142:145], v[224:227], v[20:23]
	v_mfma_f32_16x16x32_bf16 v[12:15], v[150:153], v[224:227], v[12:15]
	v_mfma_f32_16x16x32_bf16 v[60:63], v[146:149], v[178:181], v[60:63]
	v_mfma_f32_16x16x32_bf16 v[56:59], v[154:157], v[178:181], v[56:59]
	v_mfma_f32_16x16x32_bf16 v[52:55], v[146:149], v[198:201], v[52:55]
	v_mfma_f32_16x16x32_bf16 v[44:47], v[154:157], v[198:201], v[44:47]
	v_mfma_f32_16x16x32_bf16 v[36:39], v[146:149], v[206:209], v[36:39]
	v_mfma_f32_16x16x32_bf16 v[28:31], v[154:157], v[206:209], v[28:31]
	v_mfma_f32_16x16x32_bf16 v[20:23], v[146:149], v[228:231], v[20:23]
	v_mfma_f32_16x16x32_bf16 v[12:15], v[154:157], v[228:231], v[12:15]
	v_mfma_f32_16x16x32_bf16 v[48:51], v[158:161], v[174:177], v[48:51]
	v_mfma_f32_16x16x32_bf16 v[40:43], v[166:169], v[174:177], v[40:43]
	v_mfma_f32_16x16x32_bf16 v[32:35], v[158:161], v[194:197], v[32:35]
	v_mfma_f32_16x16x32_bf16 v[24:27], v[166:169], v[194:197], v[24:27]
	v_mfma_f32_16x16x32_bf16 v[16:19], v[158:161], v[202:205], v[16:19]
	v_mfma_f32_16x16x32_bf16 v[8:11], v[166:169], v[202:205], v[8:11]
	v_mfma_f32_16x16x32_bf16 v[4:7], v[158:161], v[224:227], v[4:7]
	v_mfma_f32_16x16x32_bf16 v[0:3], v[166:169], v[224:227], v[0:3]
	v_mfma_f32_16x16x32_bf16 v[48:51], v[162:165], v[178:181], v[48:51]
	v_mfma_f32_16x16x32_bf16 v[40:43], v[170:173], v[178:181], v[40:43]
	v_mfma_f32_16x16x32_bf16 v[32:35], v[162:165], v[198:201], v[32:35]
	v_mfma_f32_16x16x32_bf16 v[24:27], v[170:173], v[198:201], v[24:27]
	v_mfma_f32_16x16x32_bf16 v[16:19], v[162:165], v[206:209], v[16:19]
	v_mfma_f32_16x16x32_bf16 v[8:11], v[170:173], v[206:209], v[8:11]
	v_mfma_f32_16x16x32_bf16 v[4:7], v[162:165], v[228:231], v[4:7]
	v_mfma_f32_16x16x32_bf16 v[0:3], v[170:173], v[228:231], v[0:3]
	s_barrier
	s_movk_i32 s38, 0x100
	s_andn2_b64 vcc, exec, s[30:31]
	s_mov_b64 s[36:37], -1
	s_mov_b64 s[30:31], 0
	s_cbranch_vccz .LBB0_531
	s_and_b64 vcc, exec, s[6:7]
	s_cbranch_vccz .LBB0_534
	s_barrier

.LBB0_599:
	s_add_i32 s37, s36, 0x100
	s_and_b64 s[28:29], s[30:31], exec
	s_cselect_b32 s29, 0, s37
	s_cselect_b32 s28, 0, 0
	s_add_u32 s38, s34, s29
	s_addc_u32 s39, s35, s28
	s_add_u32 s28, s16, s36
	s_addc_u32 s29, s17, 0
	s_add_u32 s37, s28, 0x100
	s_addc_u32 s40, s29, 0
	s_add_i32 s43, 0, 0x10000
	s_and_b64 s[28:29], s[30:31], exec
	s_cselect_b32 s41, s9, s40
	s_cselect_b32 s40, s58, s37
	s_add_i32 s29, 0, 0x14000
	s_add_u32 s46, s56, s36
	s_addc_u32 s47, s57, 0
	s_add_i32 s42, s43, s4
	s_add_i32 m0, s20, 0xc000
	s_add_i32 s63, s20, 0xe000
	s_add_i32 s48, s42, 0x2000
	s_add_u32 s44, s40, 0x10000
	v_add_u32_e32 v156, s43, v145
	v_add_u32_e32 v172, s29, v145
	s_addc_u32 s45, s41, 0
	s_add_i32 s62, s29, s4
	ds_read_b128 v[136:139], v156
	ds_read_b128 v[140:143], v156 offset:1024
	ds_read_b128 v[152:155], v156 offset:2048
	ds_read_b128 v[156:159], v156 offset:3072
	ds_read_b128 v[160:163], v172
	ds_read_b128 v[164:167], v172 offset:1024
	ds_read_b128 v[168:171], v172 offset:2048
	ds_read_b128 v[172:175], v172 offset:3072
	s_add_i32 s49, s62, 0x2000
	s_add_i32 s28, 0, 0x18000
	s_add_i32 s61, 0, 0x1c000
	s_add_u32 s36, s38, 0x10000
	s_addc_u32 s37, s39, 0
	s_add_i32 s60, s28, s4
	s_add_i32 s59, s60, 0x2000
	s_add_u32 s30, s40, 0x10080
	s_addc_u32 s31, s41, 0
	s_add_i32 s43, s61, s4
	s_add_i32 s29, s43, 0x2000
	v_lshl_add_u64 v[210:211], s[46:47], 0, v[132:133]
	v_lshl_add_u64 v[210:211], v[210:211], 0, s[68:69]
	ds_read_b128 v[176:179], v151
	ds_read_b128 v[180:183], v151 offset:1024
	ds_read_b128 v[194:197], v151 offset:2048
	ds_read_b128 v[198:201], v151 offset:3072
	ds_read_b128 v[202:205], v151 offset:4096
	ds_read_b128 v[206:209], v151 offset:5120
	ds_read_b128 v[224:227], v151 offset:6144
	ds_read_b128 v[228:231], v151 offset:7168
	global_load_lds_dwordx4 v[210:211], off
	v_lshl_add_u64 v[210:211], s[46:47], 0, v[130:131]
	v_lshl_add_u64 v[210:211], v[210:211], 0, s[68:69]
	s_mov_b32 m0, s63
	s_nop 0
	global_load_lds_dwordx4 v[210:211], off
	s_waitcnt vmcnt(8)
	s_waitcnt lgkmcnt(0)
	s_barrier
	s_waitcnt lgkmcnt(0)
	v_mfma_f32_16x16x32_bf16 v[124:127], v[136:139], v[176:179], v[124:127]
	v_mfma_f32_16x16x32_bf16 v[116:119], v[152:155], v[176:179], v[116:119]
	v_mfma_f32_16x16x32_bf16 v[92:95], v[136:139], v[194:197], v[92:95]
	v_mfma_f32_16x16x32_bf16 v[84:87], v[152:155], v[194:197], v[84:87]
	v_mfma_f32_16x16x32_bf16 v[60:63], v[136:139], v[202:205], v[60:63]
	v_mfma_f32_16x16x32_bf16 v[52:55], v[152:155], v[202:205], v[52:55]
	v_mfma_f32_16x16x32_bf16 v[28:31], v[136:139], v[224:227], v[28:31]
	v_mfma_f32_16x16x32_bf16 v[20:23], v[152:155], v[224:227], v[20:23]
	v_mfma_f32_16x16x32_bf16 v[124:127], v[140:143], v[180:183], v[124:127]
	v_mfma_f32_16x16x32_bf16 v[116:119], v[156:159], v[180:183], v[116:119]
	v_mfma_f32_16x16x32_bf16 v[92:95], v[140:143], v[198:201], v[92:95]
	v_mfma_f32_16x16x32_bf16 v[84:87], v[156:159], v[198:201], v[84:87]
	v_mfma_f32_16x16x32_bf16 v[60:63], v[140:143], v[206:209], v[60:63]
	v_mfma_f32_16x16x32_bf16 v[52:55], v[156:159], v[206:209], v[52:55]
	v_mfma_f32_16x16x32_bf16 v[28:31], v[140:143], v[228:231], v[28:31]
	v_mfma_f32_16x16x32_bf16 v[20:23], v[156:159], v[228:231], v[20:23]
	v_mfma_f32_16x16x32_bf16 v[108:111], v[160:163], v[176:179], v[108:111]
	v_mfma_f32_16x16x32_bf16 v[104:107], v[168:171], v[176:179], v[104:107]
	v_mfma_f32_16x16x32_bf16 v[76:79], v[160:163], v[194:197], v[76:79]
	v_mfma_f32_16x16x32_bf16 v[72:75], v[168:171], v[194:197], v[72:75]
	v_mfma_f32_16x16x32_bf16 v[44:47], v[160:163], v[202:205], v[44:47]
	v_mfma_f32_16x16x32_bf16 v[40:43], v[168:171], v[202:205], v[40:43]
	v_mfma_f32_16x16x32_bf16 v[12:15], v[160:163], v[224:227], v[12:15]
	v_mfma_f32_16x16x32_bf16 v[8:11], v[168:171], v[224:227], v[8:11]
	v_mfma_f32_16x16x32_bf16 v[108:111], v[164:167], v[180:183], v[108:111]
	v_mfma_f32_16x16x32_bf16 v[104:107], v[172:175], v[180:183], v[104:107]
	v_mfma_f32_16x16x32_bf16 v[76:79], v[164:167], v[198:201], v[76:79]
	v_mfma_f32_16x16x32_bf16 v[72:75], v[172:175], v[198:201], v[72:75]
	v_mfma_f32_16x16x32_bf16 v[44:47], v[164:167], v[206:209], v[44:47]
	v_mfma_f32_16x16x32_bf16 v[40:43], v[172:175], v[206:209], v[40:43]
	v_mfma_f32_16x16x32_bf16 v[12:15], v[164:167], v[228:231], v[12:15]
	v_mfma_f32_16x16x32_bf16 v[8:11], v[172:175], v[228:231], v[8:11]
	s_barrier
	s_mov_b32 m0, s42
	v_lshl_add_u64 v[210:211], s[40:41], 0, v[184:185]
	ds_read_b128 v[176:179], v151 offset:16384
	ds_read_b128 v[180:183], v151 offset:17408
	ds_read_b128 v[194:197], v151 offset:18432
	ds_read_b128 v[198:201], v151 offset:19456
	ds_read_b128 v[202:205], v151 offset:20480
	ds_read_b128 v[206:209], v151 offset:21504
	ds_read_b128 v[224:227], v151 offset:22528
	ds_read_b128 v[228:231], v151 offset:23552
	global_load_lds_dwordx4 v[210:211], off
	v_lshl_add_u64 v[232:233], s[40:41], 0, v[128:129]
	s_mov_b32 m0, s48
	v_lshl_add_u64 v[234:235], s[44:45], 0, v[184:185]
	global_load_lds_dwordx4 v[232:233], off
	s_mov_b32 m0, s62
	v_lshl_add_u64 v[236:237], s[38:39], 0, v[130:131]
	global_load_lds_dwordx4 v[234:235], off
	v_lshl_add_u64 v[234:235], s[44:45], 0, v[128:129]
	s_mov_b32 m0, s49
	s_nop 0
	global_load_lds_dwordx4 v[234:235], off
	v_lshl_add_u64 v[234:235], s[38:39], 0, v[132:133]
	s_mov_b32 m0, s20
	s_nop 0
	global_load_lds_dwordx4 v[234:235], off
	s_mov_b32 m0, s21
	s_nop 0
	global_load_lds_dwordx4 v[236:237], off
	s_waitcnt vmcnt(8)
	s_waitcnt lgkmcnt(0)
	s_barrier
	s_waitcnt lgkmcnt(0)
	v_mfma_f32_16x16x32_bf16 v[120:123], v[136:139], v[176:179], v[120:123]
	v_mfma_f32_16x16x32_bf16 v[112:115], v[152:155], v[176:179], v[112:115]
	v_mfma_f32_16x16x32_bf16 v[88:91], v[136:139], v[194:197], v[88:91]
	v_mfma_f32_16x16x32_bf16 v[80:83], v[152:155], v[194:197], v[80:83]
	v_mfma_f32_16x16x32_bf16 v[56:59], v[136:139], v[202:205], v[56:59]
	v_mfma_f32_16x16x32_bf16 v[48:51], v[152:155], v[202:205], v[48:51]
	v_mfma_f32_16x16x32_bf16 v[24:27], v[136:139], v[224:227], v[24:27]
	v_mfma_f32_16x16x32_bf16 v[16:19], v[152:155], v[224:227], v[16:19]
	v_mfma_f32_16x16x32_bf16 v[120:123], v[140:143], v[180:183], v[120:123]
	v_mfma_f32_16x16x32_bf16 v[112:115], v[156:159], v[180:183], v[112:115]
	v_mfma_f32_16x16x32_bf16 v[88:91], v[140:143], v[198:201], v[88:91]
	v_mfma_f32_16x16x32_bf16 v[80:83], v[156:159], v[198:201], v[80:83]
	v_mfma_f32_16x16x32_bf16 v[56:59], v[140:143], v[206:209], v[56:59]
	v_mfma_f32_16x16x32_bf16 v[48:51], v[156:159], v[206:209], v[48:51]
	v_mfma_f32_16x16x32_bf16 v[24:27], v[140:143], v[228:231], v[24:27]
	v_mfma_f32_16x16x32_bf16 v[16:19], v[156:159], v[228:231], v[16:19]
	v_mfma_f32_16x16x32_bf16 v[100:103], v[160:163], v[176:179], v[100:103]
	v_mfma_f32_16x16x32_bf16 v[96:99], v[168:171], v[176:179], v[96:99]
	v_mfma_f32_16x16x32_bf16 v[68:71], v[160:163], v[194:197], v[68:71]
	v_mfma_f32_16x16x32_bf16 v[64:67], v[168:171], v[194:197], v[64:67]
	v_mfma_f32_16x16x32_bf16 v[36:39], v[160:163], v[202:205], v[36:39]
	v_mfma_f32_16x16x32_bf16 v[32:35], v[168:171], v[202:205], v[32:35]
	v_mfma_f32_16x16x32_bf16 v[4:7], v[160:163], v[224:227], v[4:7]
	v_mfma_f32_16x16x32_bf16 v[0:3], v[168:171], v[224:227], v[0:3]
	v_mfma_f32_16x16x32_bf16 v[100:103], v[164:167], v[180:183], v[100:103]
	v_mfma_f32_16x16x32_bf16 v[96:99], v[172:175], v[180:183], v[96:99]
	v_mfma_f32_16x16x32_bf16 v[68:71], v[164:167], v[198:201], v[68:71]
	v_mfma_f32_16x16x32_bf16 v[64:67], v[172:175], v[198:201], v[64:67]
	v_mfma_f32_16x16x32_bf16 v[36:39], v[164:167], v[206:209], v[36:39]
	v_mfma_f32_16x16x32_bf16 v[32:35], v[172:175], v[206:209], v[32:35]
	v_mfma_f32_16x16x32_bf16 v[4:7], v[164:167], v[228:231], v[4:7]
	v_mfma_f32_16x16x32_bf16 v[0:3], v[172:175], v[228:231], v[0:3]
	s_barrier
	v_add_u32_e32 v156, s28, v145
	v_add_u32_e32 v172, s61, v145
	ds_read_b128 v[136:139], v156
	ds_read_b128 v[140:143], v156 offset:1024
	ds_read_b128 v[152:155], v156 offset:2048
	ds_read_b128 v[156:159], v156 offset:3072
	ds_read_b128 v[160:163], v172
	ds_read_b128 v[164:167], v172 offset:1024
	ds_read_b128 v[168:171], v172 offset:2048
	ds_read_b128 v[172:175], v172 offset:3072
	s_mov_b32 m0, s26
	v_lshl_add_u64 v[238:239], s[36:37], 0, v[132:133]
	ds_read_b128 v[176:179], v151 offset:32768
	ds_read_b128 v[180:183], v151 offset:33792
	ds_read_b128 v[194:197], v151 offset:34816
	ds_read_b128 v[198:201], v151 offset:35840
	ds_read_b128 v[202:205], v151 offset:36864
	ds_read_b128 v[206:209], v151 offset:37888
	ds_read_b128 v[224:227], v151 offset:38912
	ds_read_b128 v[228:231], v151 offset:39936
	global_load_lds_dwordx4 v[238:239], off
	v_lshl_add_u64 v[238:239], s[36:37], 0, v[130:131]
	s_mov_b32 m0, s27
	s_nop 0
	global_load_lds_dwordx4 v[238:239], off
	s_waitcnt vmcnt(8)
	s_waitcnt lgkmcnt(0)
	s_barrier
	s_waitcnt lgkmcnt(0)
	v_mfma_f32_16x16x32_bf16 v[124:127], v[136:139], v[176:179], v[124:127]
	v_mfma_f32_16x16x32_bf16 v[116:119], v[152:155], v[176:179], v[116:119]
	v_mfma_f32_16x16x32_bf16 v[92:95], v[136:139], v[194:197], v[92:95]
	v_mfma_f32_16x16x32_bf16 v[84:87], v[152:155], v[194:197], v[84:87]
	v_mfma_f32_16x16x32_bf16 v[60:63], v[136:139], v[202:205], v[60:63]
	v_mfma_f32_16x16x32_bf16 v[52:55], v[152:155], v[202:205], v[52:55]
	v_mfma_f32_16x16x32_bf16 v[28:31], v[136:139], v[224:227], v[28:31]
	v_mfma_f32_16x16x32_bf16 v[20:23], v[152:155], v[224:227], v[20:23]
	v_mfma_f32_16x16x32_bf16 v[124:127], v[140:143], v[180:183], v[124:127]
	v_mfma_f32_16x16x32_bf16 v[116:119], v[156:159], v[180:183], v[116:119]
	v_mfma_f32_16x16x32_bf16 v[92:95], v[140:143], v[198:201], v[92:95]
	v_mfma_f32_16x16x32_bf16 v[84:87], v[156:159], v[198:201], v[84:87]
	v_mfma_f32_16x16x32_bf16 v[60:63], v[140:143], v[206:209], v[60:63]
	v_mfma_f32_16x16x32_bf16 v[52:55], v[156:159], v[206:209], v[52:55]
	v_mfma_f32_16x16x32_bf16 v[28:31], v[140:143], v[228:231], v[28:31]
	v_mfma_f32_16x16x32_bf16 v[20:23], v[156:159], v[228:231], v[20:23]
	v_mfma_f32_16x16x32_bf16 v[108:111], v[160:163], v[176:179], v[108:111]
	v_mfma_f32_16x16x32_bf16 v[104:107], v[168:171], v[176:179], v[104:107]
	v_mfma_f32_16x16x32_bf16 v[76:79], v[160:163], v[194:197], v[76:79]
	v_mfma_f32_16x16x32_bf16 v[72:75], v[168:171], v[194:197], v[72:75]
	v_mfma_f32_16x16x32_bf16 v[44:47], v[160:163], v[202:205], v[44:47]
	v_mfma_f32_16x16x32_bf16 v[40:43], v[168:171], v[202:205], v[40:43]
	v_mfma_f32_16x16x32_bf16 v[12:15], v[160:163], v[224:227], v[12:15]
	v_mfma_f32_16x16x32_bf16 v[8:11], v[168:171], v[224:227], v[8:11]
	v_mfma_f32_16x16x32_bf16 v[108:111], v[164:167], v[180:183], v[108:111]
	v_mfma_f32_16x16x32_bf16 v[104:107], v[172:175], v[180:183], v[104:107]
	v_mfma_f32_16x16x32_bf16 v[76:79], v[164:167], v[198:201], v[76:79]
	v_mfma_f32_16x16x32_bf16 v[72:75], v[172:175], v[198:201], v[72:75]
	v_mfma_f32_16x16x32_bf16 v[44:47], v[164:167], v[206:209], v[44:47]
	v_mfma_f32_16x16x32_bf16 v[40:43], v[172:175], v[206:209], v[40:43]
	v_mfma_f32_16x16x32_bf16 v[12:15], v[164:167], v[228:231], v[12:15]
	v_mfma_f32_16x16x32_bf16 v[8:11], v[172:175], v[228:231], v[8:11]
	s_barrier
	s_mov_b32 m0, s60
	v_lshl_add_u64 v[210:211], v[210:211], 0, s[68:69]
	ds_read_b128 v[176:179], v151 offset:49152
	ds_read_b128 v[180:183], v151 offset:50176
	ds_read_b128 v[194:197], v151 offset:51200
	ds_read_b128 v[198:201], v151 offset:52224
	ds_read_b128 v[202:205], v151 offset:53248
	ds_read_b128 v[206:209], v151 offset:54272
	ds_read_b128 v[224:227], v151 offset:55296
	ds_read_b128 v[228:231], v151 offset:56320
	global_load_lds_dwordx4 v[210:211], off
	v_lshl_add_u64 v[210:211], v[232:233], 0, s[68:69]
	s_mov_b32 m0, s59
	s_nop 0
	global_load_lds_dwordx4 v[210:211], off
	v_lshl_add_u64 v[210:211], s[30:31], 0, v[184:185]
	s_mov_b32 m0, s43
	s_nop 0
	global_load_lds_dwordx4 v[210:211], off
	v_lshl_add_u64 v[210:211], s[30:31], 0, v[128:129]
	s_mov_b32 m0, s29
	s_nop 0
	global_load_lds_dwordx4 v[210:211], off
	v_lshl_add_u64 v[210:211], v[234:235], 0, s[68:69]
	s_mov_b32 m0, s50
	s_nop 0
	global_load_lds_dwordx4 v[210:211], off
	v_lshl_add_u64 v[210:211], v[236:237], 0, s[68:69]
	s_mov_b32 m0, s51
	s_nop 0
	global_load_lds_dwordx4 v[210:211], off
	s_waitcnt vmcnt(8)
	s_waitcnt lgkmcnt(0)
	s_barrier
	s_waitcnt lgkmcnt(0)
	v_mfma_f32_16x16x32_bf16 v[120:123], v[136:139], v[176:179], v[120:123]
	v_mfma_f32_16x16x32_bf16 v[112:115], v[152:155], v[176:179], v[112:115]
	v_mfma_f32_16x16x32_bf16 v[88:91], v[136:139], v[194:197], v[88:91]
	v_mfma_f32_16x16x32_bf16 v[80:83], v[152:155], v[194:197], v[80:83]
	v_mfma_f32_16x16x32_bf16 v[56:59], v[136:139], v[202:205], v[56:59]
	v_mfma_f32_16x16x32_bf16 v[48:51], v[152:155], v[202:205], v[48:51]
	v_mfma_f32_16x16x32_bf16 v[24:27], v[136:139], v[224:227], v[24:27]
	v_mfma_f32_16x16x32_bf16 v[16:19], v[152:155], v[224:227], v[16:19]
	v_mfma_f32_16x16x32_bf16 v[120:123], v[140:143], v[180:183], v[120:123]
	v_mfma_f32_16x16x32_bf16 v[112:115], v[156:159], v[180:183], v[112:115]
	v_mfma_f32_16x16x32_bf16 v[88:91], v[140:143], v[198:201], v[88:91]
	v_mfma_f32_16x16x32_bf16 v[80:83], v[156:159], v[198:201], v[80:83]
	v_mfma_f32_16x16x32_bf16 v[56:59], v[140:143], v[206:209], v[56:59]
	v_mfma_f32_16x16x32_bf16 v[48:51], v[156:159], v[206:209], v[48:51]
	v_mfma_f32_16x16x32_bf16 v[24:27], v[140:143], v[228:231], v[24:27]
	v_mfma_f32_16x16x32_bf16 v[16:19], v[156:159], v[228:231], v[16:19]
	v_mfma_f32_16x16x32_bf16 v[100:103], v[160:163], v[176:179], v[100:103]
	v_mfma_f32_16x16x32_bf16 v[96:99], v[168:171], v[176:179], v[96:99]
	v_mfma_f32_16x16x32_bf16 v[68:71], v[160:163], v[194:197], v[68:71]
	v_mfma_f32_16x16x32_bf16 v[64:67], v[168:171], v[194:197], v[64:67]
	v_mfma_f32_16x16x32_bf16 v[36:39], v[160:163], v[202:205], v[36:39]
	v_mfma_f32_16x16x32_bf16 v[32:35], v[168:171], v[202:205], v[32:35]
	v_mfma_f32_16x16x32_bf16 v[4:7], v[160:163], v[224:227], v[4:7]
	v_mfma_f32_16x16x32_bf16 v[0:3], v[168:171], v[224:227], v[0:3]
	v_mfma_f32_16x16x32_bf16 v[100:103], v[164:167], v[180:183], v[100:103]
	v_mfma_f32_16x16x32_bf16 v[96:99], v[172:175], v[180:183], v[96:99]
	v_mfma_f32_16x16x32_bf16 v[68:71], v[164:167], v[198:201], v[68:71]
	v_mfma_f32_16x16x32_bf16 v[64:67], v[172:175], v[198:201], v[64:67]
	v_mfma_f32_16x16x32_bf16 v[36:39], v[164:167], v[206:209], v[36:39]
	v_mfma_f32_16x16x32_bf16 v[32:35], v[172:175], v[206:209], v[32:35]
	v_mfma_f32_16x16x32_bf16 v[4:7], v[164:167], v[228:231], v[4:7]
	v_mfma_f32_16x16x32_bf16 v[0:3], v[172:175], v[228:231], v[0:3]
	s_barrier
	s_andn2_b64 vcc, exec, s[18:19]
	s_mov_b64 s[30:31], -1
	s_mov_b64 s[18:19], 0
	s_movk_i32 s36, 0x100
	s_cbranch_vccz .LBB0_599
	s_and_b64 vcc, exec, s[6:7]
	s_cbranch_vccz .LBB0_602
	s_barrier

.LBB0_667:
	s_add_i32 s29, s28, 0x100
	s_and_b64 s[36:37], s[30:31], exec
	s_cselect_b32 s29, 0, s29
	s_cselect_b32 s36, 0, 0
	s_add_u32 s38, s34, s29
	s_addc_u32 s39, s35, s36
	s_add_u32 s29, s16, s28
	s_addc_u32 s36, s17, 0
	s_add_u32 s29, s29, 0x100
	s_addc_u32 s36, s36, 0
	s_add_i32 s42, 0, 0x10000
	s_and_b64 s[30:31], s[30:31], exec
	s_cselect_b32 s41, s9, s36
	s_cselect_b32 s40, s58, s29
	s_add_i32 s29, 0, 0x14000
	s_add_u32 s46, s56, s28
	s_addc_u32 s47, s57, 0
	s_add_i32 s49, s42, s4
	s_add_i32 m0, s20, 0xc000
	s_add_i32 s43, s20, 0xe000
	s_add_i32 s59, s49, 0x2000
	v_add_u32_e32 v75, s42, v72
	s_add_u32 s44, s40, 0x10000
	ds_read_b128 v[76:79], v75
	ds_read_b128 v[80:83], v75 offset:1024
	ds_read_b128 v[84:87], v75 offset:2048
	ds_read_b128 v[88:91], v75 offset:3072
	v_add_u32_e32 v75, s29, v72
	s_addc_u32 s45, s41, 0
	s_add_i32 s60, s29, s4
	ds_read_b128 v[92:95], v75
	ds_read_b128 v[96:99], v75 offset:1024
	ds_read_b128 v[100:103], v75 offset:2048
	ds_read_b128 v[104:107], v75 offset:3072
	s_add_i32 s61, s60, 0x2000
	s_add_i32 s62, 0, 0x18000
	s_add_i32 s63, 0, 0x1c000
	s_add_u32 s36, s38, 0x10000
	s_addc_u32 s37, s39, 0
	s_add_i32 s48, s62, s4
	s_add_i32 s28, s48, 0x2000
	s_add_u32 s30, s40, 0x10080
	s_addc_u32 s31, s41, 0
	s_add_i32 s29, s63, s4
	s_add_i32 s42, s29, 0x2000
	v_lshl_add_u64 v[140:141], s[46:47], 0, v[70:71]
	v_lshl_add_u64 v[140:141], v[140:141], 0, s[68:69]
	ds_read_b128 v[108:111], v74
	ds_read_b128 v[112:115], v74 offset:1024
	ds_read_b128 v[116:119], v74 offset:2048
	ds_read_b128 v[120:123], v74 offset:3072
	ds_read_b128 v[124:127], v74 offset:4096
	ds_read_b128 v[128:131], v74 offset:5120
	ds_read_b128 v[132:135], v74 offset:6144
	ds_read_b128 v[136:139], v74 offset:7168
	global_load_lds_dwordx4 v[140:141], off
	v_lshl_add_u64 v[140:141], s[46:47], 0, v[66:67]
	v_lshl_add_u64 v[140:141], v[140:141], 0, s[68:69]
	s_mov_b32 m0, s43
	s_nop 0
	global_load_lds_dwordx4 v[140:141], off
	s_waitcnt vmcnt(8)
	s_waitcnt lgkmcnt(0)
	s_barrier
	s_waitcnt lgkmcnt(0)
	v_mfma_f32_16x16x32_bf16 v[60:63], v[76:79], v[108:111], v[60:63]
	v_mfma_f32_16x16x32_bf16 v[56:59], v[84:87], v[108:111], v[56:59]
	v_mfma_f32_16x16x32_bf16 v[52:55], v[76:79], v[116:119], v[52:55]
	v_mfma_f32_16x16x32_bf16 v[44:47], v[84:87], v[116:119], v[44:47]
	v_mfma_f32_16x16x32_bf16 v[36:39], v[76:79], v[124:127], v[36:39]
	v_mfma_f32_16x16x32_bf16 v[28:31], v[84:87], v[124:127], v[28:31]
	v_mfma_f32_16x16x32_bf16 v[20:23], v[76:79], v[132:135], v[20:23]
	v_mfma_f32_16x16x32_bf16 v[12:15], v[84:87], v[132:135], v[12:15]
	v_mfma_f32_16x16x32_bf16 v[60:63], v[80:83], v[112:115], v[60:63]
	v_mfma_f32_16x16x32_bf16 v[56:59], v[88:91], v[112:115], v[56:59]
	v_mfma_f32_16x16x32_bf16 v[52:55], v[80:83], v[120:123], v[52:55]
	v_mfma_f32_16x16x32_bf16 v[44:47], v[88:91], v[120:123], v[44:47]
	v_mfma_f32_16x16x32_bf16 v[36:39], v[80:83], v[128:131], v[36:39]
	v_mfma_f32_16x16x32_bf16 v[28:31], v[88:91], v[128:131], v[28:31]
	v_mfma_f32_16x16x32_bf16 v[20:23], v[80:83], v[136:139], v[20:23]
	v_mfma_f32_16x16x32_bf16 v[12:15], v[88:91], v[136:139], v[12:15]
	v_mfma_f32_16x16x32_bf16 v[48:51], v[92:95], v[108:111], v[48:51]
	v_mfma_f32_16x16x32_bf16 v[40:43], v[100:103], v[108:111], v[40:43]
	v_mfma_f32_16x16x32_bf16 v[32:35], v[92:95], v[116:119], v[32:35]
	v_mfma_f32_16x16x32_bf16 v[24:27], v[100:103], v[116:119], v[24:27]
	v_mfma_f32_16x16x32_bf16 v[16:19], v[92:95], v[124:127], v[16:19]
	v_mfma_f32_16x16x32_bf16 v[8:11], v[100:103], v[124:127], v[8:11]
	v_mfma_f32_16x16x32_bf16 v[4:7], v[92:95], v[132:135], v[4:7]
	v_mfma_f32_16x16x32_bf16 v[0:3], v[100:103], v[132:135], v[0:3]
	v_mfma_f32_16x16x32_bf16 v[48:51], v[96:99], v[112:115], v[48:51]
	v_mfma_f32_16x16x32_bf16 v[40:43], v[104:107], v[112:115], v[40:43]
	v_mfma_f32_16x16x32_bf16 v[32:35], v[96:99], v[120:123], v[32:35]
	v_mfma_f32_16x16x32_bf16 v[24:27], v[104:107], v[120:123], v[24:27]
	v_mfma_f32_16x16x32_bf16 v[16:19], v[96:99], v[128:131], v[16:19]
	v_mfma_f32_16x16x32_bf16 v[8:11], v[104:107], v[128:131], v[8:11]
	v_mfma_f32_16x16x32_bf16 v[4:7], v[96:99], v[136:139], v[4:7]
	v_mfma_f32_16x16x32_bf16 v[0:3], v[104:107], v[136:139], v[0:3]
	s_barrier
	s_mov_b32 m0, s49
	v_lshl_add_u64 v[140:141], s[40:41], 0, v[68:69]
	global_load_lds_dwordx4 v[140:141], off
	v_lshl_add_u64 v[142:143], s[40:41], 0, v[64:65]
	s_mov_b32 m0, s59
	v_lshl_add_u64 v[76:77], s[44:45], 0, v[68:69]
	global_load_lds_dwordx4 v[142:143], off
	s_mov_b32 m0, s60
	v_lshl_add_u64 v[144:145], s[38:39], 0, v[70:71]
	global_load_lds_dwordx4 v[76:77], off
	v_lshl_add_u64 v[76:77], s[44:45], 0, v[64:65]
	s_mov_b32 m0, s61
	v_lshl_add_u64 v[146:147], s[38:39], 0, v[66:67]
	global_load_lds_dwordx4 v[76:77], off
	s_mov_b32 m0, s20
	s_nop 0
	global_load_lds_dwordx4 v[144:145], off
	s_mov_b32 m0, s21
	s_nop 0
	global_load_lds_dwordx4 v[146:147], off
	s_waitcnt vmcnt(8)
	s_waitcnt lgkmcnt(0)
	s_barrier
	s_barrier
	v_add_u32_e32 v75, s62, v72
	ds_read_b128 v[76:79], v75
	ds_read_b128 v[80:83], v75 offset:1024
	ds_read_b128 v[84:87], v75 offset:2048
	ds_read_b128 v[88:91], v75 offset:3072
	v_add_u32_e32 v75, s63, v72
	ds_read_b128 v[92:95], v75
	ds_read_b128 v[96:99], v75 offset:1024
	ds_read_b128 v[100:103], v75 offset:2048
	ds_read_b128 v[104:107], v75 offset:3072
	s_mov_b32 m0, s26
	v_lshl_add_u64 v[148:149], s[36:37], 0, v[70:71]
	ds_read_b128 v[108:111], v74 offset:32768
	ds_read_b128 v[112:115], v74 offset:33792
	ds_read_b128 v[116:119], v74 offset:34816
	ds_read_b128 v[120:123], v74 offset:35840
	ds_read_b128 v[124:127], v74 offset:36864
	ds_read_b128 v[128:131], v74 offset:37888
	ds_read_b128 v[132:135], v74 offset:38912
	ds_read_b128 v[136:139], v74 offset:39936
	global_load_lds_dwordx4 v[148:149], off
	v_lshl_add_u64 v[148:149], s[36:37], 0, v[66:67]
	s_mov_b32 m0, s27
	s_nop 0
	global_load_lds_dwordx4 v[148:149], off
	s_waitcnt vmcnt(8)
	s_waitcnt lgkmcnt(0)
	s_barrier
	s_waitcnt lgkmcnt(0)
	v_mfma_f32_16x16x32_bf16 v[60:63], v[76:79], v[108:111], v[60:63]
	v_mfma_f32_16x16x32_bf16 v[56:59], v[84:87], v[108:111], v[56:59]
	v_mfma_f32_16x16x32_bf16 v[52:55], v[76:79], v[116:119], v[52:55]
	v_mfma_f32_16x16x32_bf16 v[44:47], v[84:87], v[116:119], v[44:47]
	v_mfma_f32_16x16x32_bf16 v[36:39], v[76:79], v[124:127], v[36:39]
	v_mfma_f32_16x16x32_bf16 v[28:31], v[84:87], v[124:127], v[28:31]
	v_mfma_f32_16x16x32_bf16 v[20:23], v[76:79], v[132:135], v[20:23]
	v_mfma_f32_16x16x32_bf16 v[12:15], v[84:87], v[132:135], v[12:15]
	v_mfma_f32_16x16x32_bf16 v[60:63], v[80:83], v[112:115], v[60:63]
	v_mfma_f32_16x16x32_bf16 v[56:59], v[88:91], v[112:115], v[56:59]
	v_mfma_f32_16x16x32_bf16 v[52:55], v[80:83], v[120:123], v[52:55]
	v_mfma_f32_16x16x32_bf16 v[44:47], v[88:91], v[120:123], v[44:47]
	v_mfma_f32_16x16x32_bf16 v[36:39], v[80:83], v[128:131], v[36:39]
	v_mfma_f32_16x16x32_bf16 v[28:31], v[88:91], v[128:131], v[28:31]
	v_mfma_f32_16x16x32_bf16 v[20:23], v[80:83], v[136:139], v[20:23]
	v_mfma_f32_16x16x32_bf16 v[12:15], v[88:91], v[136:139], v[12:15]
	v_mfma_f32_16x16x32_bf16 v[48:51], v[92:95], v[108:111], v[48:51]
	v_mfma_f32_16x16x32_bf16 v[40:43], v[100:103], v[108:111], v[40:43]
	v_mfma_f32_16x16x32_bf16 v[32:35], v[92:95], v[116:119], v[32:35]
	v_mfma_f32_16x16x32_bf16 v[24:27], v[100:103], v[116:119], v[24:27]
	v_mfma_f32_16x16x32_bf16 v[16:19], v[92:95], v[124:127], v[16:19]
	v_mfma_f32_16x16x32_bf16 v[8:11], v[100:103], v[124:127], v[8:11]
	v_mfma_f32_16x16x32_bf16 v[4:7], v[92:95], v[132:135], v[4:7]
	v_mfma_f32_16x16x32_bf16 v[0:3], v[100:103], v[132:135], v[0:3]
	v_mfma_f32_16x16x32_bf16 v[48:51], v[96:99], v[112:115], v[48:51]
	v_mfma_f32_16x16x32_bf16 v[40:43], v[104:107], v[112:115], v[40:43]
	v_mfma_f32_16x16x32_bf16 v[32:35], v[96:99], v[120:123], v[32:35]
	v_mfma_f32_16x16x32_bf16 v[24:27], v[104:107], v[120:123], v[24:27]
	v_mfma_f32_16x16x32_bf16 v[16:19], v[96:99], v[128:131], v[16:19]
	v_mfma_f32_16x16x32_bf16 v[8:11], v[104:107], v[128:131], v[8:11]
	v_mfma_f32_16x16x32_bf16 v[4:7], v[96:99], v[136:139], v[4:7]
	v_mfma_f32_16x16x32_bf16 v[0:3], v[104:107], v[136:139], v[0:3]
	s_barrier
	s_mov_b32 m0, s48
	v_lshl_add_u64 v[76:77], v[140:141], 0, s[68:69]
	global_load_lds_dwordx4 v[76:77], off
	v_lshl_add_u64 v[76:77], v[142:143], 0, s[68:69]
	s_mov_b32 m0, s28
	s_nop 0
	global_load_lds_dwordx4 v[76:77], off
	v_lshl_add_u64 v[76:77], s[30:31], 0, v[68:69]
	s_mov_b32 m0, s29
	s_nop 0
	global_load_lds_dwordx4 v[76:77], off
	v_lshl_add_u64 v[76:77], s[30:31], 0, v[64:65]
	s_mov_b32 m0, s42
	s_nop 0
	global_load_lds_dwordx4 v[76:77], off
	v_lshl_add_u64 v[76:77], v[144:145], 0, s[68:69]
	s_mov_b32 m0, s50
	s_nop 0
	global_load_lds_dwordx4 v[76:77], off
	v_lshl_add_u64 v[76:77], v[146:147], 0, s[68:69]
	s_mov_b32 m0, s51
	s_nop 0
	global_load_lds_dwordx4 v[76:77], off
	s_waitcnt vmcnt(8)
	s_waitcnt lgkmcnt(0)
	s_barrier
	s_barrier
	s_andn2_b64 vcc, exec, s[18:19]
	s_mov_b64 s[30:31], -1
	s_mov_b64 s[18:19], 0
	s_movk_i32 s28, 0x100
	s_cbranch_vccz .LBB0_667
	s_and_b64 vcc, exec, s[6:7]
	s_cbranch_vccz .LBB0_670
	s_barrier

.LBB0_682:
	s_add_u32 s18, s16, 0x100
	s_addc_u32 s19, s17, 0
	s_add_u32 s28, s45, s16
	s_addc_u32 s29, s46, s17
	s_cmp_eq_u32 s47, 4
	s_cselect_b32 s36, 0, s18
	s_cselect_b32 s37, 0, s19
	s_cselect_b32 s30, s44, s28
	s_cselect_b32 s31, s9, s29
	s_add_u32 s36, s64, s36
	s_addc_u32 s37, s65, s37
	s_add_i32 s28, 0, 0x10000
	s_add_i32 s29, 0, 0x14000
	v_add_u32_e32 v168, s28, v154
	v_add_u32_e32 v194, s29, v154
	ds_read_b128 v[156:159], v168
	ds_read_b128 v[160:163], v168 offset:1024
	ds_read_b128 v[164:167], v168 offset:2048
	ds_read_b128 v[168:171], v168 offset:3072
	ds_read_b128 v[172:175], v194
	ds_read_b128 v[176:179], v194 offset:1024
	ds_read_b128 v[180:183], v194 offset:2048
	ds_read_b128 v[194:197], v194 offset:3072
	v_lshl_add_u64 v[210:211], v[150:151], 0, s[16:17]
	s_add_i32 m0, s20, 0xc000
	ds_read_b128 v[198:201], v155
	ds_read_b128 v[202:205], v155 offset:1024
	ds_read_b128 v[206:209], v155 offset:2048
	ds_read_b128 v[224:227], v155 offset:3072
	ds_read_b128 v[228:231], v155 offset:4096
	ds_read_b128 v[232:235], v155 offset:5120
	ds_read_b128 v[236:239], v155 offset:6144
	ds_read_b128 v[240:243], v155 offset:7168
	global_load_lds_dwordx4 v[210:211], off
	v_lshl_add_u64 v[210:211], v[152:153], 0, s[16:17]
	s_add_i32 m0, s20, 0xe000
	s_nop 0
	global_load_lds_dwordx4 v[210:211], off
	s_waitcnt vmcnt(8)
	s_waitcnt lgkmcnt(0)
	s_barrier
	s_waitcnt lgkmcnt(0)
	v_mfma_f32_16x16x32_bf16 v[124:127], v[156:159], v[198:201], v[124:127]
	v_mfma_f32_16x16x32_bf16 v[120:123], v[164:167], v[198:201], v[120:123]
	v_mfma_f32_16x16x32_bf16 v[116:119], v[156:159], v[206:209], v[116:119]
	v_mfma_f32_16x16x32_bf16 v[108:111], v[164:167], v[206:209], v[108:111]
	v_mfma_f32_16x16x32_bf16 v[100:103], v[156:159], v[228:231], v[100:103]
	v_mfma_f32_16x16x32_bf16 v[92:95], v[164:167], v[228:231], v[92:95]
	v_mfma_f32_16x16x32_bf16 v[84:87], v[156:159], v[236:239], v[84:87]
	v_mfma_f32_16x16x32_bf16 v[76:79], v[164:167], v[236:239], v[76:79]
	v_mfma_f32_16x16x32_bf16 v[124:127], v[160:163], v[202:205], v[124:127]
	v_mfma_f32_16x16x32_bf16 v[120:123], v[168:171], v[202:205], v[120:123]
	v_mfma_f32_16x16x32_bf16 v[116:119], v[160:163], v[224:227], v[116:119]
	v_mfma_f32_16x16x32_bf16 v[108:111], v[168:171], v[224:227], v[108:111]
	v_mfma_f32_16x16x32_bf16 v[100:103], v[160:163], v[232:235], v[100:103]
	v_mfma_f32_16x16x32_bf16 v[92:95], v[168:171], v[232:235], v[92:95]
	v_mfma_f32_16x16x32_bf16 v[84:87], v[160:163], v[240:243], v[84:87]
	v_mfma_f32_16x16x32_bf16 v[76:79], v[168:171], v[240:243], v[76:79]
	v_mfma_f32_16x16x32_bf16 v[112:115], v[172:175], v[198:201], v[112:115]
	v_mfma_f32_16x16x32_bf16 v[104:107], v[180:183], v[198:201], v[104:107]
	v_mfma_f32_16x16x32_bf16 v[96:99], v[172:175], v[206:209], v[96:99]
	v_mfma_f32_16x16x32_bf16 v[88:91], v[180:183], v[206:209], v[88:91]
	v_mfma_f32_16x16x32_bf16 v[80:83], v[172:175], v[228:231], v[80:83]
	v_mfma_f32_16x16x32_bf16 v[72:75], v[180:183], v[228:231], v[72:75]
	v_mfma_f32_16x16x32_bf16 v[68:71], v[172:175], v[236:239], v[68:71]
	v_mfma_f32_16x16x32_bf16 v[64:67], v[180:183], v[236:239], v[64:67]
	v_mfma_f32_16x16x32_bf16 v[112:115], v[176:179], v[202:205], v[112:115]
	v_mfma_f32_16x16x32_bf16 v[104:107], v[194:197], v[202:205], v[104:107]
	v_mfma_f32_16x16x32_bf16 v[96:99], v[176:179], v[224:227], v[96:99]
	v_mfma_f32_16x16x32_bf16 v[88:91], v[194:197], v[224:227], v[88:91]
	v_mfma_f32_16x16x32_bf16 v[80:83], v[176:179], v[232:235], v[80:83]
	v_mfma_f32_16x16x32_bf16 v[72:75], v[194:197], v[232:235], v[72:75]
	v_mfma_f32_16x16x32_bf16 v[68:71], v[176:179], v[240:243], v[68:71]
	v_mfma_f32_16x16x32_bf16 v[64:67], v[194:197], v[240:243], v[64:67]
	s_barrier
	s_add_i32 s16, s28, s4
	v_lshl_add_u64 v[210:211], s[30:31], 0, v[184:185]
	s_mov_b32 m0, s16
	ds_read_b128 v[198:201], v155 offset:16384
	ds_read_b128 v[202:205], v155 offset:17408
	ds_read_b128 v[206:209], v155 offset:18432
	ds_read_b128 v[224:227], v155 offset:19456
	ds_read_b128 v[228:231], v155 offset:20480
	ds_read_b128 v[232:235], v155 offset:21504
	ds_read_b128 v[236:239], v155 offset:22528
	ds_read_b128 v[240:243], v155 offset:23552
	global_load_lds_dwordx4 v[210:211], off
	s_add_i32 m0, s16, 0x2000
	s_add_u32 s16, s30, 0x20000
	v_lshl_add_u64 v[244:245], s[30:31], 0, v[128:129]
	s_addc_u32 s17, s31, 0
	s_add_i32 s28, s29, s4
	global_load_lds_dwordx4 v[244:245], off
	v_lshl_add_u64 v[246:247], s[16:17], 0, v[184:185]
	s_mov_b32 m0, s28
	v_lshl_add_u64 v[218:219], s[36:37], 0, v[130:131]
	global_load_lds_dwordx4 v[246:247], off
	v_lshl_add_u64 v[246:247], s[16:17], 0, v[128:129]
	s_add_i32 m0, s28, 0x2000
	s_nop 0
	global_load_lds_dwordx4 v[246:247], off
	v_lshl_add_u64 v[246:247], s[36:37], 0, v[132:133]
	s_mov_b32 m0, s20
	s_nop 0
	global_load_lds_dwordx4 v[246:247], off
	s_mov_b32 m0, s21
	s_nop 0
	global_load_lds_dwordx4 v[218:219], off
	s_waitcnt vmcnt(8)
	s_waitcnt lgkmcnt(0)
	s_barrier
	s_waitcnt lgkmcnt(0)
	v_mfma_f32_16x16x32_bf16 v[60:63], v[156:159], v[198:201], v[60:63]
	v_mfma_f32_16x16x32_bf16 v[56:59], v[164:167], v[198:201], v[56:59]
	v_mfma_f32_16x16x32_bf16 v[52:55], v[156:159], v[206:209], v[52:55]
	v_mfma_f32_16x16x32_bf16 v[44:47], v[164:167], v[206:209], v[44:47]
	v_mfma_f32_16x16x32_bf16 v[36:39], v[156:159], v[228:231], v[36:39]
	v_mfma_f32_16x16x32_bf16 v[28:31], v[164:167], v[228:231], v[28:31]
	v_mfma_f32_16x16x32_bf16 v[20:23], v[156:159], v[236:239], v[20:23]
	v_mfma_f32_16x16x32_bf16 v[12:15], v[164:167], v[236:239], v[12:15]
	v_mfma_f32_16x16x32_bf16 v[60:63], v[160:163], v[202:205], v[60:63]
	v_mfma_f32_16x16x32_bf16 v[56:59], v[168:171], v[202:205], v[56:59]
	v_mfma_f32_16x16x32_bf16 v[52:55], v[160:163], v[224:227], v[52:55]
	v_mfma_f32_16x16x32_bf16 v[44:47], v[168:171], v[224:227], v[44:47]
	v_mfma_f32_16x16x32_bf16 v[36:39], v[160:163], v[232:235], v[36:39]
	v_mfma_f32_16x16x32_bf16 v[28:31], v[168:171], v[232:235], v[28:31]
	v_mfma_f32_16x16x32_bf16 v[20:23], v[160:163], v[240:243], v[20:23]
	v_mfma_f32_16x16x32_bf16 v[12:15], v[168:171], v[240:243], v[12:15]
	v_mfma_f32_16x16x32_bf16 v[48:51], v[172:175], v[198:201], v[48:51]
	v_mfma_f32_16x16x32_bf16 v[40:43], v[180:183], v[198:201], v[40:43]
	v_mfma_f32_16x16x32_bf16 v[32:35], v[172:175], v[206:209], v[32:35]
	v_mfma_f32_16x16x32_bf16 v[24:27], v[180:183], v[206:209], v[24:27]
	v_mfma_f32_16x16x32_bf16 v[16:19], v[172:175], v[228:231], v[16:19]
	v_mfma_f32_16x16x32_bf16 v[8:11], v[180:183], v[228:231], v[8:11]
	v_mfma_f32_16x16x32_bf16 v[4:7], v[172:175], v[236:239], v[4:7]
	v_mfma_f32_16x16x32_bf16 v[0:3], v[180:183], v[236:239], v[0:3]
	v_mfma_f32_16x16x32_bf16 v[48:51], v[176:179], v[202:205], v[48:51]
	v_mfma_f32_16x16x32_bf16 v[40:43], v[194:197], v[202:205], v[40:43]
	v_mfma_f32_16x16x32_bf16 v[32:35], v[176:179], v[224:227], v[32:35]
	v_mfma_f32_16x16x32_bf16 v[24:27], v[194:197], v[224:227], v[24:27]
	v_mfma_f32_16x16x32_bf16 v[16:19], v[176:179], v[232:235], v[16:19]
	v_mfma_f32_16x16x32_bf16 v[8:11], v[194:197], v[232:235], v[8:11]
	v_mfma_f32_16x16x32_bf16 v[4:7], v[176:179], v[240:243], v[4:7]
	v_mfma_f32_16x16x32_bf16 v[0:3], v[194:197], v[240:243], v[0:3]
	s_barrier
	s_add_i32 s28, 0, 0x18000
	s_add_i32 s29, 0, 0x1c000
	v_add_u32_e32 v168, s28, v154
	v_add_u32_e32 v194, s29, v154
	ds_read_b128 v[156:159], v168
	ds_read_b128 v[160:163], v168 offset:1024
	ds_read_b128 v[164:167], v168 offset:2048
	ds_read_b128 v[168:171], v168 offset:3072
	ds_read_b128 v[172:175], v194
	ds_read_b128 v[176:179], v194 offset:1024
	ds_read_b128 v[180:183], v194 offset:2048
	ds_read_b128 v[194:197], v194 offset:3072
	s_add_u32 s16, s36, 0x20000
	s_addc_u32 s17, s37, 0
	s_mov_b32 m0, s26
	v_lshl_add_u64 v[216:217], s[16:17], 0, v[132:133]
	ds_read_b128 v[198:201], v155 offset:32768
	ds_read_b128 v[202:205], v155 offset:33792
	ds_read_b128 v[206:209], v155 offset:34816
	ds_read_b128 v[224:227], v155 offset:35840
	ds_read_b128 v[228:231], v155 offset:36864
	ds_read_b128 v[232:235], v155 offset:37888
	ds_read_b128 v[236:239], v155 offset:38912
	ds_read_b128 v[240:243], v155 offset:39936
	global_load_lds_dwordx4 v[216:217], off
	v_lshl_add_u64 v[216:217], s[16:17], 0, v[130:131]
	s_mov_b32 m0, s27
	s_nop 0
	global_load_lds_dwordx4 v[216:217], off
	s_waitcnt vmcnt(8)
	s_waitcnt lgkmcnt(0)
	s_barrier
	s_waitcnt lgkmcnt(0)
	v_mfma_f32_16x16x32_bf16 v[124:127], v[156:159], v[198:201], v[124:127]
	v_mfma_f32_16x16x32_bf16 v[120:123], v[164:167], v[198:201], v[120:123]
	v_mfma_f32_16x16x32_bf16 v[116:119], v[156:159], v[206:209], v[116:119]
	v_mfma_f32_16x16x32_bf16 v[108:111], v[164:167], v[206:209], v[108:111]
	v_mfma_f32_16x16x32_bf16 v[100:103], v[156:159], v[228:231], v[100:103]
	v_mfma_f32_16x16x32_bf16 v[92:95], v[164:167], v[228:231], v[92:95]
	v_mfma_f32_16x16x32_bf16 v[84:87], v[156:159], v[236:239], v[84:87]
	v_mfma_f32_16x16x32_bf16 v[76:79], v[164:167], v[236:239], v[76:79]
	v_mfma_f32_16x16x32_bf16 v[124:127], v[160:163], v[202:205], v[124:127]
	v_mfma_f32_16x16x32_bf16 v[120:123], v[168:171], v[202:205], v[120:123]
	v_mfma_f32_16x16x32_bf16 v[116:119], v[160:163], v[224:227], v[116:119]
	v_mfma_f32_16x16x32_bf16 v[108:111], v[168:171], v[224:227], v[108:111]
	v_mfma_f32_16x16x32_bf16 v[100:103], v[160:163], v[232:235], v[100:103]
	v_mfma_f32_16x16x32_bf16 v[92:95], v[168:171], v[232:235], v[92:95]
	v_mfma_f32_16x16x32_bf16 v[84:87], v[160:163], v[240:243], v[84:87]
	v_mfma_f32_16x16x32_bf16 v[76:79], v[168:171], v[240:243], v[76:79]
	v_mfma_f32_16x16x32_bf16 v[112:115], v[172:175], v[198:201], v[112:115]
	v_mfma_f32_16x16x32_bf16 v[104:107], v[180:183], v[198:201], v[104:107]
	v_mfma_f32_16x16x32_bf16 v[96:99], v[172:175], v[206:209], v[96:99]
	v_mfma_f32_16x16x32_bf16 v[88:91], v[180:183], v[206:209], v[88:91]
	v_mfma_f32_16x16x32_bf16 v[80:83], v[172:175], v[228:231], v[80:83]
	v_mfma_f32_16x16x32_bf16 v[72:75], v[180:183], v[228:231], v[72:75]
	v_mfma_f32_16x16x32_bf16 v[68:71], v[172:175], v[236:239], v[68:71]
	v_mfma_f32_16x16x32_bf16 v[64:67], v[180:183], v[236:239], v[64:67]
	v_mfma_f32_16x16x32_bf16 v[112:115], v[176:179], v[202:205], v[112:115]
	v_mfma_f32_16x16x32_bf16 v[104:107], v[194:197], v[202:205], v[104:107]
	v_mfma_f32_16x16x32_bf16 v[96:99], v[176:179], v[224:227], v[96:99]
	v_mfma_f32_16x16x32_bf16 v[88:91], v[194:197], v[224:227], v[88:91]
	v_mfma_f32_16x16x32_bf16 v[80:83], v[176:179], v[232:235], v[80:83]
	v_mfma_f32_16x16x32_bf16 v[72:75], v[194:197], v[232:235], v[72:75]
	v_mfma_f32_16x16x32_bf16 v[68:71], v[176:179], v[240:243], v[68:71]
	v_mfma_f32_16x16x32_bf16 v[64:67], v[194:197], v[240:243], v[64:67]
	s_barrier
	s_add_i32 s16, s28, s4
	v_lshl_add_u64 v[210:211], v[210:211], 0, s[68:69]
	s_mov_b32 m0, s16
	ds_read_b128 v[198:201], v155 offset:49152
	ds_read_b128 v[202:205], v155 offset:50176
	ds_read_b128 v[206:209], v155 offset:51200
	ds_read_b128 v[224:227], v155 offset:52224
	ds_read_b128 v[228:231], v155 offset:53248
	ds_read_b128 v[232:235], v155 offset:54272
	ds_read_b128 v[236:239], v155 offset:55296
	ds_read_b128 v[240:243], v155 offset:56320
	global_load_lds_dwordx4 v[210:211], off
	s_add_i32 m0, s16, 0x2000
	s_add_u32 s16, s30, 0x20080
	v_lshl_add_u64 v[210:211], v[244:245], 0, s[68:69]
	s_addc_u32 s17, s31, 0
	s_add_i32 s28, s29, s4
	global_load_lds_dwordx4 v[210:211], off
	v_lshl_add_u64 v[210:211], s[16:17], 0, v[184:185]
	s_mov_b32 m0, s28
	s_nop 0
	global_load_lds_dwordx4 v[210:211], off
	v_lshl_add_u64 v[210:211], s[16:17], 0, v[128:129]
	s_add_i32 m0, s28, 0x2000
	s_nop 0
	global_load_lds_dwordx4 v[210:211], off
	v_lshl_add_u64 v[210:211], v[246:247], 0, s[68:69]
	s_mov_b32 m0, s38
	s_nop 0
	global_load_lds_dwordx4 v[210:211], off
	v_lshl_add_u64 v[210:211], v[218:219], 0, s[68:69]
	s_mov_b32 m0, s39
	s_nop 0
	global_load_lds_dwordx4 v[210:211], off
	s_waitcnt vmcnt(8)
	s_waitcnt lgkmcnt(0)
	s_barrier
	s_waitcnt lgkmcnt(0)
	v_mfma_f32_16x16x32_bf16 v[60:63], v[156:159], v[198:201], v[60:63]
	v_mfma_f32_16x16x32_bf16 v[56:59], v[164:167], v[198:201], v[56:59]
	v_mfma_f32_16x16x32_bf16 v[52:55], v[156:159], v[206:209], v[52:55]
	v_mfma_f32_16x16x32_bf16 v[44:47], v[164:167], v[206:209], v[44:47]
	v_mfma_f32_16x16x32_bf16 v[36:39], v[156:159], v[228:231], v[36:39]
	v_mfma_f32_16x16x32_bf16 v[28:31], v[164:167], v[228:231], v[28:31]
	v_mfma_f32_16x16x32_bf16 v[20:23], v[156:159], v[236:239], v[20:23]
	v_mfma_f32_16x16x32_bf16 v[12:15], v[164:167], v[236:239], v[12:15]
	v_mfma_f32_16x16x32_bf16 v[60:63], v[160:163], v[202:205], v[60:63]
	v_mfma_f32_16x16x32_bf16 v[56:59], v[168:171], v[202:205], v[56:59]
	v_mfma_f32_16x16x32_bf16 v[52:55], v[160:163], v[224:227], v[52:55]
	v_mfma_f32_16x16x32_bf16 v[44:47], v[168:171], v[224:227], v[44:47]
	v_mfma_f32_16x16x32_bf16 v[36:39], v[160:163], v[232:235], v[36:39]
	v_mfma_f32_16x16x32_bf16 v[28:31], v[168:171], v[232:235], v[28:31]
	v_mfma_f32_16x16x32_bf16 v[20:23], v[160:163], v[240:243], v[20:23]
	v_mfma_f32_16x16x32_bf16 v[12:15], v[168:171], v[240:243], v[12:15]
	v_mfma_f32_16x16x32_bf16 v[48:51], v[172:175], v[198:201], v[48:51]
	v_mfma_f32_16x16x32_bf16 v[40:43], v[180:183], v[198:201], v[40:43]
	v_mfma_f32_16x16x32_bf16 v[32:35], v[172:175], v[206:209], v[32:35]
	v_mfma_f32_16x16x32_bf16 v[24:27], v[180:183], v[206:209], v[24:27]
	v_mfma_f32_16x16x32_bf16 v[16:19], v[172:175], v[228:231], v[16:19]
	v_mfma_f32_16x16x32_bf16 v[8:11], v[180:183], v[228:231], v[8:11]
	v_mfma_f32_16x16x32_bf16 v[4:7], v[172:175], v[236:239], v[4:7]
	v_mfma_f32_16x16x32_bf16 v[0:3], v[180:183], v[236:239], v[0:3]
	v_mfma_f32_16x16x32_bf16 v[48:51], v[176:179], v[202:205], v[48:51]
	v_mfma_f32_16x16x32_bf16 v[40:43], v[194:197], v[202:205], v[40:43]
	v_mfma_f32_16x16x32_bf16 v[32:35], v[176:179], v[224:227], v[32:35]
	v_mfma_f32_16x16x32_bf16 v[24:27], v[194:197], v[224:227], v[24:27]
	v_mfma_f32_16x16x32_bf16 v[16:19], v[176:179], v[232:235], v[16:19]
	v_mfma_f32_16x16x32_bf16 v[8:11], v[194:197], v[232:235], v[8:11]
	v_mfma_f32_16x16x32_bf16 v[4:7], v[176:179], v[240:243], v[4:7]
	v_mfma_f32_16x16x32_bf16 v[0:3], v[194:197], v[240:243], v[0:3]
	s_barrier
	s_add_i32 s47, s47, 2
	s_cmp_gt_u32 s47, 5
	s_mov_b64 s[16:17], s[18:19]
	s_cbranch_scc0 .LBB0_682
	s_and_b64 vcc, exec, s[6:7]
	s_cbranch_vccz .LBB0_685
	s_barrier

.LBB0_805:
	s_add_u32 s28, s30, 0xfff80080
	s_addc_u32 s29, s31, -1
	s_add_i32 s38, 0, 0x10000
	s_cmp_eq_u32 s78, 28
	s_cselect_b32 s45, s9, s29
	s_cselect_b32 s44, s11, s28
	s_cselect_b32 s41, s60, s63
	s_cselect_b32 s40, s61, s62
	s_add_i32 s39, 0, 0x14000
	v_add_u32_e32 v154, s38, v143
	v_add_u32_e32 v170, s39, v143
	ds_read_b128 v[138:141], v154
	ds_read_b128 v[146:149], v154 offset:1024
	ds_read_b128 v[150:153], v154 offset:2048
	ds_read_b128 v[154:157], v154 offset:3072
	ds_read_b128 v[158:161], v170
	ds_read_b128 v[162:165], v170 offset:1024
	ds_read_b128 v[166:169], v170 offset:2048
	ds_read_b128 v[170:173], v170 offset:3072
	v_lshl_add_u64 v[182:183], s[30:31], 0, v[134:135]
	s_add_i32 m0, s21, 0xc000
	ds_read_b128 v[174:177], v145
	ds_read_b128 v[178:181], v145 offset:1024
	ds_read_b128 v[194:197], v145 offset:2048
	ds_read_b128 v[198:201], v145 offset:3072
	ds_read_b128 v[202:205], v145 offset:4096
	ds_read_b128 v[206:209], v145 offset:5120
	ds_read_b128 v[224:227], v145 offset:6144
	ds_read_b128 v[228:231], v145 offset:7168
	global_load_lds_dwordx4 v[182:183], off
	v_lshl_add_u64 v[182:183], s[30:31], 0, v[136:137]
	s_add_i32 m0, s21, 0xe000
	s_nop 0
	global_load_lds_dwordx4 v[182:183], off
	s_waitcnt vmcnt(8)
	s_waitcnt lgkmcnt(0)
	s_barrier
	s_waitcnt lgkmcnt(0)
	v_mfma_f32_16x16x32_bf16 v[124:127], v[138:141], v[174:177], v[124:127]
	v_mfma_f32_16x16x32_bf16 v[120:123], v[150:153], v[174:177], v[120:123]
	v_mfma_f32_16x16x32_bf16 v[116:119], v[138:141], v[194:197], v[116:119]
	v_mfma_f32_16x16x32_bf16 v[104:107], v[150:153], v[194:197], v[104:107]
	v_mfma_f32_16x16x32_bf16 v[100:103], v[138:141], v[202:205], v[100:103]
	v_mfma_f32_16x16x32_bf16 v[88:91], v[150:153], v[202:205], v[88:91]
	v_mfma_f32_16x16x32_bf16 v[84:87], v[138:141], v[224:227], v[84:87]
	v_mfma_f32_16x16x32_bf16 v[72:75], v[150:153], v[224:227], v[72:75]
	v_mfma_f32_16x16x32_bf16 v[124:127], v[146:149], v[178:181], v[124:127]
	v_mfma_f32_16x16x32_bf16 v[120:123], v[154:157], v[178:181], v[120:123]
	v_mfma_f32_16x16x32_bf16 v[116:119], v[146:149], v[198:201], v[116:119]
	v_mfma_f32_16x16x32_bf16 v[104:107], v[154:157], v[198:201], v[104:107]
	v_mfma_f32_16x16x32_bf16 v[100:103], v[146:149], v[206:209], v[100:103]
	v_mfma_f32_16x16x32_bf16 v[88:91], v[154:157], v[206:209], v[88:91]
	v_mfma_f32_16x16x32_bf16 v[84:87], v[146:149], v[228:231], v[84:87]
	v_mfma_f32_16x16x32_bf16 v[72:75], v[154:157], v[228:231], v[72:75]
	v_mfma_f32_16x16x32_bf16 v[112:115], v[158:161], v[174:177], v[112:115]
	v_mfma_f32_16x16x32_bf16 v[108:111], v[166:169], v[174:177], v[108:111]
	v_mfma_f32_16x16x32_bf16 v[96:99], v[158:161], v[194:197], v[96:99]
	v_mfma_f32_16x16x32_bf16 v[92:95], v[166:169], v[194:197], v[92:95]
	v_mfma_f32_16x16x32_bf16 v[80:83], v[158:161], v[202:205], v[80:83]
	v_mfma_f32_16x16x32_bf16 v[76:79], v[166:169], v[202:205], v[76:79]
	v_mfma_f32_16x16x32_bf16 v[68:71], v[158:161], v[224:227], v[68:71]
	v_mfma_f32_16x16x32_bf16 v[64:67], v[166:169], v[224:227], v[64:67]
	v_mfma_f32_16x16x32_bf16 v[112:115], v[162:165], v[178:181], v[112:115]
	v_mfma_f32_16x16x32_bf16 v[108:111], v[170:173], v[178:181], v[108:111]
	v_mfma_f32_16x16x32_bf16 v[96:99], v[162:165], v[198:201], v[96:99]
	v_mfma_f32_16x16x32_bf16 v[92:95], v[170:173], v[198:201], v[92:95]
	v_mfma_f32_16x16x32_bf16 v[80:83], v[162:165], v[206:209], v[80:83]
	v_mfma_f32_16x16x32_bf16 v[76:79], v[170:173], v[206:209], v[76:79]
	v_mfma_f32_16x16x32_bf16 v[68:71], v[162:165], v[228:231], v[68:71]
	v_mfma_f32_16x16x32_bf16 v[64:67], v[170:173], v[228:231], v[64:67]
	s_barrier
	s_add_i32 s28, s38, s20
	v_lshl_add_u64 v[182:183], s[40:41], 0, v[184:185]
	s_mov_b32 m0, s28
	ds_read_b128 v[174:177], v145 offset:16384
	ds_read_b128 v[178:181], v145 offset:17408
	ds_read_b128 v[194:197], v145 offset:18432
	ds_read_b128 v[198:201], v145 offset:19456
	ds_read_b128 v[202:205], v145 offset:20480
	ds_read_b128 v[206:209], v145 offset:21504
	ds_read_b128 v[224:227], v145 offset:22528
	ds_read_b128 v[228:231], v145 offset:23552
	global_load_lds_dwordx4 v[182:183], off
	s_add_i32 m0, s28, 0x2000
	s_add_u32 s28, s40, 0x80000
	v_lshl_add_u64 v[210:211], s[40:41], 0, v[128:129]
	s_addc_u32 s29, s41, 0
	s_add_i32 s38, s39, s20
	global_load_lds_dwordx4 v[210:211], off
	v_lshl_add_u64 v[216:217], s[28:29], 0, v[184:185]
	s_mov_b32 m0, s38
	v_lshl_add_u64 v[218:219], s[44:45], 0, v[130:131]
	global_load_lds_dwordx4 v[216:217], off
	v_lshl_add_u64 v[216:217], s[28:29], 0, v[128:129]
	s_add_i32 m0, s38, 0x2000
	s_nop 0
	global_load_lds_dwordx4 v[216:217], off
	v_lshl_add_u64 v[216:217], s[44:45], 0, v[132:133]
	s_mov_b32 m0, s21
	s_nop 0
	global_load_lds_dwordx4 v[216:217], off
	s_mov_b32 m0, s46
	s_nop 0
	global_load_lds_dwordx4 v[218:219], off
	s_waitcnt vmcnt(8)
	s_waitcnt lgkmcnt(0)
	s_barrier
	s_waitcnt lgkmcnt(0)
	v_mfma_f32_16x16x32_bf16 v[60:63], v[138:141], v[174:177], v[60:63]
	v_mfma_f32_16x16x32_bf16 v[56:59], v[150:153], v[174:177], v[56:59]
	v_mfma_f32_16x16x32_bf16 v[52:55], v[138:141], v[194:197], v[52:55]
	v_mfma_f32_16x16x32_bf16 v[40:43], v[150:153], v[194:197], v[40:43]
	v_mfma_f32_16x16x32_bf16 v[36:39], v[138:141], v[202:205], v[36:39]
	v_mfma_f32_16x16x32_bf16 v[24:27], v[150:153], v[202:205], v[24:27]
	v_mfma_f32_16x16x32_bf16 v[20:23], v[138:141], v[224:227], v[20:23]
	v_mfma_f32_16x16x32_bf16 v[8:11], v[150:153], v[224:227], v[8:11]
	v_mfma_f32_16x16x32_bf16 v[60:63], v[146:149], v[178:181], v[60:63]
	v_mfma_f32_16x16x32_bf16 v[56:59], v[154:157], v[178:181], v[56:59]
	v_mfma_f32_16x16x32_bf16 v[52:55], v[146:149], v[198:201], v[52:55]
	v_mfma_f32_16x16x32_bf16 v[40:43], v[154:157], v[198:201], v[40:43]
	v_mfma_f32_16x16x32_bf16 v[36:39], v[146:149], v[206:209], v[36:39]
	v_mfma_f32_16x16x32_bf16 v[24:27], v[154:157], v[206:209], v[24:27]
	v_mfma_f32_16x16x32_bf16 v[20:23], v[146:149], v[228:231], v[20:23]
	v_mfma_f32_16x16x32_bf16 v[8:11], v[154:157], v[228:231], v[8:11]
	v_mfma_f32_16x16x32_bf16 v[48:51], v[158:161], v[174:177], v[48:51]
	v_mfma_f32_16x16x32_bf16 v[44:47], v[166:169], v[174:177], v[44:47]
	v_mfma_f32_16x16x32_bf16 v[32:35], v[158:161], v[194:197], v[32:35]
	v_mfma_f32_16x16x32_bf16 v[28:31], v[166:169], v[194:197], v[28:31]
	v_mfma_f32_16x16x32_bf16 v[16:19], v[158:161], v[202:205], v[16:19]
	v_mfma_f32_16x16x32_bf16 v[12:15], v[166:169], v[202:205], v[12:15]
	v_mfma_f32_16x16x32_bf16 v[4:7], v[158:161], v[224:227], v[4:7]
	v_mfma_f32_16x16x32_bf16 v[0:3], v[166:169], v[224:227], v[0:3]
	v_mfma_f32_16x16x32_bf16 v[48:51], v[162:165], v[178:181], v[48:51]
	v_mfma_f32_16x16x32_bf16 v[44:47], v[170:173], v[178:181], v[44:47]
	v_mfma_f32_16x16x32_bf16 v[32:35], v[162:165], v[198:201], v[32:35]
	v_mfma_f32_16x16x32_bf16 v[28:31], v[170:173], v[198:201], v[28:31]
	v_mfma_f32_16x16x32_bf16 v[16:19], v[162:165], v[206:209], v[16:19]
	v_mfma_f32_16x16x32_bf16 v[12:15], v[170:173], v[206:209], v[12:15]
	v_mfma_f32_16x16x32_bf16 v[4:7], v[162:165], v[228:231], v[4:7]
	v_mfma_f32_16x16x32_bf16 v[0:3], v[170:173], v[228:231], v[0:3]
	s_barrier
	s_add_i32 s38, 0, 0x18000
	s_add_i32 s39, 0, 0x1c000
	v_add_u32_e32 v154, s38, v143
	v_add_u32_e32 v170, s39, v143
	ds_read_b128 v[138:141], v154
	ds_read_b128 v[146:149], v154 offset:1024
	ds_read_b128 v[150:153], v154 offset:2048
	ds_read_b128 v[154:157], v154 offset:3072
	ds_read_b128 v[158:161], v170
	ds_read_b128 v[162:165], v170 offset:1024
	ds_read_b128 v[166:169], v170 offset:2048
	ds_read_b128 v[170:173], v170 offset:3072
	s_add_u32 s28, s44, 0x80000
	s_addc_u32 s29, s45, 0
	s_mov_b32 m0, s47
	v_lshl_add_u64 v[232:233], s[28:29], 0, v[132:133]
	ds_read_b128 v[174:177], v145 offset:32768
	ds_read_b128 v[178:181], v145 offset:33792
	ds_read_b128 v[194:197], v145 offset:34816
	ds_read_b128 v[198:201], v145 offset:35840
	ds_read_b128 v[202:205], v145 offset:36864
	ds_read_b128 v[206:209], v145 offset:37888
	ds_read_b128 v[224:227], v145 offset:38912
	ds_read_b128 v[228:231], v145 offset:39936
	global_load_lds_dwordx4 v[232:233], off
	v_lshl_add_u64 v[232:233], s[28:29], 0, v[130:131]
	s_mov_b32 m0, s50
	s_nop 0
	global_load_lds_dwordx4 v[232:233], off
	s_waitcnt vmcnt(8)
	s_waitcnt lgkmcnt(0)
	s_barrier
	s_waitcnt lgkmcnt(0)
	v_mfma_f32_16x16x32_bf16 v[124:127], v[138:141], v[174:177], v[124:127]
	v_mfma_f32_16x16x32_bf16 v[120:123], v[150:153], v[174:177], v[120:123]
	v_mfma_f32_16x16x32_bf16 v[116:119], v[138:141], v[194:197], v[116:119]
	v_mfma_f32_16x16x32_bf16 v[104:107], v[150:153], v[194:197], v[104:107]
	v_mfma_f32_16x16x32_bf16 v[100:103], v[138:141], v[202:205], v[100:103]
	v_mfma_f32_16x16x32_bf16 v[88:91], v[150:153], v[202:205], v[88:91]
	v_mfma_f32_16x16x32_bf16 v[84:87], v[138:141], v[224:227], v[84:87]
	v_mfma_f32_16x16x32_bf16 v[72:75], v[150:153], v[224:227], v[72:75]
	v_mfma_f32_16x16x32_bf16 v[124:127], v[146:149], v[178:181], v[124:127]
	v_mfma_f32_16x16x32_bf16 v[120:123], v[154:157], v[178:181], v[120:123]
	v_mfma_f32_16x16x32_bf16 v[116:119], v[146:149], v[198:201], v[116:119]
	v_mfma_f32_16x16x32_bf16 v[104:107], v[154:157], v[198:201], v[104:107]
	v_mfma_f32_16x16x32_bf16 v[100:103], v[146:149], v[206:209], v[100:103]
	v_mfma_f32_16x16x32_bf16 v[88:91], v[154:157], v[206:209], v[88:91]
	v_mfma_f32_16x16x32_bf16 v[84:87], v[146:149], v[228:231], v[84:87]
	v_mfma_f32_16x16x32_bf16 v[72:75], v[154:157], v[228:231], v[72:75]
	v_mfma_f32_16x16x32_bf16 v[112:115], v[158:161], v[174:177], v[112:115]
	v_mfma_f32_16x16x32_bf16 v[108:111], v[166:169], v[174:177], v[108:111]
	v_mfma_f32_16x16x32_bf16 v[96:99], v[158:161], v[194:197], v[96:99]
	v_mfma_f32_16x16x32_bf16 v[92:95], v[166:169], v[194:197], v[92:95]
	v_mfma_f32_16x16x32_bf16 v[80:83], v[158:161], v[202:205], v[80:83]
	v_mfma_f32_16x16x32_bf16 v[76:79], v[166:169], v[202:205], v[76:79]
	v_mfma_f32_16x16x32_bf16 v[68:71], v[158:161], v[224:227], v[68:71]
	v_mfma_f32_16x16x32_bf16 v[64:67], v[166:169], v[224:227], v[64:67]
	v_mfma_f32_16x16x32_bf16 v[112:115], v[162:165], v[178:181], v[112:115]
	v_mfma_f32_16x16x32_bf16 v[108:111], v[170:173], v[178:181], v[108:111]
	v_mfma_f32_16x16x32_bf16 v[96:99], v[162:165], v[198:201], v[96:99]
	v_mfma_f32_16x16x32_bf16 v[92:95], v[170:173], v[198:201], v[92:95]
	v_mfma_f32_16x16x32_bf16 v[80:83], v[162:165], v[206:209], v[80:83]
	v_mfma_f32_16x16x32_bf16 v[76:79], v[170:173], v[206:209], v[76:79]
	v_mfma_f32_16x16x32_bf16 v[68:71], v[162:165], v[228:231], v[68:71]
	v_mfma_f32_16x16x32_bf16 v[64:67], v[170:173], v[228:231], v[64:67]
	s_barrier
	s_add_i32 s28, s38, s20
	v_lshl_add_u64 v[182:183], v[182:183], 0, s[68:69]
	s_mov_b32 m0, s28
	ds_read_b128 v[174:177], v145 offset:49152
	ds_read_b128 v[178:181], v145 offset:50176
	ds_read_b128 v[194:197], v145 offset:51200
	ds_read_b128 v[198:201], v145 offset:52224
	ds_read_b128 v[202:205], v145 offset:53248
	ds_read_b128 v[206:209], v145 offset:54272
	ds_read_b128 v[224:227], v145 offset:55296
	ds_read_b128 v[228:231], v145 offset:56320
	global_load_lds_dwordx4 v[182:183], off
	s_add_i32 m0, s28, 0x2000
	s_add_u32 s28, s40, 0x80080
	v_lshl_add_u64 v[182:183], v[210:211], 0, s[68:69]
	s_addc_u32 s29, s41, 0
	s_add_i32 s38, s39, s20
	global_load_lds_dwordx4 v[182:183], off
	v_lshl_add_u64 v[182:183], s[28:29], 0, v[184:185]
	s_mov_b32 m0, s38
	s_nop 0
	global_load_lds_dwordx4 v[182:183], off
	v_lshl_add_u64 v[182:183], s[28:29], 0, v[128:129]
	s_add_i32 m0, s38, 0x2000
	s_nop 0
	global_load_lds_dwordx4 v[182:183], off
	v_lshl_add_u64 v[182:183], v[216:217], 0, s[68:69]
	s_mov_b32 m0, s51
	s_nop 0
	global_load_lds_dwordx4 v[182:183], off
	v_lshl_add_u64 v[182:183], v[218:219], 0, s[68:69]
	s_mov_b32 m0, s52
	s_nop 0
	global_load_lds_dwordx4 v[182:183], off
	s_waitcnt vmcnt(8)
	s_waitcnt lgkmcnt(0)
	s_barrier
	s_waitcnt lgkmcnt(0)
	v_mfma_f32_16x16x32_bf16 v[60:63], v[138:141], v[174:177], v[60:63]
	v_mfma_f32_16x16x32_bf16 v[56:59], v[150:153], v[174:177], v[56:59]
	v_mfma_f32_16x16x32_bf16 v[52:55], v[138:141], v[194:197], v[52:55]
	v_mfma_f32_16x16x32_bf16 v[40:43], v[150:153], v[194:197], v[40:43]
	v_mfma_f32_16x16x32_bf16 v[36:39], v[138:141], v[202:205], v[36:39]
	v_mfma_f32_16x16x32_bf16 v[24:27], v[150:153], v[202:205], v[24:27]
	v_mfma_f32_16x16x32_bf16 v[20:23], v[138:141], v[224:227], v[20:23]
	v_mfma_f32_16x16x32_bf16 v[8:11], v[150:153], v[224:227], v[8:11]
	v_mfma_f32_16x16x32_bf16 v[60:63], v[146:149], v[178:181], v[60:63]
	v_mfma_f32_16x16x32_bf16 v[56:59], v[154:157], v[178:181], v[56:59]
	v_mfma_f32_16x16x32_bf16 v[52:55], v[146:149], v[198:201], v[52:55]
	v_mfma_f32_16x16x32_bf16 v[40:43], v[154:157], v[198:201], v[40:43]
	v_mfma_f32_16x16x32_bf16 v[36:39], v[146:149], v[206:209], v[36:39]
	v_mfma_f32_16x16x32_bf16 v[24:27], v[154:157], v[206:209], v[24:27]
	v_mfma_f32_16x16x32_bf16 v[20:23], v[146:149], v[228:231], v[20:23]
	v_mfma_f32_16x16x32_bf16 v[8:11], v[154:157], v[228:231], v[8:11]
	v_mfma_f32_16x16x32_bf16 v[48:51], v[158:161], v[174:177], v[48:51]
	v_mfma_f32_16x16x32_bf16 v[44:47], v[166:169], v[174:177], v[44:47]
	v_mfma_f32_16x16x32_bf16 v[32:35], v[158:161], v[194:197], v[32:35]
	v_mfma_f32_16x16x32_bf16 v[28:31], v[166:169], v[194:197], v[28:31]
	v_mfma_f32_16x16x32_bf16 v[16:19], v[158:161], v[202:205], v[16:19]
	v_mfma_f32_16x16x32_bf16 v[12:15], v[166:169], v[202:205], v[12:15]
	v_mfma_f32_16x16x32_bf16 v[4:7], v[158:161], v[224:227], v[4:7]
	v_mfma_f32_16x16x32_bf16 v[0:3], v[166:169], v[224:227], v[0:3]
	v_mfma_f32_16x16x32_bf16 v[48:51], v[162:165], v[178:181], v[48:51]
	v_mfma_f32_16x16x32_bf16 v[44:47], v[170:173], v[178:181], v[44:47]
	v_mfma_f32_16x16x32_bf16 v[32:35], v[162:165], v[198:201], v[32:35]
	v_mfma_f32_16x16x32_bf16 v[28:31], v[170:173], v[198:201], v[28:31]
	v_mfma_f32_16x16x32_bf16 v[16:19], v[162:165], v[206:209], v[16:19]
	v_mfma_f32_16x16x32_bf16 v[12:15], v[170:173], v[206:209], v[12:15]
	v_mfma_f32_16x16x32_bf16 v[4:7], v[162:165], v[228:231], v[4:7]
	v_mfma_f32_16x16x32_bf16 v[0:3], v[170:173], v[228:231], v[0:3]
	s_barrier
	s_add_i32 s78, s78, 2
	s_add_u32 s30, s30, 0x100
	s_addc_u32 s31, s31, 0
	s_add_u32 s62, s62, 0x100
	s_addc_u32 s63, s63, 0
	s_cmp_gt_u32 s78, 29
	s_cbranch_scc0 .LBB0_805
	s_and_b64 vcc, exec, s[6:7]
	s_cbranch_vccz .LBB0_808
	s_barrier

.LBB0_822:
	s_add_u32 s38, s46, s50
	s_addc_u32 s39, s47, 0
	s_add_u32 s42, s38, 0x100
	s_addc_u32 s43, s39, 0
	s_and_b64 s[28:29], s[78:79], exec
	s_cselect_b32 s53, s11, s43
	s_cselect_b32 s52, s13, s42
	s_add_u32 s28, s6, s50
	s_addc_u32 s29, s7, 0
	s_add_u32 s42, s28, 0x100
	s_addc_u32 s43, s29, 0
	s_add_i32 s76, 0, 0x10000
	s_and_b64 s[28:29], s[78:79], exec
	s_cselect_b32 s61, s36, s43
	s_cselect_b32 s60, s37, s42
	s_add_i32 s29, 0, 0x14000
	s_add_u32 vcc_lo, s38, 0x80080
	s_addc_u32 vcc_hi, s39, 0
	s_add_i32 s85, s76, s20
	s_add_i32 m0, s21, 0xc000
	s_add_i32 s90, s21, 0xe000
	s_add_i32 s49, s85, 0x2000
	v_add_u32_e32 v153, s76, v150
	s_add_u32 s62, s60, 0x80000
	ds_read_b128 v[154:157], v153
	ds_read_b128 v[158:161], v153 offset:1024
	ds_read_b128 v[162:165], v153 offset:2048
	ds_read_b128 v[166:169], v153 offset:3072
	v_add_u32_e32 v153, s29, v150
	s_addc_u32 s63, s61, 0
	s_add_i32 s43, s29, s20
	ds_read_b128 v[170:173], v153
	ds_read_b128 v[174:177], v153 offset:1024
	ds_read_b128 v[178:181], v153 offset:2048
	ds_read_b128 v[194:197], v153 offset:3072
	s_add_i32 s42, s43, 0x2000
	s_add_i32 s39, 0, 0x18000
	s_add_i32 s28, 0, 0x1c000
	s_add_u32 s50, s52, 0x80000
	s_addc_u32 s51, s53, 0
	s_add_i32 s38, s39, s20
	s_add_i32 s48, s38, 0x2000
	s_add_u32 s78, s60, 0x80080
	s_addc_u32 s79, s61, 0
	s_add_i32 s76, s28, s20
	s_add_i32 s29, s76, 0x2000
	v_lshl_add_u64 v[182:183], vcc, 0, v[132:133]
	ds_read_b128 v[198:201], v152
	ds_read_b128 v[202:205], v152 offset:1024
	ds_read_b128 v[206:209], v152 offset:2048
	ds_read_b128 v[224:227], v152 offset:3072
	ds_read_b128 v[228:231], v152 offset:4096
	ds_read_b128 v[232:235], v152 offset:5120
	ds_read_b128 v[236:239], v152 offset:6144
	ds_read_b128 v[240:243], v152 offset:7168
	global_load_lds_dwordx4 v[182:183], off
	v_lshl_add_u64 v[182:183], vcc, 0, v[130:131]
	s_mov_b32 m0, s90
	s_nop 0
	global_load_lds_dwordx4 v[182:183], off
	s_waitcnt vmcnt(8)
	s_waitcnt lgkmcnt(0)
	s_barrier
	s_waitcnt lgkmcnt(0)
	v_mfma_f32_16x16x32_bf16 v[124:127], v[154:157], v[198:201], v[124:127]
	v_mfma_f32_16x16x32_bf16 v[120:123], v[162:165], v[198:201], v[120:123]
	v_mfma_f32_16x16x32_bf16 v[116:119], v[154:157], v[206:209], v[116:119]
	v_mfma_f32_16x16x32_bf16 v[112:115], v[162:165], v[206:209], v[112:115]
	v_mfma_f32_16x16x32_bf16 v[108:111], v[154:157], v[228:231], v[108:111]
	v_mfma_f32_16x16x32_bf16 v[104:107], v[162:165], v[228:231], v[104:107]
	v_mfma_f32_16x16x32_bf16 v[96:99], v[154:157], v[236:239], v[96:99]
	v_mfma_f32_16x16x32_bf16 v[88:91], v[162:165], v[236:239], v[88:91]
	v_mfma_f32_16x16x32_bf16 v[124:127], v[158:161], v[202:205], v[124:127]
	v_mfma_f32_16x16x32_bf16 v[120:123], v[166:169], v[202:205], v[120:123]
	v_mfma_f32_16x16x32_bf16 v[116:119], v[158:161], v[224:227], v[116:119]
	v_mfma_f32_16x16x32_bf16 v[112:115], v[166:169], v[224:227], v[112:115]
	v_mfma_f32_16x16x32_bf16 v[108:111], v[158:161], v[232:235], v[108:111]
	v_mfma_f32_16x16x32_bf16 v[104:107], v[166:169], v[232:235], v[104:107]
	v_mfma_f32_16x16x32_bf16 v[96:99], v[158:161], v[240:243], v[96:99]
	v_mfma_f32_16x16x32_bf16 v[88:91], v[166:169], v[240:243], v[88:91]
	v_mfma_f32_16x16x32_bf16 v[100:103], v[170:173], v[198:201], v[100:103]
	v_mfma_f32_16x16x32_bf16 v[92:95], v[178:181], v[198:201], v[92:95]
	v_mfma_f32_16x16x32_bf16 v[84:87], v[170:173], v[206:209], v[84:87]
	v_mfma_f32_16x16x32_bf16 v[80:83], v[178:181], v[206:209], v[80:83]
	v_mfma_f32_16x16x32_bf16 v[76:79], v[170:173], v[228:231], v[76:79]
	v_mfma_f32_16x16x32_bf16 v[72:75], v[178:181], v[228:231], v[72:75]
	v_mfma_f32_16x16x32_bf16 v[68:71], v[170:173], v[236:239], v[68:71]
	v_mfma_f32_16x16x32_bf16 v[64:67], v[178:181], v[236:239], v[64:67]
	v_mfma_f32_16x16x32_bf16 v[100:103], v[174:177], v[202:205], v[100:103]
	v_mfma_f32_16x16x32_bf16 v[92:95], v[194:197], v[202:205], v[92:95]
	v_mfma_f32_16x16x32_bf16 v[84:87], v[174:177], v[224:227], v[84:87]
	v_mfma_f32_16x16x32_bf16 v[80:83], v[194:197], v[224:227], v[80:83]
	v_mfma_f32_16x16x32_bf16 v[76:79], v[174:177], v[232:235], v[76:79]
	v_mfma_f32_16x16x32_bf16 v[72:75], v[194:197], v[232:235], v[72:75]
	v_mfma_f32_16x16x32_bf16 v[68:71], v[174:177], v[240:243], v[68:71]
	v_mfma_f32_16x16x32_bf16 v[64:67], v[194:197], v[240:243], v[64:67]
	s_barrier
	s_mov_b32 m0, s85
	v_lshl_add_u64 v[182:183], s[60:61], 0, v[184:185]
	ds_read_b128 v[198:201], v152 offset:16384
	ds_read_b128 v[202:205], v152 offset:17408
	ds_read_b128 v[206:209], v152 offset:18432
	ds_read_b128 v[224:227], v152 offset:19456
	ds_read_b128 v[228:231], v152 offset:20480
	ds_read_b128 v[232:235], v152 offset:21504
	ds_read_b128 v[236:239], v152 offset:22528
	ds_read_b128 v[240:243], v152 offset:23552
	global_load_lds_dwordx4 v[182:183], off
	v_lshl_add_u64 v[210:211], s[60:61], 0, v[128:129]
	s_mov_b32 m0, s49
	v_lshl_add_u64 v[216:217], s[62:63], 0, v[184:185]
	global_load_lds_dwordx4 v[210:211], off
	s_mov_b32 m0, s43
	v_lshl_add_u64 v[218:219], s[52:53], 0, v[130:131]
	global_load_lds_dwordx4 v[216:217], off
	v_lshl_add_u64 v[216:217], s[62:63], 0, v[128:129]
	s_mov_b32 m0, s42
	s_nop 0
	global_load_lds_dwordx4 v[216:217], off
	v_lshl_add_u64 v[216:217], s[52:53], 0, v[132:133]
	s_mov_b32 m0, s21
	s_nop 0
	global_load_lds_dwordx4 v[216:217], off
	s_mov_b32 m0, s88
	s_nop 0
	global_load_lds_dwordx4 v[218:219], off
	s_waitcnt vmcnt(8)
	s_waitcnt lgkmcnt(0)
	s_barrier
	s_waitcnt lgkmcnt(0)
	v_mfma_f32_16x16x32_bf16 v[60:63], v[154:157], v[198:201], v[60:63]
	v_mfma_f32_16x16x32_bf16 v[56:59], v[162:165], v[198:201], v[56:59]
	v_mfma_f32_16x16x32_bf16 v[52:55], v[154:157], v[206:209], v[52:55]
	v_mfma_f32_16x16x32_bf16 v[48:51], v[162:165], v[206:209], v[48:51]
	v_mfma_f32_16x16x32_bf16 v[44:47], v[154:157], v[228:231], v[44:47]
	v_mfma_f32_16x16x32_bf16 v[40:43], v[162:165], v[228:231], v[40:43]
	v_mfma_f32_16x16x32_bf16 v[32:35], v[154:157], v[236:239], v[32:35]
	v_mfma_f32_16x16x32_bf16 v[24:27], v[162:165], v[236:239], v[24:27]
	v_mfma_f32_16x16x32_bf16 v[60:63], v[158:161], v[202:205], v[60:63]
	v_mfma_f32_16x16x32_bf16 v[56:59], v[166:169], v[202:205], v[56:59]
	v_mfma_f32_16x16x32_bf16 v[52:55], v[158:161], v[224:227], v[52:55]
	v_mfma_f32_16x16x32_bf16 v[48:51], v[166:169], v[224:227], v[48:51]
	v_mfma_f32_16x16x32_bf16 v[44:47], v[158:161], v[232:235], v[44:47]
	v_mfma_f32_16x16x32_bf16 v[40:43], v[166:169], v[232:235], v[40:43]
	v_mfma_f32_16x16x32_bf16 v[32:35], v[158:161], v[240:243], v[32:35]
	v_mfma_f32_16x16x32_bf16 v[24:27], v[166:169], v[240:243], v[24:27]
	v_mfma_f32_16x16x32_bf16 v[36:39], v[170:173], v[198:201], v[36:39]
	v_mfma_f32_16x16x32_bf16 v[28:31], v[178:181], v[198:201], v[28:31]
	v_mfma_f32_16x16x32_bf16 v[20:23], v[170:173], v[206:209], v[20:23]
	v_mfma_f32_16x16x32_bf16 v[16:19], v[178:181], v[206:209], v[16:19]
	v_mfma_f32_16x16x32_bf16 v[12:15], v[170:173], v[228:231], v[12:15]
	v_mfma_f32_16x16x32_bf16 v[8:11], v[178:181], v[228:231], v[8:11]
	v_mfma_f32_16x16x32_bf16 v[4:7], v[170:173], v[236:239], v[4:7]
	v_mfma_f32_16x16x32_bf16 v[0:3], v[178:181], v[236:239], v[0:3]
	v_mfma_f32_16x16x32_bf16 v[36:39], v[174:177], v[202:205], v[36:39]
	v_mfma_f32_16x16x32_bf16 v[28:31], v[194:197], v[202:205], v[28:31]
	v_mfma_f32_16x16x32_bf16 v[20:23], v[174:177], v[224:227], v[20:23]
	v_mfma_f32_16x16x32_bf16 v[16:19], v[194:197], v[224:227], v[16:19]
	v_mfma_f32_16x16x32_bf16 v[12:15], v[174:177], v[232:235], v[12:15]
	v_mfma_f32_16x16x32_bf16 v[8:11], v[194:197], v[232:235], v[8:11]
	v_mfma_f32_16x16x32_bf16 v[4:7], v[174:177], v[240:243], v[4:7]
	v_mfma_f32_16x16x32_bf16 v[0:3], v[194:197], v[240:243], v[0:3]
	s_barrier
	v_add_u32_e32 v153, s39, v150
	ds_read_b128 v[154:157], v153
	ds_read_b128 v[158:161], v153 offset:1024
	ds_read_b128 v[162:165], v153 offset:2048
	ds_read_b128 v[166:169], v153 offset:3072
	v_add_u32_e32 v153, s28, v150
	ds_read_b128 v[170:173], v153
	ds_read_b128 v[174:177], v153 offset:1024
	ds_read_b128 v[178:181], v153 offset:2048
	ds_read_b128 v[194:197], v153 offset:3072
	s_mov_b32 m0, s89
	v_lshl_add_u64 v[244:245], s[50:51], 0, v[132:133]
	ds_read_b128 v[198:201], v152 offset:32768
	ds_read_b128 v[202:205], v152 offset:33792
	ds_read_b128 v[206:209], v152 offset:34816
	ds_read_b128 v[224:227], v152 offset:35840
	ds_read_b128 v[228:231], v152 offset:36864
	ds_read_b128 v[232:235], v152 offset:37888
	ds_read_b128 v[236:239], v152 offset:38912
	ds_read_b128 v[240:243], v152 offset:39936
	global_load_lds_dwordx4 v[244:245], off
	v_lshl_add_u64 v[244:245], s[50:51], 0, v[130:131]
	s_mov_b32 m0, s92
	s_nop 0
	global_load_lds_dwordx4 v[244:245], off
	s_waitcnt vmcnt(8)
	s_waitcnt lgkmcnt(0)
	s_barrier
	s_waitcnt lgkmcnt(0)
	v_mfma_f32_16x16x32_bf16 v[124:127], v[154:157], v[198:201], v[124:127]
	v_mfma_f32_16x16x32_bf16 v[120:123], v[162:165], v[198:201], v[120:123]
	v_mfma_f32_16x16x32_bf16 v[116:119], v[154:157], v[206:209], v[116:119]
	v_mfma_f32_16x16x32_bf16 v[112:115], v[162:165], v[206:209], v[112:115]
	v_mfma_f32_16x16x32_bf16 v[108:111], v[154:157], v[228:231], v[108:111]
	v_mfma_f32_16x16x32_bf16 v[104:107], v[162:165], v[228:231], v[104:107]
	v_mfma_f32_16x16x32_bf16 v[96:99], v[154:157], v[236:239], v[96:99]
	v_mfma_f32_16x16x32_bf16 v[88:91], v[162:165], v[236:239], v[88:91]
	v_mfma_f32_16x16x32_bf16 v[124:127], v[158:161], v[202:205], v[124:127]
	v_mfma_f32_16x16x32_bf16 v[120:123], v[166:169], v[202:205], v[120:123]
	v_mfma_f32_16x16x32_bf16 v[116:119], v[158:161], v[224:227], v[116:119]
	v_mfma_f32_16x16x32_bf16 v[112:115], v[166:169], v[224:227], v[112:115]
	v_mfma_f32_16x16x32_bf16 v[108:111], v[158:161], v[232:235], v[108:111]
	v_mfma_f32_16x16x32_bf16 v[104:107], v[166:169], v[232:235], v[104:107]
	v_mfma_f32_16x16x32_bf16 v[96:99], v[158:161], v[240:243], v[96:99]
	v_mfma_f32_16x16x32_bf16 v[88:91], v[166:169], v[240:243], v[88:91]
	v_mfma_f32_16x16x32_bf16 v[100:103], v[170:173], v[198:201], v[100:103]
	v_mfma_f32_16x16x32_bf16 v[92:95], v[178:181], v[198:201], v[92:95]
	v_mfma_f32_16x16x32_bf16 v[84:87], v[170:173], v[206:209], v[84:87]
	v_mfma_f32_16x16x32_bf16 v[80:83], v[178:181], v[206:209], v[80:83]
	v_mfma_f32_16x16x32_bf16 v[76:79], v[170:173], v[228:231], v[76:79]
	v_mfma_f32_16x16x32_bf16 v[72:75], v[178:181], v[228:231], v[72:75]
	v_mfma_f32_16x16x32_bf16 v[68:71], v[170:173], v[236:239], v[68:71]
	v_mfma_f32_16x16x32_bf16 v[64:67], v[178:181], v[236:239], v[64:67]
	v_mfma_f32_16x16x32_bf16 v[100:103], v[174:177], v[202:205], v[100:103]
	v_mfma_f32_16x16x32_bf16 v[92:95], v[194:197], v[202:205], v[92:95]
	v_mfma_f32_16x16x32_bf16 v[84:87], v[174:177], v[224:227], v[84:87]
	v_mfma_f32_16x16x32_bf16 v[80:83], v[194:197], v[224:227], v[80:83]
	v_mfma_f32_16x16x32_bf16 v[76:79], v[174:177], v[232:235], v[76:79]
	v_mfma_f32_16x16x32_bf16 v[72:75], v[194:197], v[232:235], v[72:75]
	v_mfma_f32_16x16x32_bf16 v[68:71], v[174:177], v[240:243], v[68:71]
	v_mfma_f32_16x16x32_bf16 v[64:67], v[194:197], v[240:243], v[64:67]
	s_barrier
	s_mov_b32 m0, s38
	v_lshl_add_u64 v[182:183], v[182:183], 0, s[68:69]
	ds_read_b128 v[198:201], v152 offset:49152
	ds_read_b128 v[202:205], v152 offset:50176
	ds_read_b128 v[206:209], v152 offset:51200
	ds_read_b128 v[224:227], v152 offset:52224
	ds_read_b128 v[228:231], v152 offset:53248
	ds_read_b128 v[232:235], v152 offset:54272
	ds_read_b128 v[236:239], v152 offset:55296
	ds_read_b128 v[240:243], v152 offset:56320
	global_load_lds_dwordx4 v[182:183], off
	v_lshl_add_u64 v[182:183], v[210:211], 0, s[68:69]
	s_mov_b32 m0, s48
	s_nop 0
	global_load_lds_dwordx4 v[182:183], off
	v_lshl_add_u64 v[182:183], s[78:79], 0, v[184:185]
	s_mov_b32 m0, s76
	s_nop 0
	global_load_lds_dwordx4 v[182:183], off
	v_lshl_add_u64 v[182:183], s[78:79], 0, v[128:129]
	s_mov_b32 m0, s29
	s_nop 0
	global_load_lds_dwordx4 v[182:183], off
	v_lshl_add_u64 v[182:183], v[216:217], 0, s[68:69]
	s_mov_b32 m0, s93
	s_nop 0
	global_load_lds_dwordx4 v[182:183], off
	v_lshl_add_u64 v[182:183], v[218:219], 0, s[68:69]
	s_mov_b32 m0, s94
	s_nop 0
	global_load_lds_dwordx4 v[182:183], off
	s_waitcnt vmcnt(8)
	s_waitcnt lgkmcnt(0)
	s_barrier
	s_waitcnt lgkmcnt(0)
	v_mfma_f32_16x16x32_bf16 v[60:63], v[154:157], v[198:201], v[60:63]
	v_mfma_f32_16x16x32_bf16 v[56:59], v[162:165], v[198:201], v[56:59]
	v_mfma_f32_16x16x32_bf16 v[52:55], v[154:157], v[206:209], v[52:55]
	v_mfma_f32_16x16x32_bf16 v[48:51], v[162:165], v[206:209], v[48:51]
	v_mfma_f32_16x16x32_bf16 v[44:47], v[154:157], v[228:231], v[44:47]
	v_mfma_f32_16x16x32_bf16 v[40:43], v[162:165], v[228:231], v[40:43]
	v_mfma_f32_16x16x32_bf16 v[32:35], v[154:157], v[236:239], v[32:35]
	v_mfma_f32_16x16x32_bf16 v[24:27], v[162:165], v[236:239], v[24:27]
	v_mfma_f32_16x16x32_bf16 v[60:63], v[158:161], v[202:205], v[60:63]
	v_mfma_f32_16x16x32_bf16 v[56:59], v[166:169], v[202:205], v[56:59]
	v_mfma_f32_16x16x32_bf16 v[52:55], v[158:161], v[224:227], v[52:55]
	v_mfma_f32_16x16x32_bf16 v[48:51], v[166:169], v[224:227], v[48:51]
	v_mfma_f32_16x16x32_bf16 v[44:47], v[158:161], v[232:235], v[44:47]
	v_mfma_f32_16x16x32_bf16 v[40:43], v[166:169], v[232:235], v[40:43]
	v_mfma_f32_16x16x32_bf16 v[32:35], v[158:161], v[240:243], v[32:35]
	v_mfma_f32_16x16x32_bf16 v[24:27], v[166:169], v[240:243], v[24:27]
	v_mfma_f32_16x16x32_bf16 v[36:39], v[170:173], v[198:201], v[36:39]
	v_mfma_f32_16x16x32_bf16 v[28:31], v[178:181], v[198:201], v[28:31]
	v_mfma_f32_16x16x32_bf16 v[20:23], v[170:173], v[206:209], v[20:23]
	v_mfma_f32_16x16x32_bf16 v[16:19], v[178:181], v[206:209], v[16:19]
	v_mfma_f32_16x16x32_bf16 v[12:15], v[170:173], v[228:231], v[12:15]
	v_mfma_f32_16x16x32_bf16 v[8:11], v[178:181], v[228:231], v[8:11]
	v_mfma_f32_16x16x32_bf16 v[4:7], v[170:173], v[236:239], v[4:7]
	v_mfma_f32_16x16x32_bf16 v[0:3], v[178:181], v[236:239], v[0:3]
	v_mfma_f32_16x16x32_bf16 v[36:39], v[174:177], v[202:205], v[36:39]
	v_mfma_f32_16x16x32_bf16 v[28:31], v[194:197], v[202:205], v[28:31]
	v_mfma_f32_16x16x32_bf16 v[20:23], v[174:177], v[224:227], v[20:23]
	v_mfma_f32_16x16x32_bf16 v[16:19], v[194:197], v[224:227], v[16:19]
	v_mfma_f32_16x16x32_bf16 v[12:15], v[174:177], v[232:235], v[12:15]
	v_mfma_f32_16x16x32_bf16 v[8:11], v[194:197], v[232:235], v[8:11]
	v_mfma_f32_16x16x32_bf16 v[4:7], v[174:177], v[240:243], v[4:7]
	v_mfma_f32_16x16x32_bf16 v[0:3], v[194:197], v[240:243], v[0:3]
	s_barrier
	s_movk_i32 s50, 0x100
	s_andn2_b64 vcc, exec, s[58:59]
	s_mov_b64 s[78:79], -1
	s_mov_b64 s[58:59], 0
	s_cbranch_vccz .LBB0_822
	s_and_b64 vcc, exec, s[8:9]
	s_cbranch_vccz .LBB0_825
	s_barrier

.LBB0_842:
	s_add_u32 s28, s30, 0xfffc0080
	s_addc_u32 s29, s31, -1
	s_add_i32 s42, 0, 0x10000
	s_cmp_eq_u32 s60, 12
	s_cselect_b32 s45, s9, s29
	s_cselect_b32 s44, s11, s28
	s_cselect_b32 s41, s36, s59
	s_cselect_b32 s40, s37, s58
	s_add_i32 s43, 0, 0x14000
	v_add_u32_e32 v154, s42, v147
	v_add_u32_e32 v170, s43, v147
	ds_read_b128 v[138:141], v154
	ds_read_b128 v[142:145], v154 offset:1024
	ds_read_b128 v[150:153], v154 offset:2048
	ds_read_b128 v[154:157], v154 offset:3072
	ds_read_b128 v[158:161], v170
	ds_read_b128 v[162:165], v170 offset:1024
	ds_read_b128 v[166:169], v170 offset:2048
	ds_read_b128 v[170:173], v170 offset:3072
	v_lshl_add_u64 v[182:183], s[30:31], 0, v[134:135]
	s_add_i32 m0, s21, 0xc000
	ds_read_b128 v[174:177], v149
	ds_read_b128 v[178:181], v149 offset:1024
	ds_read_b128 v[194:197], v149 offset:2048
	ds_read_b128 v[198:201], v149 offset:3072
	ds_read_b128 v[202:205], v149 offset:4096
	ds_read_b128 v[206:209], v149 offset:5120
	ds_read_b128 v[224:227], v149 offset:6144
	ds_read_b128 v[228:231], v149 offset:7168
	global_load_lds_dwordx4 v[182:183], off
	v_lshl_add_u64 v[182:183], s[30:31], 0, v[136:137]
	s_add_i32 m0, s21, 0xe000
	s_nop 0
	global_load_lds_dwordx4 v[182:183], off
	s_waitcnt vmcnt(8)
	s_waitcnt lgkmcnt(0)
	s_barrier
	s_waitcnt lgkmcnt(0)
	v_mfma_f32_16x16x32_bf16 v[124:127], v[138:141], v[174:177], v[124:127]
	v_mfma_f32_16x16x32_bf16 v[120:123], v[150:153], v[174:177], v[120:123]
	v_mfma_f32_16x16x32_bf16 v[108:111], v[138:141], v[194:197], v[108:111]
	v_mfma_f32_16x16x32_bf16 v[104:107], v[150:153], v[194:197], v[104:107]
	v_mfma_f32_16x16x32_bf16 v[92:95], v[138:141], v[202:205], v[92:95]
	v_mfma_f32_16x16x32_bf16 v[88:91], v[150:153], v[202:205], v[88:91]
	v_mfma_f32_16x16x32_bf16 v[76:79], v[138:141], v[224:227], v[76:79]
	v_mfma_f32_16x16x32_bf16 v[72:75], v[150:153], v[224:227], v[72:75]
	v_mfma_f32_16x16x32_bf16 v[124:127], v[142:145], v[178:181], v[124:127]
	v_mfma_f32_16x16x32_bf16 v[120:123], v[154:157], v[178:181], v[120:123]
	v_mfma_f32_16x16x32_bf16 v[108:111], v[142:145], v[198:201], v[108:111]
	v_mfma_f32_16x16x32_bf16 v[104:107], v[154:157], v[198:201], v[104:107]
	v_mfma_f32_16x16x32_bf16 v[92:95], v[142:145], v[206:209], v[92:95]
	v_mfma_f32_16x16x32_bf16 v[88:91], v[154:157], v[206:209], v[88:91]
	v_mfma_f32_16x16x32_bf16 v[76:79], v[142:145], v[228:231], v[76:79]
	v_mfma_f32_16x16x32_bf16 v[72:75], v[154:157], v[228:231], v[72:75]
	v_mfma_f32_16x16x32_bf16 v[116:119], v[158:161], v[174:177], v[116:119]
	v_mfma_f32_16x16x32_bf16 v[112:115], v[166:169], v[174:177], v[112:115]
	v_mfma_f32_16x16x32_bf16 v[100:103], v[158:161], v[194:197], v[100:103]
	v_mfma_f32_16x16x32_bf16 v[96:99], v[166:169], v[194:197], v[96:99]
	v_mfma_f32_16x16x32_bf16 v[84:87], v[158:161], v[202:205], v[84:87]
	v_mfma_f32_16x16x32_bf16 v[80:83], v[166:169], v[202:205], v[80:83]
	v_mfma_f32_16x16x32_bf16 v[68:71], v[158:161], v[224:227], v[68:71]
	v_mfma_f32_16x16x32_bf16 v[64:67], v[166:169], v[224:227], v[64:67]
	v_mfma_f32_16x16x32_bf16 v[116:119], v[162:165], v[178:181], v[116:119]
	v_mfma_f32_16x16x32_bf16 v[112:115], v[170:173], v[178:181], v[112:115]
	v_mfma_f32_16x16x32_bf16 v[100:103], v[162:165], v[198:201], v[100:103]
	v_mfma_f32_16x16x32_bf16 v[96:99], v[170:173], v[198:201], v[96:99]
	v_mfma_f32_16x16x32_bf16 v[84:87], v[162:165], v[206:209], v[84:87]
	v_mfma_f32_16x16x32_bf16 v[80:83], v[170:173], v[206:209], v[80:83]
	v_mfma_f32_16x16x32_bf16 v[68:71], v[162:165], v[228:231], v[68:71]
	v_mfma_f32_16x16x32_bf16 v[64:67], v[170:173], v[228:231], v[64:67]
	s_barrier
	s_add_i32 s28, s42, s20
	v_lshl_add_u64 v[182:183], s[40:41], 0, v[184:185]
	s_mov_b32 m0, s28
	ds_read_b128 v[174:177], v149 offset:16384
	ds_read_b128 v[178:181], v149 offset:17408
	ds_read_b128 v[194:197], v149 offset:18432
	ds_read_b128 v[198:201], v149 offset:19456
	ds_read_b128 v[202:205], v149 offset:20480
	ds_read_b128 v[206:209], v149 offset:21504
	ds_read_b128 v[224:227], v149 offset:22528
	ds_read_b128 v[228:231], v149 offset:23552
	global_load_lds_dwordx4 v[182:183], off
	s_add_i32 m0, s28, 0x2000
	s_add_u32 s28, s40, 0x40000
	v_lshl_add_u64 v[210:211], s[40:41], 0, v[128:129]
	s_addc_u32 s29, s41, 0
	s_add_i32 s42, s43, s20
	global_load_lds_dwordx4 v[210:211], off
	v_lshl_add_u64 v[216:217], s[28:29], 0, v[184:185]
	s_mov_b32 m0, s42
	v_lshl_add_u64 v[218:219], s[44:45], 0, v[130:131]
	global_load_lds_dwordx4 v[216:217], off
	v_lshl_add_u64 v[216:217], s[28:29], 0, v[128:129]
	s_add_i32 m0, s42, 0x2000
	s_nop 0
	global_load_lds_dwordx4 v[216:217], off
	v_lshl_add_u64 v[216:217], s[44:45], 0, v[132:133]
	s_mov_b32 m0, s21
	s_nop 0
	global_load_lds_dwordx4 v[216:217], off
	s_mov_b32 m0, s26
	s_nop 0
	global_load_lds_dwordx4 v[218:219], off
	s_waitcnt vmcnt(8)
	s_waitcnt lgkmcnt(0)
	s_barrier
	s_waitcnt lgkmcnt(0)
	v_mfma_f32_16x16x32_bf16 v[60:63], v[138:141], v[174:177], v[60:63]
	v_mfma_f32_16x16x32_bf16 v[56:59], v[150:153], v[174:177], v[56:59]
	v_mfma_f32_16x16x32_bf16 v[44:47], v[138:141], v[194:197], v[44:47]
	v_mfma_f32_16x16x32_bf16 v[40:43], v[150:153], v[194:197], v[40:43]
	v_mfma_f32_16x16x32_bf16 v[28:31], v[138:141], v[202:205], v[28:31]
	v_mfma_f32_16x16x32_bf16 v[24:27], v[150:153], v[202:205], v[24:27]
	v_mfma_f32_16x16x32_bf16 v[12:15], v[138:141], v[224:227], v[12:15]
	v_mfma_f32_16x16x32_bf16 v[8:11], v[150:153], v[224:227], v[8:11]
	v_mfma_f32_16x16x32_bf16 v[60:63], v[142:145], v[178:181], v[60:63]
	v_mfma_f32_16x16x32_bf16 v[56:59], v[154:157], v[178:181], v[56:59]
	v_mfma_f32_16x16x32_bf16 v[44:47], v[142:145], v[198:201], v[44:47]
	v_mfma_f32_16x16x32_bf16 v[40:43], v[154:157], v[198:201], v[40:43]
	v_mfma_f32_16x16x32_bf16 v[28:31], v[142:145], v[206:209], v[28:31]
	v_mfma_f32_16x16x32_bf16 v[24:27], v[154:157], v[206:209], v[24:27]
	v_mfma_f32_16x16x32_bf16 v[12:15], v[142:145], v[228:231], v[12:15]
	v_mfma_f32_16x16x32_bf16 v[8:11], v[154:157], v[228:231], v[8:11]
	v_mfma_f32_16x16x32_bf16 v[52:55], v[158:161], v[174:177], v[52:55]
	v_mfma_f32_16x16x32_bf16 v[48:51], v[166:169], v[174:177], v[48:51]
	v_mfma_f32_16x16x32_bf16 v[36:39], v[158:161], v[194:197], v[36:39]
	v_mfma_f32_16x16x32_bf16 v[32:35], v[166:169], v[194:197], v[32:35]
	v_mfma_f32_16x16x32_bf16 v[20:23], v[158:161], v[202:205], v[20:23]
	v_mfma_f32_16x16x32_bf16 v[16:19], v[166:169], v[202:205], v[16:19]
	v_mfma_f32_16x16x32_bf16 v[4:7], v[158:161], v[224:227], v[4:7]
	v_mfma_f32_16x16x32_bf16 v[0:3], v[166:169], v[224:227], v[0:3]
	v_mfma_f32_16x16x32_bf16 v[52:55], v[162:165], v[178:181], v[52:55]
	v_mfma_f32_16x16x32_bf16 v[48:51], v[170:173], v[178:181], v[48:51]
	v_mfma_f32_16x16x32_bf16 v[36:39], v[162:165], v[198:201], v[36:39]
	v_mfma_f32_16x16x32_bf16 v[32:35], v[170:173], v[198:201], v[32:35]
	v_mfma_f32_16x16x32_bf16 v[20:23], v[162:165], v[206:209], v[20:23]
	v_mfma_f32_16x16x32_bf16 v[16:19], v[170:173], v[206:209], v[16:19]
	v_mfma_f32_16x16x32_bf16 v[4:7], v[162:165], v[228:231], v[4:7]
	v_mfma_f32_16x16x32_bf16 v[0:3], v[170:173], v[228:231], v[0:3]
	s_barrier
	s_add_i32 s42, 0, 0x18000
	s_add_i32 s43, 0, 0x1c000
	v_add_u32_e32 v154, s42, v147
	v_add_u32_e32 v170, s43, v147
	ds_read_b128 v[138:141], v154
	ds_read_b128 v[142:145], v154 offset:1024
	ds_read_b128 v[150:153], v154 offset:2048
	ds_read_b128 v[154:157], v154 offset:3072
	ds_read_b128 v[158:161], v170
	ds_read_b128 v[162:165], v170 offset:1024
	ds_read_b128 v[166:169], v170 offset:2048
	ds_read_b128 v[170:173], v170 offset:3072
	s_add_u32 s28, s44, 0x40000
	s_addc_u32 s29, s45, 0
	s_mov_b32 m0, s27
	v_lshl_add_u64 v[232:233], s[28:29], 0, v[132:133]
	ds_read_b128 v[174:177], v149 offset:32768
	ds_read_b128 v[178:181], v149 offset:33792
	ds_read_b128 v[194:197], v149 offset:34816
	ds_read_b128 v[198:201], v149 offset:35840
	ds_read_b128 v[202:205], v149 offset:36864
	ds_read_b128 v[206:209], v149 offset:37888
	ds_read_b128 v[224:227], v149 offset:38912
	ds_read_b128 v[228:231], v149 offset:39936
	global_load_lds_dwordx4 v[232:233], off
	v_lshl_add_u64 v[232:233], s[28:29], 0, v[130:131]
	s_mov_b32 m0, s46
	s_nop 0
	global_load_lds_dwordx4 v[232:233], off
	s_waitcnt vmcnt(8)
	s_waitcnt lgkmcnt(0)
	s_barrier
	s_waitcnt lgkmcnt(0)
	v_mfma_f32_16x16x32_bf16 v[124:127], v[138:141], v[174:177], v[124:127]
	v_mfma_f32_16x16x32_bf16 v[120:123], v[150:153], v[174:177], v[120:123]
	v_mfma_f32_16x16x32_bf16 v[108:111], v[138:141], v[194:197], v[108:111]
	v_mfma_f32_16x16x32_bf16 v[104:107], v[150:153], v[194:197], v[104:107]
	v_mfma_f32_16x16x32_bf16 v[92:95], v[138:141], v[202:205], v[92:95]
	v_mfma_f32_16x16x32_bf16 v[88:91], v[150:153], v[202:205], v[88:91]
	v_mfma_f32_16x16x32_bf16 v[76:79], v[138:141], v[224:227], v[76:79]
	v_mfma_f32_16x16x32_bf16 v[72:75], v[150:153], v[224:227], v[72:75]
	v_mfma_f32_16x16x32_bf16 v[124:127], v[142:145], v[178:181], v[124:127]
	v_mfma_f32_16x16x32_bf16 v[120:123], v[154:157], v[178:181], v[120:123]
	v_mfma_f32_16x16x32_bf16 v[108:111], v[142:145], v[198:201], v[108:111]
	v_mfma_f32_16x16x32_bf16 v[104:107], v[154:157], v[198:201], v[104:107]
	v_mfma_f32_16x16x32_bf16 v[92:95], v[142:145], v[206:209], v[92:95]
	v_mfma_f32_16x16x32_bf16 v[88:91], v[154:157], v[206:209], v[88:91]
	v_mfma_f32_16x16x32_bf16 v[76:79], v[142:145], v[228:231], v[76:79]
	v_mfma_f32_16x16x32_bf16 v[72:75], v[154:157], v[228:231], v[72:75]
	v_mfma_f32_16x16x32_bf16 v[116:119], v[158:161], v[174:177], v[116:119]
	v_mfma_f32_16x16x32_bf16 v[112:115], v[166:169], v[174:177], v[112:115]
	v_mfma_f32_16x16x32_bf16 v[100:103], v[158:161], v[194:197], v[100:103]
	v_mfma_f32_16x16x32_bf16 v[96:99], v[166:169], v[194:197], v[96:99]
	v_mfma_f32_16x16x32_bf16 v[84:87], v[158:161], v[202:205], v[84:87]
	v_mfma_f32_16x16x32_bf16 v[80:83], v[166:169], v[202:205], v[80:83]
	v_mfma_f32_16x16x32_bf16 v[68:71], v[158:161], v[224:227], v[68:71]
	v_mfma_f32_16x16x32_bf16 v[64:67], v[166:169], v[224:227], v[64:67]
	v_mfma_f32_16x16x32_bf16 v[116:119], v[162:165], v[178:181], v[116:119]
	v_mfma_f32_16x16x32_bf16 v[112:115], v[170:173], v[178:181], v[112:115]
	v_mfma_f32_16x16x32_bf16 v[100:103], v[162:165], v[198:201], v[100:103]
	v_mfma_f32_16x16x32_bf16 v[96:99], v[170:173], v[198:201], v[96:99]
	v_mfma_f32_16x16x32_bf16 v[84:87], v[162:165], v[206:209], v[84:87]
	v_mfma_f32_16x16x32_bf16 v[80:83], v[170:173], v[206:209], v[80:83]
	v_mfma_f32_16x16x32_bf16 v[68:71], v[162:165], v[228:231], v[68:71]
	v_mfma_f32_16x16x32_bf16 v[64:67], v[170:173], v[228:231], v[64:67]
	s_barrier
	s_add_i32 s28, s42, s20
	v_lshl_add_u64 v[182:183], v[182:183], 0, s[68:69]
	s_mov_b32 m0, s28
	ds_read_b128 v[174:177], v149 offset:49152
	ds_read_b128 v[178:181], v149 offset:50176
	ds_read_b128 v[194:197], v149 offset:51200
	ds_read_b128 v[198:201], v149 offset:52224
	ds_read_b128 v[202:205], v149 offset:53248
	ds_read_b128 v[206:209], v149 offset:54272
	ds_read_b128 v[224:227], v149 offset:55296
	ds_read_b128 v[228:231], v149 offset:56320
	global_load_lds_dwordx4 v[182:183], off
	s_add_i32 m0, s28, 0x2000
	s_add_u32 s28, s40, 0x40080
	v_lshl_add_u64 v[182:183], v[210:211], 0, s[68:69]
	s_addc_u32 s29, s41, 0
	s_add_i32 s40, s43, s20
	global_load_lds_dwordx4 v[182:183], off
	v_lshl_add_u64 v[182:183], s[28:29], 0, v[184:185]
	s_mov_b32 m0, s40
	s_nop 0
	global_load_lds_dwordx4 v[182:183], off
	v_lshl_add_u64 v[182:183], s[28:29], 0, v[128:129]
	s_add_i32 m0, s40, 0x2000
	s_nop 0
	global_load_lds_dwordx4 v[182:183], off
	v_lshl_add_u64 v[182:183], v[216:217], 0, s[68:69]
	s_mov_b32 m0, s47
	s_nop 0
	global_load_lds_dwordx4 v[182:183], off
	v_lshl_add_u64 v[182:183], v[218:219], 0, s[68:69]
	s_mov_b32 m0, s50
	s_nop 0
	global_load_lds_dwordx4 v[182:183], off
	s_waitcnt vmcnt(8)
	s_waitcnt lgkmcnt(0)
	s_barrier
	s_waitcnt lgkmcnt(0)
	v_mfma_f32_16x16x32_bf16 v[60:63], v[138:141], v[174:177], v[60:63]
	v_mfma_f32_16x16x32_bf16 v[56:59], v[150:153], v[174:177], v[56:59]
	v_mfma_f32_16x16x32_bf16 v[44:47], v[138:141], v[194:197], v[44:47]
	v_mfma_f32_16x16x32_bf16 v[40:43], v[150:153], v[194:197], v[40:43]
	v_mfma_f32_16x16x32_bf16 v[28:31], v[138:141], v[202:205], v[28:31]
	v_mfma_f32_16x16x32_bf16 v[24:27], v[150:153], v[202:205], v[24:27]
	v_mfma_f32_16x16x32_bf16 v[12:15], v[138:141], v[224:227], v[12:15]
	v_mfma_f32_16x16x32_bf16 v[8:11], v[150:153], v[224:227], v[8:11]
	v_mfma_f32_16x16x32_bf16 v[60:63], v[142:145], v[178:181], v[60:63]
	v_mfma_f32_16x16x32_bf16 v[56:59], v[154:157], v[178:181], v[56:59]
	v_mfma_f32_16x16x32_bf16 v[44:47], v[142:145], v[198:201], v[44:47]
	v_mfma_f32_16x16x32_bf16 v[40:43], v[154:157], v[198:201], v[40:43]
	v_mfma_f32_16x16x32_bf16 v[28:31], v[142:145], v[206:209], v[28:31]
	v_mfma_f32_16x16x32_bf16 v[24:27], v[154:157], v[206:209], v[24:27]
	v_mfma_f32_16x16x32_bf16 v[12:15], v[142:145], v[228:231], v[12:15]
	v_mfma_f32_16x16x32_bf16 v[8:11], v[154:157], v[228:231], v[8:11]
	v_mfma_f32_16x16x32_bf16 v[52:55], v[158:161], v[174:177], v[52:55]
	v_mfma_f32_16x16x32_bf16 v[48:51], v[166:169], v[174:177], v[48:51]
	v_mfma_f32_16x16x32_bf16 v[36:39], v[158:161], v[194:197], v[36:39]
	v_mfma_f32_16x16x32_bf16 v[32:35], v[166:169], v[194:197], v[32:35]
	v_mfma_f32_16x16x32_bf16 v[20:23], v[158:161], v[202:205], v[20:23]
	v_mfma_f32_16x16x32_bf16 v[16:19], v[166:169], v[202:205], v[16:19]
	v_mfma_f32_16x16x32_bf16 v[4:7], v[158:161], v[224:227], v[4:7]
	v_mfma_f32_16x16x32_bf16 v[0:3], v[166:169], v[224:227], v[0:3]
	v_mfma_f32_16x16x32_bf16 v[52:55], v[162:165], v[178:181], v[52:55]
	v_mfma_f32_16x16x32_bf16 v[48:51], v[170:173], v[178:181], v[48:51]
	v_mfma_f32_16x16x32_bf16 v[36:39], v[162:165], v[198:201], v[36:39]
	v_mfma_f32_16x16x32_bf16 v[32:35], v[170:173], v[198:201], v[32:35]
	v_mfma_f32_16x16x32_bf16 v[20:23], v[162:165], v[206:209], v[20:23]
	v_mfma_f32_16x16x32_bf16 v[16:19], v[170:173], v[206:209], v[16:19]
	v_mfma_f32_16x16x32_bf16 v[4:7], v[162:165], v[228:231], v[4:7]
	v_mfma_f32_16x16x32_bf16 v[0:3], v[170:173], v[228:231], v[0:3]
	s_barrier
	s_add_i32 s60, s60, 2
	s_add_u32 s30, s30, 0x100
	s_addc_u32 s31, s31, 0
	s_add_u32 s58, s58, 0x100
	s_addc_u32 s59, s59, 0
	s_cmp_gt_u32 s60, 13
	s_cbranch_scc0 .LBB0_842
	s_and_b64 vcc, exec, s[6:7]
	s_cbranch_vccz .LBB0_845
	s_barrier

.LBB0_859:
	s_add_u32 s42, s40, s50
	s_addc_u32 s43, s41, 0
	s_add_u32 s48, s42, 0x100
	s_addc_u32 s49, s43, 0
	s_and_b64 s[28:29], s[46:47], exec
	s_cselect_b32 s53, s11, s49
	s_cselect_b32 s52, s13, s48
	s_add_u32 s28, s6, s50
	s_addc_u32 s29, s7, 0
	s_add_u32 s48, s28, 0x100
	s_addc_u32 s49, s29, 0
	s_add_i32 s76, 0, 0x10000
	s_and_b64 s[28:29], s[46:47], exec
	s_cselect_b32 s59, s93, s49
	s_cselect_b32 s58, s94, s48
	s_add_i32 s29, 0, 0x14000
	s_add_u32 s62, s42, 0x40080
	s_addc_u32 s63, s43, 0
	s_add_i32 s85, s76, s20
	s_add_i32 m0, s21, 0xc000
	s_add_i32 s90, s21, 0xe000
	s_add_i32 s42, s85, 0x2000
	v_add_u32_e32 v153, s76, v150
	s_add_u32 s60, s58, 0x40000
	ds_read_b128 v[154:157], v153
	ds_read_b128 v[158:161], v153 offset:1024
	ds_read_b128 v[162:165], v153 offset:2048
	ds_read_b128 v[166:169], v153 offset:3072
	v_add_u32_e32 v153, s29, v150
	s_addc_u32 s61, s59, 0
	s_add_i32 s49, s29, s20
	ds_read_b128 v[170:173], v153
	ds_read_b128 v[174:177], v153 offset:1024
	ds_read_b128 v[178:181], v153 offset:2048
	ds_read_b128 v[194:197], v153 offset:3072
	s_add_i32 s43, s49, 0x2000
	s_add_i32 s48, 0, 0x18000
	s_add_i32 s28, 0, 0x1c000
	s_add_u32 s50, s52, 0x40000
	s_addc_u32 s51, s53, 0
	s_add_i32 vcc_lo, s48, s20
	s_add_i32 s95, vcc_lo, 0x2000
	s_add_u32 s46, s58, 0x40080
	s_addc_u32 s47, s59, 0
	s_add_i32 s76, s28, s20
	s_add_i32 s29, s76, 0x2000
	v_lshl_add_u64 v[182:183], s[62:63], 0, v[132:133]
	ds_read_b128 v[198:201], v152
	ds_read_b128 v[202:205], v152 offset:1024
	ds_read_b128 v[206:209], v152 offset:2048
	ds_read_b128 v[224:227], v152 offset:3072
	ds_read_b128 v[228:231], v152 offset:4096
	ds_read_b128 v[232:235], v152 offset:5120
	ds_read_b128 v[236:239], v152 offset:6144
	ds_read_b128 v[240:243], v152 offset:7168
	global_load_lds_dwordx4 v[182:183], off
	v_lshl_add_u64 v[182:183], s[62:63], 0, v[130:131]
	s_mov_b32 m0, s90
	s_nop 0
	global_load_lds_dwordx4 v[182:183], off
	s_waitcnt vmcnt(8)
	s_waitcnt lgkmcnt(0)
	s_barrier
	s_waitcnt lgkmcnt(0)
	v_mfma_f32_16x16x32_bf16 v[124:127], v[154:157], v[198:201], v[124:127]
	v_mfma_f32_16x16x32_bf16 v[120:123], v[162:165], v[198:201], v[120:123]
	v_mfma_f32_16x16x32_bf16 v[116:119], v[154:157], v[206:209], v[116:119]
	v_mfma_f32_16x16x32_bf16 v[112:115], v[162:165], v[206:209], v[112:115]
	v_mfma_f32_16x16x32_bf16 v[108:111], v[154:157], v[228:231], v[108:111]
	v_mfma_f32_16x16x32_bf16 v[104:107], v[162:165], v[228:231], v[104:107]
	v_mfma_f32_16x16x32_bf16 v[96:99], v[154:157], v[236:239], v[96:99]
	v_mfma_f32_16x16x32_bf16 v[88:91], v[162:165], v[236:239], v[88:91]
	v_mfma_f32_16x16x32_bf16 v[124:127], v[158:161], v[202:205], v[124:127]
	v_mfma_f32_16x16x32_bf16 v[120:123], v[166:169], v[202:205], v[120:123]
	v_mfma_f32_16x16x32_bf16 v[116:119], v[158:161], v[224:227], v[116:119]
	v_mfma_f32_16x16x32_bf16 v[112:115], v[166:169], v[224:227], v[112:115]
	v_mfma_f32_16x16x32_bf16 v[108:111], v[158:161], v[232:235], v[108:111]
	v_mfma_f32_16x16x32_bf16 v[104:107], v[166:169], v[232:235], v[104:107]
	v_mfma_f32_16x16x32_bf16 v[96:99], v[158:161], v[240:243], v[96:99]
	v_mfma_f32_16x16x32_bf16 v[88:91], v[166:169], v[240:243], v[88:91]
	v_mfma_f32_16x16x32_bf16 v[100:103], v[170:173], v[198:201], v[100:103]
	v_mfma_f32_16x16x32_bf16 v[92:95], v[178:181], v[198:201], v[92:95]
	v_mfma_f32_16x16x32_bf16 v[84:87], v[170:173], v[206:209], v[84:87]
	v_mfma_f32_16x16x32_bf16 v[80:83], v[178:181], v[206:209], v[80:83]
	v_mfma_f32_16x16x32_bf16 v[76:79], v[170:173], v[228:231], v[76:79]
	v_mfma_f32_16x16x32_bf16 v[72:75], v[178:181], v[228:231], v[72:75]
	v_mfma_f32_16x16x32_bf16 v[68:71], v[170:173], v[236:239], v[68:71]
	v_mfma_f32_16x16x32_bf16 v[64:67], v[178:181], v[236:239], v[64:67]
	v_mfma_f32_16x16x32_bf16 v[100:103], v[174:177], v[202:205], v[100:103]
	v_mfma_f32_16x16x32_bf16 v[92:95], v[194:197], v[202:205], v[92:95]
	v_mfma_f32_16x16x32_bf16 v[84:87], v[174:177], v[224:227], v[84:87]
	v_mfma_f32_16x16x32_bf16 v[80:83], v[194:197], v[224:227], v[80:83]
	v_mfma_f32_16x16x32_bf16 v[76:79], v[174:177], v[232:235], v[76:79]
	v_mfma_f32_16x16x32_bf16 v[72:75], v[194:197], v[232:235], v[72:75]
	v_mfma_f32_16x16x32_bf16 v[68:71], v[174:177], v[240:243], v[68:71]
	v_mfma_f32_16x16x32_bf16 v[64:67], v[194:197], v[240:243], v[64:67]
	s_barrier
	s_mov_b32 m0, s85
	v_lshl_add_u64 v[182:183], s[58:59], 0, v[184:185]
	ds_read_b128 v[198:201], v152 offset:16384
	ds_read_b128 v[202:205], v152 offset:17408
	ds_read_b128 v[206:209], v152 offset:18432
	ds_read_b128 v[224:227], v152 offset:19456
	ds_read_b128 v[228:231], v152 offset:20480
	ds_read_b128 v[232:235], v152 offset:21504
	ds_read_b128 v[236:239], v152 offset:22528
	ds_read_b128 v[240:243], v152 offset:23552
	global_load_lds_dwordx4 v[182:183], off
	v_lshl_add_u64 v[210:211], s[58:59], 0, v[128:129]
	s_mov_b32 m0, s42
	v_lshl_add_u64 v[216:217], s[60:61], 0, v[184:185]
	global_load_lds_dwordx4 v[210:211], off
	s_mov_b32 m0, s49
	v_lshl_add_u64 v[218:219], s[52:53], 0, v[130:131]
	global_load_lds_dwordx4 v[216:217], off
	v_lshl_add_u64 v[216:217], s[60:61], 0, v[128:129]
	s_mov_b32 m0, s43
	s_nop 0
	global_load_lds_dwordx4 v[216:217], off
	v_lshl_add_u64 v[216:217], s[52:53], 0, v[132:133]
	s_mov_b32 m0, s21
	s_nop 0
	global_load_lds_dwordx4 v[216:217], off
	s_mov_b32 m0, s26
	s_nop 0
	global_load_lds_dwordx4 v[218:219], off
	s_waitcnt vmcnt(8)
	s_waitcnt lgkmcnt(0)
	s_barrier
	s_waitcnt lgkmcnt(0)
	v_mfma_f32_16x16x32_bf16 v[60:63], v[154:157], v[198:201], v[60:63]
	v_mfma_f32_16x16x32_bf16 v[56:59], v[162:165], v[198:201], v[56:59]
	v_mfma_f32_16x16x32_bf16 v[52:55], v[154:157], v[206:209], v[52:55]
	v_mfma_f32_16x16x32_bf16 v[48:51], v[162:165], v[206:209], v[48:51]
	v_mfma_f32_16x16x32_bf16 v[44:47], v[154:157], v[228:231], v[44:47]
	v_mfma_f32_16x16x32_bf16 v[40:43], v[162:165], v[228:231], v[40:43]
	v_mfma_f32_16x16x32_bf16 v[32:35], v[154:157], v[236:239], v[32:35]
	v_mfma_f32_16x16x32_bf16 v[24:27], v[162:165], v[236:239], v[24:27]
	v_mfma_f32_16x16x32_bf16 v[60:63], v[158:161], v[202:205], v[60:63]
	v_mfma_f32_16x16x32_bf16 v[56:59], v[166:169], v[202:205], v[56:59]
	v_mfma_f32_16x16x32_bf16 v[52:55], v[158:161], v[224:227], v[52:55]
	v_mfma_f32_16x16x32_bf16 v[48:51], v[166:169], v[224:227], v[48:51]
	v_mfma_f32_16x16x32_bf16 v[44:47], v[158:161], v[232:235], v[44:47]
	v_mfma_f32_16x16x32_bf16 v[40:43], v[166:169], v[232:235], v[40:43]
	v_mfma_f32_16x16x32_bf16 v[32:35], v[158:161], v[240:243], v[32:35]
	v_mfma_f32_16x16x32_bf16 v[24:27], v[166:169], v[240:243], v[24:27]
	v_mfma_f32_16x16x32_bf16 v[36:39], v[170:173], v[198:201], v[36:39]
	v_mfma_f32_16x16x32_bf16 v[28:31], v[178:181], v[198:201], v[28:31]
	v_mfma_f32_16x16x32_bf16 v[20:23], v[170:173], v[206:209], v[20:23]
	v_mfma_f32_16x16x32_bf16 v[16:19], v[178:181], v[206:209], v[16:19]
	v_mfma_f32_16x16x32_bf16 v[12:15], v[170:173], v[228:231], v[12:15]
	v_mfma_f32_16x16x32_bf16 v[8:11], v[178:181], v[228:231], v[8:11]
	v_mfma_f32_16x16x32_bf16 v[4:7], v[170:173], v[236:239], v[4:7]
	v_mfma_f32_16x16x32_bf16 v[0:3], v[178:181], v[236:239], v[0:3]
	v_mfma_f32_16x16x32_bf16 v[36:39], v[174:177], v[202:205], v[36:39]
	v_mfma_f32_16x16x32_bf16 v[28:31], v[194:197], v[202:205], v[28:31]
	v_mfma_f32_16x16x32_bf16 v[20:23], v[174:177], v[224:227], v[20:23]
	v_mfma_f32_16x16x32_bf16 v[16:19], v[194:197], v[224:227], v[16:19]
	v_mfma_f32_16x16x32_bf16 v[12:15], v[174:177], v[232:235], v[12:15]
	v_mfma_f32_16x16x32_bf16 v[8:11], v[194:197], v[232:235], v[8:11]
	v_mfma_f32_16x16x32_bf16 v[4:7], v[174:177], v[240:243], v[4:7]
	v_mfma_f32_16x16x32_bf16 v[0:3], v[194:197], v[240:243], v[0:3]
	s_barrier
	v_add_u32_e32 v153, s48, v150
	ds_read_b128 v[154:157], v153
	ds_read_b128 v[158:161], v153 offset:1024
	ds_read_b128 v[162:165], v153 offset:2048
	ds_read_b128 v[166:169], v153 offset:3072
	v_add_u32_e32 v153, s28, v150
	ds_read_b128 v[170:173], v153
	ds_read_b128 v[174:177], v153 offset:1024
	ds_read_b128 v[178:181], v153 offset:2048
	ds_read_b128 v[194:197], v153 offset:3072
	s_mov_b32 m0, s27
	v_lshl_add_u64 v[244:245], s[50:51], 0, v[132:133]
	ds_read_b128 v[198:201], v152 offset:32768
	ds_read_b128 v[202:205], v152 offset:33792
	ds_read_b128 v[206:209], v152 offset:34816
	ds_read_b128 v[224:227], v152 offset:35840
	ds_read_b128 v[228:231], v152 offset:36864
	ds_read_b128 v[232:235], v152 offset:37888
	ds_read_b128 v[236:239], v152 offset:38912
	ds_read_b128 v[240:243], v152 offset:39936
	global_load_lds_dwordx4 v[244:245], off
	v_lshl_add_u64 v[244:245], s[50:51], 0, v[130:131]
	s_mov_b32 m0, s79
	s_nop 0
	global_load_lds_dwordx4 v[244:245], off
	s_waitcnt vmcnt(8)
	s_waitcnt lgkmcnt(0)
	s_barrier
	s_waitcnt lgkmcnt(0)
	v_mfma_f32_16x16x32_bf16 v[124:127], v[154:157], v[198:201], v[124:127]
	v_mfma_f32_16x16x32_bf16 v[120:123], v[162:165], v[198:201], v[120:123]
	v_mfma_f32_16x16x32_bf16 v[116:119], v[154:157], v[206:209], v[116:119]
	v_mfma_f32_16x16x32_bf16 v[112:115], v[162:165], v[206:209], v[112:115]
	v_mfma_f32_16x16x32_bf16 v[108:111], v[154:157], v[228:231], v[108:111]
	v_mfma_f32_16x16x32_bf16 v[104:107], v[162:165], v[228:231], v[104:107]
	v_mfma_f32_16x16x32_bf16 v[96:99], v[154:157], v[236:239], v[96:99]
	v_mfma_f32_16x16x32_bf16 v[88:91], v[162:165], v[236:239], v[88:91]
	v_mfma_f32_16x16x32_bf16 v[124:127], v[158:161], v[202:205], v[124:127]
	v_mfma_f32_16x16x32_bf16 v[120:123], v[166:169], v[202:205], v[120:123]
	v_mfma_f32_16x16x32_bf16 v[116:119], v[158:161], v[224:227], v[116:119]
	v_mfma_f32_16x16x32_bf16 v[112:115], v[166:169], v[224:227], v[112:115]
	v_mfma_f32_16x16x32_bf16 v[108:111], v[158:161], v[232:235], v[108:111]
	v_mfma_f32_16x16x32_bf16 v[104:107], v[166:169], v[232:235], v[104:107]
	v_mfma_f32_16x16x32_bf16 v[96:99], v[158:161], v[240:243], v[96:99]
	v_mfma_f32_16x16x32_bf16 v[88:91], v[166:169], v[240:243], v[88:91]
	v_mfma_f32_16x16x32_bf16 v[100:103], v[170:173], v[198:201], v[100:103]
	v_mfma_f32_16x16x32_bf16 v[92:95], v[178:181], v[198:201], v[92:95]
	v_mfma_f32_16x16x32_bf16 v[84:87], v[170:173], v[206:209], v[84:87]
	v_mfma_f32_16x16x32_bf16 v[80:83], v[178:181], v[206:209], v[80:83]
	v_mfma_f32_16x16x32_bf16 v[76:79], v[170:173], v[228:231], v[76:79]
	v_mfma_f32_16x16x32_bf16 v[72:75], v[178:181], v[228:231], v[72:75]
	v_mfma_f32_16x16x32_bf16 v[68:71], v[170:173], v[236:239], v[68:71]
	v_mfma_f32_16x16x32_bf16 v[64:67], v[178:181], v[236:239], v[64:67]
	v_mfma_f32_16x16x32_bf16 v[100:103], v[174:177], v[202:205], v[100:103]
	v_mfma_f32_16x16x32_bf16 v[92:95], v[194:197], v[202:205], v[92:95]
	v_mfma_f32_16x16x32_bf16 v[84:87], v[174:177], v[224:227], v[84:87]
	v_mfma_f32_16x16x32_bf16 v[80:83], v[194:197], v[224:227], v[80:83]
	v_mfma_f32_16x16x32_bf16 v[76:79], v[174:177], v[232:235], v[76:79]
	v_mfma_f32_16x16x32_bf16 v[72:75], v[194:197], v[232:235], v[72:75]
	v_mfma_f32_16x16x32_bf16 v[68:71], v[174:177], v[240:243], v[68:71]
	v_mfma_f32_16x16x32_bf16 v[64:67], v[194:197], v[240:243], v[64:67]
	s_barrier
	s_mov_b32 m0, vcc_lo
	v_lshl_add_u64 v[182:183], v[182:183], 0, s[68:69]
	ds_read_b128 v[198:201], v152 offset:49152
	ds_read_b128 v[202:205], v152 offset:50176
	ds_read_b128 v[206:209], v152 offset:51200
	ds_read_b128 v[224:227], v152 offset:52224
	ds_read_b128 v[228:231], v152 offset:53248
	ds_read_b128 v[232:235], v152 offset:54272
	ds_read_b128 v[236:239], v152 offset:55296
	ds_read_b128 v[240:243], v152 offset:56320
	global_load_lds_dwordx4 v[182:183], off
	v_lshl_add_u64 v[182:183], v[210:211], 0, s[68:69]
	s_mov_b32 m0, s95
	s_nop 0
	global_load_lds_dwordx4 v[182:183], off
	v_lshl_add_u64 v[182:183], s[46:47], 0, v[184:185]
	s_mov_b32 m0, s76
	s_nop 0
	global_load_lds_dwordx4 v[182:183], off
	v_lshl_add_u64 v[182:183], s[46:47], 0, v[128:129]
	s_mov_b32 m0, s29
	s_nop 0
	global_load_lds_dwordx4 v[182:183], off
	v_lshl_add_u64 v[182:183], v[216:217], 0, s[68:69]
	s_mov_b32 m0, s88
	s_nop 0
	global_load_lds_dwordx4 v[182:183], off
	v_lshl_add_u64 v[182:183], v[218:219], 0, s[68:69]
	s_mov_b32 m0, s89
	s_nop 0
	global_load_lds_dwordx4 v[182:183], off
	s_waitcnt vmcnt(8)
	s_waitcnt lgkmcnt(0)
	s_barrier
	s_waitcnt lgkmcnt(0)
	v_mfma_f32_16x16x32_bf16 v[60:63], v[154:157], v[198:201], v[60:63]
	v_mfma_f32_16x16x32_bf16 v[56:59], v[162:165], v[198:201], v[56:59]
	v_mfma_f32_16x16x32_bf16 v[52:55], v[154:157], v[206:209], v[52:55]
	v_mfma_f32_16x16x32_bf16 v[48:51], v[162:165], v[206:209], v[48:51]
	v_mfma_f32_16x16x32_bf16 v[44:47], v[154:157], v[228:231], v[44:47]
	v_mfma_f32_16x16x32_bf16 v[40:43], v[162:165], v[228:231], v[40:43]
	v_mfma_f32_16x16x32_bf16 v[32:35], v[154:157], v[236:239], v[32:35]
	v_mfma_f32_16x16x32_bf16 v[24:27], v[162:165], v[236:239], v[24:27]
	v_mfma_f32_16x16x32_bf16 v[60:63], v[158:161], v[202:205], v[60:63]
	v_mfma_f32_16x16x32_bf16 v[56:59], v[166:169], v[202:205], v[56:59]
	v_mfma_f32_16x16x32_bf16 v[52:55], v[158:161], v[224:227], v[52:55]
	v_mfma_f32_16x16x32_bf16 v[48:51], v[166:169], v[224:227], v[48:51]
	v_mfma_f32_16x16x32_bf16 v[44:47], v[158:161], v[232:235], v[44:47]
	v_mfma_f32_16x16x32_bf16 v[40:43], v[166:169], v[232:235], v[40:43]
	v_mfma_f32_16x16x32_bf16 v[32:35], v[158:161], v[240:243], v[32:35]
	v_mfma_f32_16x16x32_bf16 v[24:27], v[166:169], v[240:243], v[24:27]
	v_mfma_f32_16x16x32_bf16 v[36:39], v[170:173], v[198:201], v[36:39]
	v_mfma_f32_16x16x32_bf16 v[28:31], v[178:181], v[198:201], v[28:31]
	v_mfma_f32_16x16x32_bf16 v[20:23], v[170:173], v[206:209], v[20:23]
	v_mfma_f32_16x16x32_bf16 v[16:19], v[178:181], v[206:209], v[16:19]
	v_mfma_f32_16x16x32_bf16 v[12:15], v[170:173], v[228:231], v[12:15]
	v_mfma_f32_16x16x32_bf16 v[8:11], v[178:181], v[228:231], v[8:11]
	v_mfma_f32_16x16x32_bf16 v[4:7], v[170:173], v[236:239], v[4:7]
	v_mfma_f32_16x16x32_bf16 v[0:3], v[178:181], v[236:239], v[0:3]
	v_mfma_f32_16x16x32_bf16 v[36:39], v[174:177], v[202:205], v[36:39]
	v_mfma_f32_16x16x32_bf16 v[28:31], v[194:197], v[202:205], v[28:31]
	v_mfma_f32_16x16x32_bf16 v[20:23], v[174:177], v[224:227], v[20:23]
	v_mfma_f32_16x16x32_bf16 v[16:19], v[194:197], v[224:227], v[16:19]
	v_mfma_f32_16x16x32_bf16 v[12:15], v[174:177], v[232:235], v[12:15]
	v_mfma_f32_16x16x32_bf16 v[8:11], v[194:197], v[232:235], v[8:11]
	v_mfma_f32_16x16x32_bf16 v[4:7], v[174:177], v[240:243], v[4:7]
	v_mfma_f32_16x16x32_bf16 v[0:3], v[194:197], v[240:243], v[0:3]
	s_barrier
	s_movk_i32 s50, 0x100
	s_andn2_b64 vcc, exec, s[44:45]
	s_mov_b64 s[46:47], -1
	s_mov_b64 s[44:45], 0
	s_cbranch_vccz .LBB0_859
	s_and_b64 vcc, exec, s[8:9]
	s_cbranch_vccz .LBB0_862
	s_barrier

.LBB0_991:
	s_add_u32 s28, s40, 0xfff80080
	s_addc_u32 s29, s41, -1
	s_add_i32 s48, 0, 0x10000
	s_cmp_eq_u32 s79, 28
	s_cselect_b32 s45, s11, s29
	s_cselect_b32 s44, s13, s28
	s_cselect_b32 s43, s60, s63
	s_cselect_b32 s42, s61, s62
	s_add_i32 s49, 0, 0x14000
	s_waitcnt vmcnt(0)
	v_add_u32_e32 v60, s48, v169
	v_add_u32_e32 v166, s49, v169
	ds_read_b128 v[40:43], v60
	ds_read_b128 v[44:47], v60 offset:1024
	ds_read_b128 v[56:59], v60 offset:2048
	ds_read_b128 v[60:63], v60 offset:3072
	ds_read_b128 v[144:147], v166
	ds_read_b128 v[148:151], v166 offset:1024
	ds_read_b128 v[162:165], v166 offset:2048
	ds_read_b128 v[172:175], v166 offset:3072
	v_lshl_add_u64 v[166:167], s[40:41], 0, v[158:159]
	s_add_i32 m0, s26, 0xc000
	ds_read_b128 v[176:179], v171
	ds_read_b128 v[180:183], v171 offset:1024
	ds_read_b128 v[194:197], v171 offset:2048
	ds_read_b128 v[198:201], v171 offset:3072
	ds_read_b128 v[202:205], v171 offset:4096
	ds_read_b128 v[206:209], v171 offset:5120
	ds_read_b128 v[224:227], v171 offset:6144
	ds_read_b128 v[228:231], v171 offset:7168
	global_load_lds_dwordx4 v[166:167], off
	v_lshl_add_u64 v[166:167], s[40:41], 0, v[160:161]
	s_add_i32 m0, s26, 0xe000
	s_nop 0
	global_load_lds_dwordx4 v[166:167], off
	s_waitcnt vmcnt(8)
	s_waitcnt lgkmcnt(0)
	s_barrier
	s_waitcnt lgkmcnt(0)
	v_mfma_f32_16x16x32_bf16 v[140:143], v[40:43], v[176:179], v[140:143]
	v_mfma_f32_16x16x32_bf16 v[136:139], v[56:59], v[176:179], v[136:139]
	v_mfma_f32_16x16x32_bf16 v[124:127], v[40:43], v[194:197], v[124:127]
	v_mfma_f32_16x16x32_bf16 v[120:123], v[56:59], v[194:197], v[120:123]
	v_mfma_f32_16x16x32_bf16 v[108:111], v[40:43], v[202:205], v[108:111]
	v_mfma_f32_16x16x32_bf16 v[104:107], v[56:59], v[202:205], v[104:107]
	v_mfma_f32_16x16x32_bf16 v[92:95], v[40:43], v[224:227], v[92:95]
	v_mfma_f32_16x16x32_bf16 v[88:91], v[56:59], v[224:227], v[88:91]
	v_mfma_f32_16x16x32_bf16 v[140:143], v[44:47], v[180:183], v[140:143]
	v_mfma_f32_16x16x32_bf16 v[136:139], v[60:63], v[180:183], v[136:139]
	v_mfma_f32_16x16x32_bf16 v[124:127], v[44:47], v[198:201], v[124:127]
	v_mfma_f32_16x16x32_bf16 v[120:123], v[60:63], v[198:201], v[120:123]
	v_mfma_f32_16x16x32_bf16 v[108:111], v[44:47], v[206:209], v[108:111]
	v_mfma_f32_16x16x32_bf16 v[104:107], v[60:63], v[206:209], v[104:107]
	v_mfma_f32_16x16x32_bf16 v[92:95], v[44:47], v[228:231], v[92:95]
	v_mfma_f32_16x16x32_bf16 v[88:91], v[60:63], v[228:231], v[88:91]
	v_mfma_f32_16x16x32_bf16 v[132:135], v[144:147], v[176:179], v[132:135]
	v_mfma_f32_16x16x32_bf16 v[128:131], v[162:165], v[176:179], v[128:131]
	v_mfma_f32_16x16x32_bf16 v[116:119], v[144:147], v[194:197], v[116:119]
	v_mfma_f32_16x16x32_bf16 v[112:115], v[162:165], v[194:197], v[112:115]
	v_mfma_f32_16x16x32_bf16 v[100:103], v[144:147], v[202:205], v[100:103]
	v_mfma_f32_16x16x32_bf16 v[96:99], v[162:165], v[202:205], v[96:99]
	v_mfma_f32_16x16x32_bf16 v[84:87], v[144:147], v[224:227], v[84:87]
	v_mfma_f32_16x16x32_bf16 v[80:83], v[162:165], v[224:227], v[80:83]
	v_mfma_f32_16x16x32_bf16 v[132:135], v[148:151], v[180:183], v[132:135]
	v_mfma_f32_16x16x32_bf16 v[128:131], v[172:175], v[180:183], v[128:131]
	v_mfma_f32_16x16x32_bf16 v[116:119], v[148:151], v[198:201], v[116:119]
	v_mfma_f32_16x16x32_bf16 v[112:115], v[172:175], v[198:201], v[112:115]
	v_mfma_f32_16x16x32_bf16 v[100:103], v[148:151], v[206:209], v[100:103]
	v_mfma_f32_16x16x32_bf16 v[96:99], v[172:175], v[206:209], v[96:99]
	v_mfma_f32_16x16x32_bf16 v[84:87], v[148:151], v[228:231], v[84:87]
	v_mfma_f32_16x16x32_bf16 v[80:83], v[172:175], v[228:231], v[80:83]
	s_barrier
	s_add_i32 s28, s48, s46
	v_lshl_add_u64 v[166:167], s[42:43], 0, v[184:185]
	s_mov_b32 m0, s28
	ds_read_b128 v[176:179], v171 offset:16384
	ds_read_b128 v[180:183], v171 offset:17408
	ds_read_b128 v[194:197], v171 offset:18432
	ds_read_b128 v[198:201], v171 offset:19456
	ds_read_b128 v[202:205], v171 offset:20480
	ds_read_b128 v[206:209], v171 offset:21504
	ds_read_b128 v[224:227], v171 offset:22528
	ds_read_b128 v[228:231], v171 offset:23552
	global_load_lds_dwordx4 v[166:167], off
	s_add_i32 m0, s28, 0x2000
	s_add_u32 s28, s42, 0x80000
	v_lshl_add_u64 v[210:211], s[42:43], 0, v[152:153]
	s_addc_u32 s29, s43, 0
	s_add_i32 s48, s49, s46
	global_load_lds_dwordx4 v[210:211], off
	v_lshl_add_u64 v[216:217], s[28:29], 0, v[184:185]
	s_mov_b32 m0, s48
	v_lshl_add_u64 v[218:219], s[44:45], 0, v[154:155]
	global_load_lds_dwordx4 v[216:217], off
	v_lshl_add_u64 v[216:217], s[28:29], 0, v[152:153]
	s_add_i32 m0, s48, 0x2000
	s_nop 0
	global_load_lds_dwordx4 v[216:217], off
	v_lshl_add_u64 v[216:217], s[44:45], 0, v[156:157]
	s_mov_b32 m0, s26
	s_nop 0
	global_load_lds_dwordx4 v[216:217], off
	s_mov_b32 m0, s27
	s_nop 0
	global_load_lds_dwordx4 v[218:219], off
	s_waitcnt vmcnt(8)
	s_waitcnt lgkmcnt(0)
	s_barrier
	s_waitcnt lgkmcnt(0)
	v_mfma_f32_16x16x32_bf16 v[76:79], v[40:43], v[176:179], v[76:79]
	v_mfma_f32_16x16x32_bf16 v[72:75], v[56:59], v[176:179], v[72:75]
	v_mfma_f32_16x16x32_bf16 v[52:55], v[40:43], v[194:197], v[52:55]
	v_mfma_f32_16x16x32_bf16 v[48:51], v[56:59], v[194:197], v[48:51]
	v_mfma_f32_16x16x32_bf16 v[28:31], v[40:43], v[202:205], v[28:31]
	v_mfma_f32_16x16x32_bf16 v[24:27], v[56:59], v[202:205], v[24:27]
	v_mfma_f32_16x16x32_bf16 v[12:15], v[40:43], v[224:227], v[12:15]
	v_mfma_f32_16x16x32_bf16 v[8:11], v[56:59], v[224:227], v[8:11]
	v_mfma_f32_16x16x32_bf16 v[76:79], v[44:47], v[180:183], v[76:79]
	v_mfma_f32_16x16x32_bf16 v[72:75], v[60:63], v[180:183], v[72:75]
	v_mfma_f32_16x16x32_bf16 v[52:55], v[44:47], v[198:201], v[52:55]
	v_mfma_f32_16x16x32_bf16 v[48:51], v[60:63], v[198:201], v[48:51]
	v_mfma_f32_16x16x32_bf16 v[28:31], v[44:47], v[206:209], v[28:31]
	v_mfma_f32_16x16x32_bf16 v[24:27], v[60:63], v[206:209], v[24:27]
	v_mfma_f32_16x16x32_bf16 v[12:15], v[44:47], v[228:231], v[12:15]
	v_mfma_f32_16x16x32_bf16 v[8:11], v[60:63], v[228:231], v[8:11]
	v_mfma_f32_16x16x32_bf16 v[36:39], v[144:147], v[194:197], v[36:39]
	v_mfma_f32_16x16x32_bf16 v[32:35], v[162:165], v[194:197], v[32:35]
	v_mfma_f32_16x16x32_bf16 v[20:23], v[144:147], v[202:205], v[20:23]
	v_mfma_f32_16x16x32_bf16 v[16:19], v[162:165], v[202:205], v[16:19]
	v_mfma_f32_16x16x32_bf16 v[4:7], v[144:147], v[224:227], v[4:7]
	v_mfma_f32_16x16x32_bf16 v[0:3], v[162:165], v[224:227], v[0:3]
	v_mfma_f32_16x16x32_bf16 v[40:43], v[144:147], v[176:179], v[68:71]
	v_mfma_f32_16x16x32_bf16 v[44:47], v[162:165], v[176:179], v[64:67]
	v_mfma_f32_16x16x32_bf16 v[36:39], v[148:151], v[198:201], v[36:39]
	v_mfma_f32_16x16x32_bf16 v[32:35], v[172:175], v[198:201], v[32:35]
	v_mfma_f32_16x16x32_bf16 v[20:23], v[148:151], v[206:209], v[20:23]
	v_mfma_f32_16x16x32_bf16 v[16:19], v[172:175], v[206:209], v[16:19]
	v_mfma_f32_16x16x32_bf16 v[4:7], v[148:151], v[228:231], v[4:7]
	v_mfma_f32_16x16x32_bf16 v[0:3], v[172:175], v[228:231], v[0:3]
	v_mfma_f32_16x16x32_bf16 v[40:43], v[148:151], v[180:183], v[40:43]
	v_mfma_f32_16x16x32_bf16 v[44:47], v[172:175], v[180:183], v[44:47]
	s_barrier
	s_add_i32 s48, 0, 0x18000
	s_add_i32 s49, 0, 0x1c000
	v_add_u32_e32 v68, s48, v169
	v_add_u32_e32 v172, s49, v169
	ds_read_b128 v[56:59], v68
	ds_read_b128 v[60:63], v68 offset:1024
	ds_read_b128 v[64:67], v68 offset:2048
	ds_read_b128 v[68:71], v68 offset:3072
	ds_read_b128 v[144:147], v172
	ds_read_b128 v[148:151], v172 offset:1024
	ds_read_b128 v[162:165], v172 offset:2048
	ds_read_b128 v[172:175], v172 offset:3072
	s_add_u32 s28, s44, 0x80000
	s_addc_u32 s29, s45, 0
	s_mov_b32 m0, s47
	v_lshl_add_u64 v[232:233], s[28:29], 0, v[156:157]
	ds_read_b128 v[176:179], v171 offset:32768
	ds_read_b128 v[180:183], v171 offset:33792
	ds_read_b128 v[194:197], v171 offset:34816
	ds_read_b128 v[198:201], v171 offset:35840
	ds_read_b128 v[202:205], v171 offset:36864
	ds_read_b128 v[206:209], v171 offset:37888
	ds_read_b128 v[224:227], v171 offset:38912
	ds_read_b128 v[228:231], v171 offset:39936
	global_load_lds_dwordx4 v[232:233], off
	v_lshl_add_u64 v[232:233], s[28:29], 0, v[154:155]
	s_mov_b32 m0, s50
	s_nop 0
	global_load_lds_dwordx4 v[232:233], off
	s_waitcnt vmcnt(8)
	s_waitcnt lgkmcnt(0)
	s_barrier
	s_waitcnt lgkmcnt(0)
	v_mfma_f32_16x16x32_bf16 v[140:143], v[56:59], v[176:179], v[140:143]
	v_mfma_f32_16x16x32_bf16 v[136:139], v[64:67], v[176:179], v[136:139]
	v_mfma_f32_16x16x32_bf16 v[124:127], v[56:59], v[194:197], v[124:127]
	v_mfma_f32_16x16x32_bf16 v[120:123], v[64:67], v[194:197], v[120:123]
	v_mfma_f32_16x16x32_bf16 v[108:111], v[56:59], v[202:205], v[108:111]
	v_mfma_f32_16x16x32_bf16 v[104:107], v[64:67], v[202:205], v[104:107]
	v_mfma_f32_16x16x32_bf16 v[92:95], v[56:59], v[224:227], v[92:95]
	v_mfma_f32_16x16x32_bf16 v[88:91], v[64:67], v[224:227], v[88:91]
	v_mfma_f32_16x16x32_bf16 v[140:143], v[60:63], v[180:183], v[140:143]
	v_mfma_f32_16x16x32_bf16 v[136:139], v[68:71], v[180:183], v[136:139]
	v_mfma_f32_16x16x32_bf16 v[124:127], v[60:63], v[198:201], v[124:127]
	v_mfma_f32_16x16x32_bf16 v[120:123], v[68:71], v[198:201], v[120:123]
	v_mfma_f32_16x16x32_bf16 v[108:111], v[60:63], v[206:209], v[108:111]
	v_mfma_f32_16x16x32_bf16 v[104:107], v[68:71], v[206:209], v[104:107]
	v_mfma_f32_16x16x32_bf16 v[92:95], v[60:63], v[228:231], v[92:95]
	v_mfma_f32_16x16x32_bf16 v[88:91], v[68:71], v[228:231], v[88:91]
	v_mfma_f32_16x16x32_bf16 v[132:135], v[144:147], v[176:179], v[132:135]
	v_mfma_f32_16x16x32_bf16 v[128:131], v[162:165], v[176:179], v[128:131]
	v_mfma_f32_16x16x32_bf16 v[116:119], v[144:147], v[194:197], v[116:119]
	v_mfma_f32_16x16x32_bf16 v[112:115], v[162:165], v[194:197], v[112:115]
	v_mfma_f32_16x16x32_bf16 v[100:103], v[144:147], v[202:205], v[100:103]
	v_mfma_f32_16x16x32_bf16 v[96:99], v[162:165], v[202:205], v[96:99]
	v_mfma_f32_16x16x32_bf16 v[84:87], v[144:147], v[224:227], v[84:87]
	v_mfma_f32_16x16x32_bf16 v[80:83], v[162:165], v[224:227], v[80:83]
	v_mfma_f32_16x16x32_bf16 v[132:135], v[148:151], v[180:183], v[132:135]
	v_mfma_f32_16x16x32_bf16 v[128:131], v[172:175], v[180:183], v[128:131]
	v_mfma_f32_16x16x32_bf16 v[116:119], v[148:151], v[198:201], v[116:119]
	v_mfma_f32_16x16x32_bf16 v[112:115], v[172:175], v[198:201], v[112:115]
	v_mfma_f32_16x16x32_bf16 v[100:103], v[148:151], v[206:209], v[100:103]
	v_mfma_f32_16x16x32_bf16 v[96:99], v[172:175], v[206:209], v[96:99]
	v_mfma_f32_16x16x32_bf16 v[84:87], v[148:151], v[228:231], v[84:87]
	v_mfma_f32_16x16x32_bf16 v[80:83], v[172:175], v[228:231], v[80:83]
	s_barrier
	s_add_i32 s28, s48, s46
	v_lshl_add_u64 v[166:167], v[166:167], 0, s[68:69]
	s_mov_b32 m0, s28
	ds_read_b128 v[176:179], v171 offset:49152
	ds_read_b128 v[180:183], v171 offset:50176
	ds_read_b128 v[194:197], v171 offset:51200
	ds_read_b128 v[198:201], v171 offset:52224
	ds_read_b128 v[202:205], v171 offset:53248
	ds_read_b128 v[206:209], v171 offset:54272
	ds_read_b128 v[224:227], v171 offset:55296
	ds_read_b128 v[228:231], v171 offset:56320
	global_load_lds_dwordx4 v[166:167], off
	s_add_i32 m0, s28, 0x2000
	s_add_u32 s28, s42, 0x80080
	v_lshl_add_u64 v[166:167], v[210:211], 0, s[68:69]
	s_addc_u32 s29, s43, 0
	s_add_i32 s42, s49, s46
	global_load_lds_dwordx4 v[166:167], off
	v_lshl_add_u64 v[166:167], s[28:29], 0, v[184:185]
	s_mov_b32 m0, s42
	s_nop 0
	global_load_lds_dwordx4 v[166:167], off
	v_lshl_add_u64 v[166:167], s[28:29], 0, v[152:153]
	s_add_i32 m0, s42, 0x2000
	s_nop 0
	global_load_lds_dwordx4 v[166:167], off
	v_lshl_add_u64 v[166:167], v[216:217], 0, s[68:69]
	s_mov_b32 m0, s53
	s_nop 0
	global_load_lds_dwordx4 v[166:167], off
	v_lshl_add_u64 v[166:167], v[218:219], 0, s[68:69]
	s_mov_b32 m0, s58
	s_nop 0
	global_load_lds_dwordx4 v[166:167], off
	s_waitcnt vmcnt(8)
	s_waitcnt lgkmcnt(0)
	s_barrier
	s_waitcnt lgkmcnt(0)
	v_mfma_f32_16x16x32_bf16 v[76:79], v[56:59], v[176:179], v[76:79]
	v_mfma_f32_16x16x32_bf16 v[72:75], v[64:67], v[176:179], v[72:75]
	v_mfma_f32_16x16x32_bf16 v[52:55], v[56:59], v[194:197], v[52:55]
	v_mfma_f32_16x16x32_bf16 v[48:51], v[64:67], v[194:197], v[48:51]
	v_mfma_f32_16x16x32_bf16 v[28:31], v[56:59], v[202:205], v[28:31]
	v_mfma_f32_16x16x32_bf16 v[24:27], v[64:67], v[202:205], v[24:27]
	v_mfma_f32_16x16x32_bf16 v[12:15], v[56:59], v[224:227], v[12:15]
	v_mfma_f32_16x16x32_bf16 v[8:11], v[64:67], v[224:227], v[8:11]
	v_mfma_f32_16x16x32_bf16 v[76:79], v[60:63], v[180:183], v[76:79]
	v_mfma_f32_16x16x32_bf16 v[72:75], v[68:71], v[180:183], v[72:75]
	v_mfma_f32_16x16x32_bf16 v[52:55], v[60:63], v[198:201], v[52:55]
	v_mfma_f32_16x16x32_bf16 v[48:51], v[68:71], v[198:201], v[48:51]
	v_mfma_f32_16x16x32_bf16 v[28:31], v[60:63], v[206:209], v[28:31]
	v_mfma_f32_16x16x32_bf16 v[24:27], v[68:71], v[206:209], v[24:27]
	v_mfma_f32_16x16x32_bf16 v[12:15], v[60:63], v[228:231], v[12:15]
	v_mfma_f32_16x16x32_bf16 v[8:11], v[68:71], v[228:231], v[8:11]
	v_mfma_f32_16x16x32_bf16 v[40:43], v[144:147], v[176:179], v[40:43]
	v_mfma_f32_16x16x32_bf16 v[68:71], v[148:151], v[180:183], v[40:43]
	v_mfma_f32_16x16x32_bf16 v[40:43], v[162:165], v[176:179], v[44:47]
	v_mfma_f32_16x16x32_bf16 v[36:39], v[144:147], v[194:197], v[36:39]
	v_mfma_f32_16x16x32_bf16 v[32:35], v[162:165], v[194:197], v[32:35]
	v_mfma_f32_16x16x32_bf16 v[20:23], v[144:147], v[202:205], v[20:23]
	v_mfma_f32_16x16x32_bf16 v[16:19], v[162:165], v[202:205], v[16:19]
	v_mfma_f32_16x16x32_bf16 v[4:7], v[144:147], v[224:227], v[4:7]
	v_mfma_f32_16x16x32_bf16 v[0:3], v[162:165], v[224:227], v[0:3]
	v_mfma_f32_16x16x32_bf16 v[64:67], v[172:175], v[180:183], v[40:43]
	v_mfma_f32_16x16x32_bf16 v[36:39], v[148:151], v[198:201], v[36:39]
	v_mfma_f32_16x16x32_bf16 v[32:35], v[172:175], v[198:201], v[32:35]
	v_mfma_f32_16x16x32_bf16 v[20:23], v[148:151], v[206:209], v[20:23]
	v_mfma_f32_16x16x32_bf16 v[16:19], v[172:175], v[206:209], v[16:19]
	v_mfma_f32_16x16x32_bf16 v[4:7], v[148:151], v[228:231], v[4:7]
	v_mfma_f32_16x16x32_bf16 v[0:3], v[172:175], v[228:231], v[0:3]
	s_barrier
	s_add_i32 s79, s79, 2
	s_add_u32 s40, s40, 0x100
	s_addc_u32 s41, s41, 0
	s_add_u32 s62, s62, 0x100
	s_addc_u32 s63, s63, 0
	s_cmp_gt_u32 s79, 29
	s_cbranch_scc0 .LBB0_991
	s_and_b64 vcc, exec, s[8:9]
	s_cbranch_vccz .LBB0_994
	s_barrier

.LBB0_1136:
	s_add_u32 s48, s42, s50
	s_addc_u32 s49, s43, 0
	s_add_u32 s51, s48, 0x100
	s_addc_u32 s52, s49, 0
	s_and_b64 s[28:29], s[46:47], exec
	s_cselect_b32 s53, s11, s52
	s_cselect_b32 s52, s13, s51
	s_add_u32 s28, s38, s50
	s_addc_u32 s29, s39, 0
	s_add_u32 s50, s28, 0x100
	s_addc_u32 s51, s29, 0
	s_add_i32 s76, 0, 0x10000
	s_and_b64 s[28:29], s[46:47], exec
	s_cselect_b32 s59, s93, s51
	s_cselect_b32 s58, s94, s50
	s_add_i32 s47, 0, 0x14000
	s_add_u32 s62, s48, 0x80080
	s_addc_u32 s63, s49, 0
	s_add_i32 s49, s76, s20
	s_add_i32 m0, s21, 0xc000
	s_add_i32 s91, s21, 0xe000
	s_add_i32 s29, s49, 0x2000
	s_add_u32 s60, s58, 0x80000
	v_add_u32_e32 v132, s76, v168
	v_add_u32_e32 v166, s47, v168
	s_addc_u32 s61, s59, 0
	s_add_i32 vcc_hi, s47, s20
	ds_read_b128 v[112:115], v132
	ds_read_b128 v[116:119], v132 offset:1024
	ds_read_b128 v[124:127], v132 offset:2048
	ds_read_b128 v[132:135], v132 offset:3072
	ds_read_b128 v[172:175], v166
	ds_read_b128 v[176:179], v166 offset:1024
	ds_read_b128 v[180:183], v166 offset:2048
	ds_read_b128 v[194:197], v166 offset:3072
	s_add_i32 s85, vcc_hi, 0x2000
	s_add_i32 s48, 0, 0x18000
	s_add_i32 s28, 0, 0x1c000
	s_add_u32 s50, s52, 0x80000
	s_addc_u32 s51, s53, 0
	s_add_i32 vcc_lo, s48, s20
	s_add_i32 s95, vcc_lo, 0x2000
	s_add_u32 s46, s58, 0x80080
	s_addc_u32 s47, s59, 0
	s_add_i32 s76, s28, s20
	s_add_i32 s90, s76, 0x2000
	v_lshl_add_u64 v[166:167], s[62:63], 0, v[148:149]
	ds_read_b128 v[198:201], v170
	ds_read_b128 v[202:205], v170 offset:1024
	ds_read_b128 v[206:209], v170 offset:2048
	ds_read_b128 v[224:227], v170 offset:3072
	ds_read_b128 v[228:231], v170 offset:4096
	ds_read_b128 v[232:235], v170 offset:5120
	ds_read_b128 v[236:239], v170 offset:6144
	ds_read_b128 v[240:243], v170 offset:7168
	global_load_lds_dwordx4 v[166:167], off
	v_lshl_add_u64 v[166:167], s[62:63], 0, v[146:147]
	s_mov_b32 m0, s91
	s_nop 0
	global_load_lds_dwordx4 v[166:167], off
	s_waitcnt vmcnt(8)
	s_waitcnt lgkmcnt(0)
	s_barrier
	s_waitcnt lgkmcnt(0)
	v_mfma_f32_16x16x32_bf16 v[140:143], v[112:115], v[198:201], v[140:143]
	v_mfma_f32_16x16x32_bf16 v[136:139], v[124:127], v[198:201], v[136:139]
	v_mfma_f32_16x16x32_bf16 v[108:111], v[112:115], v[206:209], v[108:111]
	v_mfma_f32_16x16x32_bf16 v[104:107], v[124:127], v[206:209], v[104:107]
	v_mfma_f32_16x16x32_bf16 v[92:95], v[112:115], v[228:231], v[92:95]
	v_mfma_f32_16x16x32_bf16 v[88:91], v[124:127], v[228:231], v[88:91]
	v_mfma_f32_16x16x32_bf16 v[76:79], v[112:115], v[236:239], v[76:79]
	v_mfma_f32_16x16x32_bf16 v[72:75], v[124:127], v[236:239], v[72:75]
	v_mfma_f32_16x16x32_bf16 v[140:143], v[116:119], v[202:205], v[140:143]
	v_mfma_f32_16x16x32_bf16 v[136:139], v[132:135], v[202:205], v[136:139]
	v_mfma_f32_16x16x32_bf16 v[108:111], v[116:119], v[224:227], v[108:111]
	v_mfma_f32_16x16x32_bf16 v[104:107], v[132:135], v[224:227], v[104:107]
	v_mfma_f32_16x16x32_bf16 v[92:95], v[116:119], v[232:235], v[92:95]
	v_mfma_f32_16x16x32_bf16 v[88:91], v[132:135], v[232:235], v[88:91]
	v_mfma_f32_16x16x32_bf16 v[76:79], v[116:119], v[240:243], v[76:79]
	v_mfma_f32_16x16x32_bf16 v[72:75], v[132:135], v[240:243], v[72:75]
	v_mfma_f32_16x16x32_bf16 v[128:131], v[172:175], v[198:201], v[128:131]
	v_mfma_f32_16x16x32_bf16 v[120:123], v[180:183], v[198:201], v[120:123]
	v_mfma_f32_16x16x32_bf16 v[100:103], v[172:175], v[206:209], v[100:103]
	v_mfma_f32_16x16x32_bf16 v[96:99], v[180:183], v[206:209], v[96:99]
	v_mfma_f32_16x16x32_bf16 v[84:87], v[172:175], v[228:231], v[84:87]
	v_mfma_f32_16x16x32_bf16 v[80:83], v[180:183], v[228:231], v[80:83]
	v_mfma_f32_16x16x32_bf16 v[68:71], v[172:175], v[236:239], v[68:71]
	v_mfma_f32_16x16x32_bf16 v[64:67], v[180:183], v[236:239], v[64:67]
	v_mfma_f32_16x16x32_bf16 v[128:131], v[176:179], v[202:205], v[128:131]
	v_mfma_f32_16x16x32_bf16 v[120:123], v[194:197], v[202:205], v[120:123]
	v_mfma_f32_16x16x32_bf16 v[100:103], v[176:179], v[224:227], v[100:103]
	v_mfma_f32_16x16x32_bf16 v[96:99], v[194:197], v[224:227], v[96:99]
	v_mfma_f32_16x16x32_bf16 v[84:87], v[176:179], v[232:235], v[84:87]
	v_mfma_f32_16x16x32_bf16 v[80:83], v[194:197], v[232:235], v[80:83]
	v_mfma_f32_16x16x32_bf16 v[68:71], v[176:179], v[240:243], v[68:71]
	v_mfma_f32_16x16x32_bf16 v[64:67], v[194:197], v[240:243], v[64:67]
	s_barrier
	s_mov_b32 m0, s49
	v_lshl_add_u64 v[166:167], s[58:59], 0, v[184:185]
	ds_read_b128 v[198:201], v170 offset:16384
	ds_read_b128 v[202:205], v170 offset:17408
	ds_read_b128 v[206:209], v170 offset:18432
	ds_read_b128 v[224:227], v170 offset:19456
	ds_read_b128 v[228:231], v170 offset:20480
	ds_read_b128 v[232:235], v170 offset:21504
	ds_read_b128 v[236:239], v170 offset:22528
	ds_read_b128 v[240:243], v170 offset:23552
	global_load_lds_dwordx4 v[166:167], off
	v_lshl_add_u64 v[210:211], s[58:59], 0, v[144:145]
	s_mov_b32 m0, s29
	v_lshl_add_u64 v[216:217], s[60:61], 0, v[184:185]
	global_load_lds_dwordx4 v[210:211], off
	s_mov_b32 m0, vcc_hi
	v_lshl_add_u64 v[218:219], s[52:53], 0, v[146:147]
	global_load_lds_dwordx4 v[216:217], off
	v_lshl_add_u64 v[216:217], s[60:61], 0, v[144:145]
	s_mov_b32 m0, s85
	s_nop 0
	global_load_lds_dwordx4 v[216:217], off
	v_lshl_add_u64 v[216:217], s[52:53], 0, v[148:149]
	s_mov_b32 m0, s21
	s_nop 0
	global_load_lds_dwordx4 v[216:217], off
	s_mov_b32 m0, s26
	s_nop 0
	global_load_lds_dwordx4 v[218:219], off
	s_waitcnt vmcnt(8)
	s_waitcnt lgkmcnt(0)
	s_barrier
	s_waitcnt lgkmcnt(0)
	v_mfma_f32_16x16x32_bf16 v[60:63], v[112:115], v[198:201], v[60:63]
	v_mfma_f32_16x16x32_bf16 v[56:59], v[124:127], v[198:201], v[56:59]
	v_mfma_f32_16x16x32_bf16 v[44:47], v[112:115], v[206:209], v[44:47]
	v_mfma_f32_16x16x32_bf16 v[40:43], v[124:127], v[206:209], v[40:43]
	v_mfma_f32_16x16x32_bf16 v[36:39], v[112:115], v[228:231], v[36:39]
	v_mfma_f32_16x16x32_bf16 v[28:31], v[124:127], v[228:231], v[28:31]
	v_mfma_f32_16x16x32_bf16 v[20:23], v[112:115], v[236:239], v[20:23]
	v_mfma_f32_16x16x32_bf16 v[12:15], v[124:127], v[236:239], v[12:15]
	v_mfma_f32_16x16x32_bf16 v[60:63], v[116:119], v[202:205], v[60:63]
	v_mfma_f32_16x16x32_bf16 v[56:59], v[132:135], v[202:205], v[56:59]
	v_mfma_f32_16x16x32_bf16 v[44:47], v[116:119], v[224:227], v[44:47]
	v_mfma_f32_16x16x32_bf16 v[40:43], v[132:135], v[224:227], v[40:43]
	v_mfma_f32_16x16x32_bf16 v[36:39], v[116:119], v[232:235], v[36:39]
	v_mfma_f32_16x16x32_bf16 v[28:31], v[132:135], v[232:235], v[28:31]
	v_mfma_f32_16x16x32_bf16 v[20:23], v[116:119], v[240:243], v[20:23]
	v_mfma_f32_16x16x32_bf16 v[12:15], v[132:135], v[240:243], v[12:15]
	v_mfma_f32_16x16x32_bf16 v[52:55], v[172:175], v[198:201], v[52:55]
	v_mfma_f32_16x16x32_bf16 v[48:51], v[180:183], v[198:201], v[48:51]
	v_mfma_f32_16x16x32_bf16 v[32:35], v[172:175], v[206:209], v[32:35]
	v_mfma_f32_16x16x32_bf16 v[24:27], v[180:183], v[206:209], v[24:27]
	v_mfma_f32_16x16x32_bf16 v[16:19], v[172:175], v[228:231], v[16:19]
	v_mfma_f32_16x16x32_bf16 v[8:11], v[180:183], v[228:231], v[8:11]
	v_mfma_f32_16x16x32_bf16 v[4:7], v[172:175], v[236:239], v[4:7]
	v_mfma_f32_16x16x32_bf16 v[0:3], v[180:183], v[236:239], v[0:3]
	v_mfma_f32_16x16x32_bf16 v[52:55], v[176:179], v[202:205], v[52:55]
	v_mfma_f32_16x16x32_bf16 v[48:51], v[194:197], v[202:205], v[48:51]
	v_mfma_f32_16x16x32_bf16 v[32:35], v[176:179], v[224:227], v[32:35]
	v_mfma_f32_16x16x32_bf16 v[24:27], v[194:197], v[224:227], v[24:27]
	v_mfma_f32_16x16x32_bf16 v[16:19], v[176:179], v[232:235], v[16:19]
	v_mfma_f32_16x16x32_bf16 v[8:11], v[194:197], v[232:235], v[8:11]
	v_mfma_f32_16x16x32_bf16 v[4:7], v[176:179], v[240:243], v[4:7]
	v_mfma_f32_16x16x32_bf16 v[0:3], v[194:197], v[240:243], v[0:3]
	s_barrier
	v_add_u32_e32 v132, s48, v168
	v_add_u32_e32 v171, s28, v168
	ds_read_b128 v[112:115], v132
	ds_read_b128 v[116:119], v132 offset:1024
	ds_read_b128 v[124:127], v132 offset:2048
	ds_read_b128 v[132:135], v132 offset:3072
	ds_read_b128 v[172:175], v171
	ds_read_b128 v[176:179], v171 offset:1024
	ds_read_b128 v[180:183], v171 offset:2048
	ds_read_b128 v[194:197], v171 offset:3072
	s_mov_b32 m0, s27
	v_lshl_add_u64 v[244:245], s[50:51], 0, v[148:149]
	ds_read_b128 v[198:201], v170 offset:32768
	ds_read_b128 v[202:205], v170 offset:33792
	ds_read_b128 v[206:209], v170 offset:34816
	ds_read_b128 v[224:227], v170 offset:35840
	ds_read_b128 v[228:231], v170 offset:36864
	ds_read_b128 v[232:235], v170 offset:37888
	ds_read_b128 v[236:239], v170 offset:38912
	ds_read_b128 v[240:243], v170 offset:39936
	global_load_lds_dwordx4 v[244:245], off
	v_lshl_add_u64 v[244:245], s[50:51], 0, v[146:147]
	s_mov_b32 m0, s79
	s_nop 0
	global_load_lds_dwordx4 v[244:245], off
	s_waitcnt vmcnt(8)
	s_waitcnt lgkmcnt(0)
	s_barrier
	s_waitcnt lgkmcnt(0)
	v_mfma_f32_16x16x32_bf16 v[140:143], v[112:115], v[198:201], v[140:143]
	v_mfma_f32_16x16x32_bf16 v[136:139], v[124:127], v[198:201], v[136:139]
	v_mfma_f32_16x16x32_bf16 v[108:111], v[112:115], v[206:209], v[108:111]
	v_mfma_f32_16x16x32_bf16 v[104:107], v[124:127], v[206:209], v[104:107]
	v_mfma_f32_16x16x32_bf16 v[92:95], v[112:115], v[228:231], v[92:95]
	v_mfma_f32_16x16x32_bf16 v[88:91], v[124:127], v[228:231], v[88:91]
	v_mfma_f32_16x16x32_bf16 v[76:79], v[112:115], v[236:239], v[76:79]
	v_mfma_f32_16x16x32_bf16 v[72:75], v[124:127], v[236:239], v[72:75]
	v_mfma_f32_16x16x32_bf16 v[140:143], v[116:119], v[202:205], v[140:143]
	v_mfma_f32_16x16x32_bf16 v[136:139], v[132:135], v[202:205], v[136:139]
	v_mfma_f32_16x16x32_bf16 v[108:111], v[116:119], v[224:227], v[108:111]
	v_mfma_f32_16x16x32_bf16 v[104:107], v[132:135], v[224:227], v[104:107]
	v_mfma_f32_16x16x32_bf16 v[92:95], v[116:119], v[232:235], v[92:95]
	v_mfma_f32_16x16x32_bf16 v[88:91], v[132:135], v[232:235], v[88:91]
	v_mfma_f32_16x16x32_bf16 v[76:79], v[116:119], v[240:243], v[76:79]
	v_mfma_f32_16x16x32_bf16 v[72:75], v[132:135], v[240:243], v[72:75]
	v_mfma_f32_16x16x32_bf16 v[128:131], v[172:175], v[198:201], v[128:131]
	v_mfma_f32_16x16x32_bf16 v[120:123], v[180:183], v[198:201], v[120:123]
	v_mfma_f32_16x16x32_bf16 v[100:103], v[172:175], v[206:209], v[100:103]
	v_mfma_f32_16x16x32_bf16 v[96:99], v[180:183], v[206:209], v[96:99]
	v_mfma_f32_16x16x32_bf16 v[84:87], v[172:175], v[228:231], v[84:87]
	v_mfma_f32_16x16x32_bf16 v[80:83], v[180:183], v[228:231], v[80:83]
	v_mfma_f32_16x16x32_bf16 v[68:71], v[172:175], v[236:239], v[68:71]
	v_mfma_f32_16x16x32_bf16 v[64:67], v[180:183], v[236:239], v[64:67]
	v_mfma_f32_16x16x32_bf16 v[128:131], v[176:179], v[202:205], v[128:131]
	v_mfma_f32_16x16x32_bf16 v[120:123], v[194:197], v[202:205], v[120:123]
	v_mfma_f32_16x16x32_bf16 v[100:103], v[176:179], v[224:227], v[100:103]
	v_mfma_f32_16x16x32_bf16 v[96:99], v[194:197], v[224:227], v[96:99]
	v_mfma_f32_16x16x32_bf16 v[84:87], v[176:179], v[232:235], v[84:87]
	v_mfma_f32_16x16x32_bf16 v[80:83], v[194:197], v[232:235], v[80:83]
	v_mfma_f32_16x16x32_bf16 v[68:71], v[176:179], v[240:243], v[68:71]
	v_mfma_f32_16x16x32_bf16 v[64:67], v[194:197], v[240:243], v[64:67]
	s_barrier
	s_mov_b32 m0, vcc_lo
	v_lshl_add_u64 v[166:167], v[166:167], 0, s[68:69]
	ds_read_b128 v[198:201], v170 offset:49152
	ds_read_b128 v[202:205], v170 offset:50176
	ds_read_b128 v[206:209], v170 offset:51200
	ds_read_b128 v[224:227], v170 offset:52224
	ds_read_b128 v[228:231], v170 offset:53248
	ds_read_b128 v[232:235], v170 offset:54272
	ds_read_b128 v[236:239], v170 offset:55296
	ds_read_b128 v[240:243], v170 offset:56320
	global_load_lds_dwordx4 v[166:167], off
	v_lshl_add_u64 v[166:167], v[210:211], 0, s[68:69]
	s_mov_b32 m0, s95
	s_nop 0
	global_load_lds_dwordx4 v[166:167], off
	v_lshl_add_u64 v[166:167], s[46:47], 0, v[184:185]
	s_mov_b32 m0, s76
	s_nop 0
	global_load_lds_dwordx4 v[166:167], off
	v_lshl_add_u64 v[166:167], s[46:47], 0, v[144:145]
	s_mov_b32 m0, s90
	s_nop 0
	global_load_lds_dwordx4 v[166:167], off
	v_lshl_add_u64 v[166:167], v[216:217], 0, s[68:69]
	s_mov_b32 m0, s88
	s_nop 0
	global_load_lds_dwordx4 v[166:167], off
	v_lshl_add_u64 v[166:167], v[218:219], 0, s[68:69]
	s_mov_b32 m0, s89
	s_nop 0
	global_load_lds_dwordx4 v[166:167], off
	s_waitcnt vmcnt(8)
	s_waitcnt lgkmcnt(0)
	s_barrier
	s_waitcnt lgkmcnt(0)
	v_mfma_f32_16x16x32_bf16 v[60:63], v[112:115], v[198:201], v[60:63]
	v_mfma_f32_16x16x32_bf16 v[56:59], v[124:127], v[198:201], v[56:59]
	v_mfma_f32_16x16x32_bf16 v[44:47], v[112:115], v[206:209], v[44:47]
	v_mfma_f32_16x16x32_bf16 v[40:43], v[124:127], v[206:209], v[40:43]
	v_mfma_f32_16x16x32_bf16 v[36:39], v[112:115], v[228:231], v[36:39]
	v_mfma_f32_16x16x32_bf16 v[28:31], v[124:127], v[228:231], v[28:31]
	v_mfma_f32_16x16x32_bf16 v[20:23], v[112:115], v[236:239], v[20:23]
	v_mfma_f32_16x16x32_bf16 v[12:15], v[124:127], v[236:239], v[12:15]
	v_mfma_f32_16x16x32_bf16 v[60:63], v[116:119], v[202:205], v[60:63]
	v_mfma_f32_16x16x32_bf16 v[56:59], v[132:135], v[202:205], v[56:59]
	v_mfma_f32_16x16x32_bf16 v[44:47], v[116:119], v[224:227], v[44:47]
	v_mfma_f32_16x16x32_bf16 v[40:43], v[132:135], v[224:227], v[40:43]
	v_mfma_f32_16x16x32_bf16 v[36:39], v[116:119], v[232:235], v[36:39]
	v_mfma_f32_16x16x32_bf16 v[28:31], v[132:135], v[232:235], v[28:31]
	v_mfma_f32_16x16x32_bf16 v[20:23], v[116:119], v[240:243], v[20:23]
	v_mfma_f32_16x16x32_bf16 v[12:15], v[132:135], v[240:243], v[12:15]
	v_mfma_f32_16x16x32_bf16 v[52:55], v[172:175], v[198:201], v[52:55]
	v_mfma_f32_16x16x32_bf16 v[48:51], v[180:183], v[198:201], v[48:51]
	v_mfma_f32_16x16x32_bf16 v[32:35], v[172:175], v[206:209], v[32:35]
	v_mfma_f32_16x16x32_bf16 v[24:27], v[180:183], v[206:209], v[24:27]
	v_mfma_f32_16x16x32_bf16 v[16:19], v[172:175], v[228:231], v[16:19]
	v_mfma_f32_16x16x32_bf16 v[8:11], v[180:183], v[228:231], v[8:11]
	v_mfma_f32_16x16x32_bf16 v[4:7], v[172:175], v[236:239], v[4:7]
	v_mfma_f32_16x16x32_bf16 v[0:3], v[180:183], v[236:239], v[0:3]
	v_mfma_f32_16x16x32_bf16 v[52:55], v[176:179], v[202:205], v[52:55]
	v_mfma_f32_16x16x32_bf16 v[48:51], v[194:197], v[202:205], v[48:51]
	v_mfma_f32_16x16x32_bf16 v[32:35], v[176:179], v[224:227], v[32:35]
	v_mfma_f32_16x16x32_bf16 v[24:27], v[194:197], v[224:227], v[24:27]
	v_mfma_f32_16x16x32_bf16 v[16:19], v[176:179], v[232:235], v[16:19]
	v_mfma_f32_16x16x32_bf16 v[8:11], v[194:197], v[232:235], v[8:11]
	v_mfma_f32_16x16x32_bf16 v[4:7], v[176:179], v[240:243], v[4:7]
	v_mfma_f32_16x16x32_bf16 v[0:3], v[194:197], v[240:243], v[0:3]
	s_barrier
	s_movk_i32 s50, 0x100
	s_andn2_b64 vcc, exec, s[44:45]
	s_mov_b64 s[46:47], -1
	s_mov_b64 s[44:45], 0
	s_cbranch_vccz .LBB0_1136
	s_and_b64 vcc, exec, s[8:9]
	s_cbranch_vccz .LBB0_1139
	s_barrier

.LBB0_1419:
	s_add_u32 s28, s24, 0xfff80080
	s_addc_u32 s29, s25, -1
	s_add_i32 s48, 0, 0x10000
	s_cmp_eq_u32 s17, 28
	s_cselect_b32 s31, s9, s29
	s_cselect_b32 s30, s11, s28
	s_cselect_b64 vcc, -1, 0
	s_add_i32 s28, 0, 0x14000
	v_add_u32_e32 v164, s48, v147
	v_add_u32_e32 v180, s28, v147
	ds_read_b128 v[152:155], v164
	ds_read_b128 v[156:159], v164 offset:1024
	ds_read_b128 v[160:163], v164 offset:2048
	ds_read_b128 v[164:167], v164 offset:3072
	ds_read_b128 v[168:171], v180
	ds_read_b128 v[172:175], v180 offset:1024
	ds_read_b128 v[176:179], v180 offset:2048
	ds_read_b128 v[180:183], v180 offset:3072
	v_cndmask_b32_e32 v211, v145, v150, vcc
	v_cndmask_b32_e32 v210, v144, v151, vcc
	v_lshl_add_u64 v[216:217], s[24:25], 0, v[136:137]
	s_add_i32 m0, s19, 0xc000
	ds_read_b128 v[194:197], v149
	ds_read_b128 v[198:201], v149 offset:1024
	ds_read_b128 v[202:205], v149 offset:2048
	ds_read_b128 v[206:209], v149 offset:3072
	ds_read_b128 v[224:227], v149 offset:4096
	ds_read_b128 v[228:231], v149 offset:5120
	ds_read_b128 v[232:235], v149 offset:6144
	ds_read_b128 v[236:239], v149 offset:7168
	global_load_lds_dwordx4 v[216:217], off
	v_lshl_add_u64 v[216:217], s[24:25], 0, v[138:139]
	s_add_i32 m0, s19, 0xe000
	s_nop 0
	global_load_lds_dwordx4 v[216:217], off
	s_waitcnt vmcnt(8)
	s_waitcnt lgkmcnt(0)
	s_barrier
	s_waitcnt lgkmcnt(0)
	v_mfma_f32_16x16x32_bf16 v[124:127], v[152:155], v[194:197], v[124:127]
	v_mfma_f32_16x16x32_bf16 v[116:119], v[160:163], v[194:197], v[116:119]
	v_mfma_f32_16x16x32_bf16 v[108:111], v[152:155], v[202:205], v[108:111]
	v_mfma_f32_16x16x32_bf16 v[100:103], v[160:163], v[202:205], v[100:103]
	v_mfma_f32_16x16x32_bf16 v[92:95], v[152:155], v[224:227], v[92:95]
	v_mfma_f32_16x16x32_bf16 v[84:87], v[160:163], v[224:227], v[84:87]
	v_mfma_f32_16x16x32_bf16 v[76:79], v[152:155], v[232:235], v[76:79]
	v_mfma_f32_16x16x32_bf16 v[68:71], v[160:163], v[232:235], v[68:71]
	v_mfma_f32_16x16x32_bf16 v[124:127], v[156:159], v[198:201], v[124:127]
	v_mfma_f32_16x16x32_bf16 v[116:119], v[164:167], v[198:201], v[116:119]
	v_mfma_f32_16x16x32_bf16 v[108:111], v[156:159], v[206:209], v[108:111]
	v_mfma_f32_16x16x32_bf16 v[100:103], v[164:167], v[206:209], v[100:103]
	v_mfma_f32_16x16x32_bf16 v[92:95], v[156:159], v[228:231], v[92:95]
	v_mfma_f32_16x16x32_bf16 v[84:87], v[164:167], v[228:231], v[84:87]
	v_mfma_f32_16x16x32_bf16 v[76:79], v[156:159], v[236:239], v[76:79]
	v_mfma_f32_16x16x32_bf16 v[68:71], v[164:167], v[236:239], v[68:71]
	v_mfma_f32_16x16x32_bf16 v[120:123], v[168:171], v[194:197], v[120:123]
	v_mfma_f32_16x16x32_bf16 v[112:115], v[176:179], v[194:197], v[112:115]
	v_mfma_f32_16x16x32_bf16 v[104:107], v[168:171], v[202:205], v[104:107]
	v_mfma_f32_16x16x32_bf16 v[96:99], v[176:179], v[202:205], v[96:99]
	v_mfma_f32_16x16x32_bf16 v[88:91], v[168:171], v[224:227], v[88:91]
	v_mfma_f32_16x16x32_bf16 v[80:83], v[176:179], v[224:227], v[80:83]
	v_mfma_f32_16x16x32_bf16 v[72:75], v[168:171], v[232:235], v[72:75]
	v_mfma_f32_16x16x32_bf16 v[64:67], v[176:179], v[232:235], v[64:67]
	v_mfma_f32_16x16x32_bf16 v[120:123], v[172:175], v[198:201], v[120:123]
	v_mfma_f32_16x16x32_bf16 v[112:115], v[180:183], v[198:201], v[112:115]
	v_mfma_f32_16x16x32_bf16 v[104:107], v[172:175], v[206:209], v[104:107]
	v_mfma_f32_16x16x32_bf16 v[96:99], v[180:183], v[206:209], v[96:99]
	v_mfma_f32_16x16x32_bf16 v[88:91], v[172:175], v[228:231], v[88:91]
	v_mfma_f32_16x16x32_bf16 v[80:83], v[180:183], v[228:231], v[80:83]
	v_mfma_f32_16x16x32_bf16 v[72:75], v[172:175], v[236:239], v[72:75]
	v_mfma_f32_16x16x32_bf16 v[64:67], v[180:183], v[236:239], v[64:67]
	s_barrier
	s_add_i32 s29, s48, s50
	v_lshl_add_u64 v[216:217], v[210:211], 0, v[130:131]
	s_mov_b32 m0, s29
	ds_read_b128 v[194:197], v149 offset:16384
	ds_read_b128 v[198:201], v149 offset:17408
	ds_read_b128 v[202:205], v149 offset:18432
	ds_read_b128 v[206:209], v149 offset:19456
	ds_read_b128 v[224:227], v149 offset:20480
	ds_read_b128 v[228:231], v149 offset:21504
	ds_read_b128 v[232:235], v149 offset:22528
	ds_read_b128 v[236:239], v149 offset:23552
	global_load_lds_dwordx4 v[216:217], off
	v_lshl_add_u64 v[218:219], v[210:211], 0, v[134:135]
	s_add_i32 m0, s29, 0x2000
	v_lshl_add_u64 v[220:221], v[210:211], 0, s[72:73]
	s_add_i32 s28, s28, s50
	global_load_lds_dwordx4 v[218:219], off
	v_lshl_add_u64 v[240:241], v[220:221], 0, v[130:131]
	s_mov_b32 m0, s28
	v_lshl_add_u64 v[220:221], v[220:221], 0, v[134:135]
	global_load_lds_dwordx4 v[240:241], off
	s_add_i32 m0, s28, 0x2000
	v_lshl_add_u64 v[240:241], s[30:31], 0, v[132:133]
	global_load_lds_dwordx4 v[220:221], off
	v_lshl_add_u64 v[220:221], s[30:31], 0, v[128:129]
	s_mov_b32 m0, s19
	s_nop 0
	global_load_lds_dwordx4 v[220:221], off
	s_mov_b32 m0, s51
	s_nop 0
	global_load_lds_dwordx4 v[240:241], off
	s_waitcnt vmcnt(8)
	s_waitcnt lgkmcnt(0)
	s_barrier
	s_waitcnt lgkmcnt(0)
	v_mfma_f32_16x16x32_bf16 v[60:63], v[152:155], v[194:197], v[60:63]
	v_mfma_f32_16x16x32_bf16 v[52:55], v[160:163], v[194:197], v[52:55]
	v_mfma_f32_16x16x32_bf16 v[44:47], v[152:155], v[202:205], v[44:47]
	v_mfma_f32_16x16x32_bf16 v[36:39], v[160:163], v[202:205], v[36:39]
	v_mfma_f32_16x16x32_bf16 v[28:31], v[152:155], v[224:227], v[28:31]
	v_mfma_f32_16x16x32_bf16 v[20:23], v[160:163], v[224:227], v[20:23]
	v_mfma_f32_16x16x32_bf16 v[12:15], v[152:155], v[232:235], v[12:15]
	v_mfma_f32_16x16x32_bf16 v[4:7], v[160:163], v[232:235], v[4:7]
	v_mfma_f32_16x16x32_bf16 v[60:63], v[156:159], v[198:201], v[60:63]
	v_mfma_f32_16x16x32_bf16 v[52:55], v[164:167], v[198:201], v[52:55]
	v_mfma_f32_16x16x32_bf16 v[44:47], v[156:159], v[206:209], v[44:47]
	v_mfma_f32_16x16x32_bf16 v[36:39], v[164:167], v[206:209], v[36:39]
	v_mfma_f32_16x16x32_bf16 v[28:31], v[156:159], v[228:231], v[28:31]
	v_mfma_f32_16x16x32_bf16 v[20:23], v[164:167], v[228:231], v[20:23]
	v_mfma_f32_16x16x32_bf16 v[12:15], v[156:159], v[236:239], v[12:15]
	v_mfma_f32_16x16x32_bf16 v[4:7], v[164:167], v[236:239], v[4:7]
	v_mfma_f32_16x16x32_bf16 v[56:59], v[168:171], v[194:197], v[56:59]
	v_mfma_f32_16x16x32_bf16 v[48:51], v[176:179], v[194:197], v[48:51]
	v_mfma_f32_16x16x32_bf16 v[40:43], v[168:171], v[202:205], v[40:43]
	v_mfma_f32_16x16x32_bf16 v[32:35], v[176:179], v[202:205], v[32:35]
	v_mfma_f32_16x16x32_bf16 v[24:27], v[168:171], v[224:227], v[24:27]
	v_mfma_f32_16x16x32_bf16 v[16:19], v[176:179], v[224:227], v[16:19]
	v_mfma_f32_16x16x32_bf16 v[8:11], v[168:171], v[232:235], v[8:11]
	v_mfma_f32_16x16x32_bf16 v[0:3], v[176:179], v[232:235], v[0:3]
	v_mfma_f32_16x16x32_bf16 v[56:59], v[172:175], v[198:201], v[56:59]
	v_mfma_f32_16x16x32_bf16 v[48:51], v[180:183], v[198:201], v[48:51]
	v_mfma_f32_16x16x32_bf16 v[40:43], v[172:175], v[206:209], v[40:43]
	v_mfma_f32_16x16x32_bf16 v[32:35], v[180:183], v[206:209], v[32:35]
	v_mfma_f32_16x16x32_bf16 v[24:27], v[172:175], v[228:231], v[24:27]
	v_mfma_f32_16x16x32_bf16 v[16:19], v[180:183], v[228:231], v[16:19]
	v_mfma_f32_16x16x32_bf16 v[8:11], v[172:175], v[236:239], v[8:11]
	v_mfma_f32_16x16x32_bf16 v[0:3], v[180:183], v[236:239], v[0:3]
	s_barrier
	s_add_i32 s48, 0, 0x18000
	s_add_i32 s49, 0, 0x1c000
	v_add_u32_e32 v164, s48, v147
	v_add_u32_e32 v180, s49, v147
	ds_read_b128 v[152:155], v164
	ds_read_b128 v[156:159], v164 offset:1024
	ds_read_b128 v[160:163], v164 offset:2048
	ds_read_b128 v[164:167], v164 offset:3072
	ds_read_b128 v[168:171], v180
	ds_read_b128 v[172:175], v180 offset:1024
	ds_read_b128 v[176:179], v180 offset:2048
	ds_read_b128 v[180:183], v180 offset:3072
	s_add_u32 s28, s30, 0x80000
	s_addc_u32 s29, s31, 0
	s_mov_b32 m0, s52
	v_lshl_add_u64 v[242:243], s[28:29], 0, v[128:129]
	ds_read_b128 v[194:197], v149 offset:32768
	ds_read_b128 v[198:201], v149 offset:33792
	ds_read_b128 v[202:205], v149 offset:34816
	ds_read_b128 v[206:209], v149 offset:35840
	ds_read_b128 v[224:227], v149 offset:36864
	ds_read_b128 v[228:231], v149 offset:37888
	ds_read_b128 v[232:235], v149 offset:38912
	ds_read_b128 v[236:239], v149 offset:39936
	global_load_lds_dwordx4 v[242:243], off
	v_lshl_add_u64 v[242:243], s[28:29], 0, v[132:133]
	s_mov_b32 m0, s53
	s_nop 0
	global_load_lds_dwordx4 v[242:243], off
	s_waitcnt vmcnt(8)
	s_waitcnt lgkmcnt(0)
	s_barrier
	s_waitcnt lgkmcnt(0)
	v_mfma_f32_16x16x32_bf16 v[124:127], v[152:155], v[194:197], v[124:127]
	v_mfma_f32_16x16x32_bf16 v[116:119], v[160:163], v[194:197], v[116:119]
	v_mfma_f32_16x16x32_bf16 v[108:111], v[152:155], v[202:205], v[108:111]
	v_mfma_f32_16x16x32_bf16 v[100:103], v[160:163], v[202:205], v[100:103]
	v_mfma_f32_16x16x32_bf16 v[92:95], v[152:155], v[224:227], v[92:95]
	v_mfma_f32_16x16x32_bf16 v[84:87], v[160:163], v[224:227], v[84:87]
	v_mfma_f32_16x16x32_bf16 v[76:79], v[152:155], v[232:235], v[76:79]
	v_mfma_f32_16x16x32_bf16 v[68:71], v[160:163], v[232:235], v[68:71]
	v_mfma_f32_16x16x32_bf16 v[124:127], v[156:159], v[198:201], v[124:127]
	v_mfma_f32_16x16x32_bf16 v[116:119], v[164:167], v[198:201], v[116:119]
	v_mfma_f32_16x16x32_bf16 v[108:111], v[156:159], v[206:209], v[108:111]
	v_mfma_f32_16x16x32_bf16 v[100:103], v[164:167], v[206:209], v[100:103]
	v_mfma_f32_16x16x32_bf16 v[92:95], v[156:159], v[228:231], v[92:95]
	v_mfma_f32_16x16x32_bf16 v[84:87], v[164:167], v[228:231], v[84:87]
	v_mfma_f32_16x16x32_bf16 v[76:79], v[156:159], v[236:239], v[76:79]
	v_mfma_f32_16x16x32_bf16 v[68:71], v[164:167], v[236:239], v[68:71]
	v_mfma_f32_16x16x32_bf16 v[120:123], v[168:171], v[194:197], v[120:123]
	v_mfma_f32_16x16x32_bf16 v[112:115], v[176:179], v[194:197], v[112:115]
	v_mfma_f32_16x16x32_bf16 v[104:107], v[168:171], v[202:205], v[104:107]
	v_mfma_f32_16x16x32_bf16 v[96:99], v[176:179], v[202:205], v[96:99]
	v_mfma_f32_16x16x32_bf16 v[88:91], v[168:171], v[224:227], v[88:91]
	v_mfma_f32_16x16x32_bf16 v[80:83], v[176:179], v[224:227], v[80:83]
	v_mfma_f32_16x16x32_bf16 v[72:75], v[168:171], v[232:235], v[72:75]
	v_mfma_f32_16x16x32_bf16 v[64:67], v[176:179], v[232:235], v[64:67]
	v_mfma_f32_16x16x32_bf16 v[120:123], v[172:175], v[198:201], v[120:123]
	v_mfma_f32_16x16x32_bf16 v[112:115], v[180:183], v[198:201], v[112:115]
	v_mfma_f32_16x16x32_bf16 v[104:107], v[172:175], v[206:209], v[104:107]
	v_mfma_f32_16x16x32_bf16 v[96:99], v[180:183], v[206:209], v[96:99]
	v_mfma_f32_16x16x32_bf16 v[88:91], v[172:175], v[228:231], v[88:91]
	v_mfma_f32_16x16x32_bf16 v[80:83], v[180:183], v[228:231], v[80:83]
	v_mfma_f32_16x16x32_bf16 v[72:75], v[172:175], v[236:239], v[72:75]
	v_mfma_f32_16x16x32_bf16 v[64:67], v[180:183], v[236:239], v[64:67]
	s_barrier
	s_add_i32 s28, s48, s50
	v_lshl_add_u64 v[216:217], v[216:217], 0, s[68:69]
	s_mov_b32 m0, s28
	ds_read_b128 v[194:197], v149 offset:49152
	ds_read_b128 v[198:201], v149 offset:50176
	ds_read_b128 v[202:205], v149 offset:51200
	ds_read_b128 v[206:209], v149 offset:52224
	ds_read_b128 v[224:227], v149 offset:53248
	ds_read_b128 v[228:231], v149 offset:54272
	ds_read_b128 v[232:235], v149 offset:55296
	ds_read_b128 v[236:239], v149 offset:56320
	global_load_lds_dwordx4 v[216:217], off
	v_lshl_add_u64 v[216:217], v[218:219], 0, s[68:69]
	s_add_i32 m0, s28, 0x2000
	v_lshl_add_u64 v[210:211], v[210:211], 0, s[74:75]
	s_add_i32 s28, s49, s50
	global_load_lds_dwordx4 v[216:217], off
	v_lshl_add_u64 v[216:217], v[210:211], 0, v[130:131]
	s_mov_b32 m0, s28
	v_lshl_add_u64 v[210:211], v[210:211], 0, v[134:135]
	global_load_lds_dwordx4 v[216:217], off
	s_add_i32 m0, s28, 0x2000
	s_nop 0
	global_load_lds_dwordx4 v[210:211], off
	v_lshl_add_u64 v[210:211], v[220:221], 0, s[68:69]
	s_mov_b32 m0, s58
	s_nop 0
	global_load_lds_dwordx4 v[210:211], off
	v_lshl_add_u64 v[210:211], v[240:241], 0, s[68:69]
	s_mov_b32 m0, s59
	s_nop 0
	global_load_lds_dwordx4 v[210:211], off
	s_waitcnt vmcnt(8)
	s_waitcnt lgkmcnt(0)
	s_barrier
	s_waitcnt lgkmcnt(0)
	v_mfma_f32_16x16x32_bf16 v[60:63], v[152:155], v[194:197], v[60:63]
	v_mfma_f32_16x16x32_bf16 v[52:55], v[160:163], v[194:197], v[52:55]
	v_mfma_f32_16x16x32_bf16 v[44:47], v[152:155], v[202:205], v[44:47]
	v_mfma_f32_16x16x32_bf16 v[36:39], v[160:163], v[202:205], v[36:39]
	v_mfma_f32_16x16x32_bf16 v[28:31], v[152:155], v[224:227], v[28:31]
	v_mfma_f32_16x16x32_bf16 v[20:23], v[160:163], v[224:227], v[20:23]
	v_mfma_f32_16x16x32_bf16 v[12:15], v[152:155], v[232:235], v[12:15]
	v_mfma_f32_16x16x32_bf16 v[4:7], v[160:163], v[232:235], v[4:7]
	v_mfma_f32_16x16x32_bf16 v[60:63], v[156:159], v[198:201], v[60:63]
	v_mfma_f32_16x16x32_bf16 v[52:55], v[164:167], v[198:201], v[52:55]
	v_mfma_f32_16x16x32_bf16 v[44:47], v[156:159], v[206:209], v[44:47]
	v_mfma_f32_16x16x32_bf16 v[36:39], v[164:167], v[206:209], v[36:39]
	v_mfma_f32_16x16x32_bf16 v[28:31], v[156:159], v[228:231], v[28:31]
	v_mfma_f32_16x16x32_bf16 v[20:23], v[164:167], v[228:231], v[20:23]
	v_mfma_f32_16x16x32_bf16 v[12:15], v[156:159], v[236:239], v[12:15]
	v_mfma_f32_16x16x32_bf16 v[4:7], v[164:167], v[236:239], v[4:7]
	v_mfma_f32_16x16x32_bf16 v[56:59], v[168:171], v[194:197], v[56:59]
	v_mfma_f32_16x16x32_bf16 v[48:51], v[176:179], v[194:197], v[48:51]
	v_mfma_f32_16x16x32_bf16 v[40:43], v[168:171], v[202:205], v[40:43]
	v_mfma_f32_16x16x32_bf16 v[32:35], v[176:179], v[202:205], v[32:35]
	v_mfma_f32_16x16x32_bf16 v[24:27], v[168:171], v[224:227], v[24:27]
	v_mfma_f32_16x16x32_bf16 v[16:19], v[176:179], v[224:227], v[16:19]
	v_mfma_f32_16x16x32_bf16 v[8:11], v[168:171], v[232:235], v[8:11]
	v_mfma_f32_16x16x32_bf16 v[0:3], v[176:179], v[232:235], v[0:3]
	v_mfma_f32_16x16x32_bf16 v[56:59], v[172:175], v[198:201], v[56:59]
	v_mfma_f32_16x16x32_bf16 v[48:51], v[180:183], v[198:201], v[48:51]
	v_mfma_f32_16x16x32_bf16 v[40:43], v[172:175], v[206:209], v[40:43]
	v_mfma_f32_16x16x32_bf16 v[32:35], v[180:183], v[206:209], v[32:35]
	v_mfma_f32_16x16x32_bf16 v[24:27], v[172:175], v[228:231], v[24:27]
	v_mfma_f32_16x16x32_bf16 v[16:19], v[180:183], v[228:231], v[16:19]
	v_mfma_f32_16x16x32_bf16 v[8:11], v[172:175], v[236:239], v[8:11]
	v_mfma_f32_16x16x32_bf16 v[0:3], v[180:183], v[236:239], v[0:3]
	s_barrier
	s_add_i32 s17, s17, 2
	s_add_u32 s24, s24, 0x100
	s_addc_u32 s25, s25, 0
	s_cmp_gt_u32 s17, 29
	v_lshl_add_u64 v[144:145], v[144:145], 0, s[76:77]
	s_cbranch_scc0 .LBB0_1419
	s_and_b64 vcc, exec, s[6:7]
	s_cbranch_vccz .LBB0_1422
	s_barrier

.LBB0_1491:
	s_add_u32 s14, s12, 0x100
	s_addc_u32 s15, s13, 0
	s_add_i32 s28, 0, 0x10000
	s_cmp_eq_u32 s59, 40
	s_cselect_b32 s17, s53, s15
	s_cselect_b32 s16, s58, s14
	s_cselect_b64 vcc, -1, 0
	s_add_i32 s29, 0, 0x14000
	v_add_u32_e32 v164, s28, v147
	v_add_u32_e32 v180, s29, v147
	ds_read_b128 v[152:155], v164
	ds_read_b128 v[156:159], v164 offset:1024
	ds_read_b128 v[160:163], v164 offset:2048
	ds_read_b128 v[164:167], v164 offset:3072
	ds_read_b128 v[168:171], v180
	ds_read_b128 v[172:175], v180 offset:1024
	ds_read_b128 v[176:179], v180 offset:2048
	ds_read_b128 v[180:183], v180 offset:3072
	v_cndmask_b32_e32 v211, v145, v150, vcc
	v_cndmask_b32_e32 v210, v144, v151, vcc
	v_lshl_add_u64 v[216:217], s[12:13], 0, v[136:137]
	s_add_i32 m0, s40, 0xc000
	ds_read_b128 v[194:197], v149
	ds_read_b128 v[198:201], v149 offset:1024
	ds_read_b128 v[202:205], v149 offset:2048
	ds_read_b128 v[206:209], v149 offset:3072
	ds_read_b128 v[224:227], v149 offset:4096
	ds_read_b128 v[228:231], v149 offset:5120
	ds_read_b128 v[232:235], v149 offset:6144
	ds_read_b128 v[236:239], v149 offset:7168
	global_load_lds_dwordx4 v[216:217], off
	v_lshl_add_u64 v[216:217], s[12:13], 0, v[138:139]
	s_add_i32 m0, s40, 0xe000
	s_nop 0
	global_load_lds_dwordx4 v[216:217], off
	s_waitcnt vmcnt(8)
	s_waitcnt lgkmcnt(0)
	s_barrier
	s_waitcnt lgkmcnt(0)
	v_mfma_f32_16x16x32_bf16 v[124:127], v[152:155], v[194:197], v[124:127]
	v_mfma_f32_16x16x32_bf16 v[120:123], v[160:163], v[194:197], v[120:123]
	v_mfma_f32_16x16x32_bf16 v[116:119], v[152:155], v[202:205], v[116:119]
	v_mfma_f32_16x16x32_bf16 v[108:111], v[160:163], v[202:205], v[108:111]
	v_mfma_f32_16x16x32_bf16 v[100:103], v[152:155], v[224:227], v[100:103]
	v_mfma_f32_16x16x32_bf16 v[92:95], v[160:163], v[224:227], v[92:95]
	v_mfma_f32_16x16x32_bf16 v[80:83], v[152:155], v[232:235], v[80:83]
	v_mfma_f32_16x16x32_bf16 v[72:75], v[160:163], v[232:235], v[72:75]
	v_mfma_f32_16x16x32_bf16 v[124:127], v[156:159], v[198:201], v[124:127]
	v_mfma_f32_16x16x32_bf16 v[120:123], v[164:167], v[198:201], v[120:123]
	v_mfma_f32_16x16x32_bf16 v[116:119], v[156:159], v[206:209], v[116:119]
	v_mfma_f32_16x16x32_bf16 v[108:111], v[164:167], v[206:209], v[108:111]
	v_mfma_f32_16x16x32_bf16 v[100:103], v[156:159], v[228:231], v[100:103]
	v_mfma_f32_16x16x32_bf16 v[92:95], v[164:167], v[228:231], v[92:95]
	v_mfma_f32_16x16x32_bf16 v[80:83], v[156:159], v[236:239], v[80:83]
	v_mfma_f32_16x16x32_bf16 v[72:75], v[164:167], v[236:239], v[72:75]
	v_mfma_f32_16x16x32_bf16 v[112:115], v[168:171], v[194:197], v[112:115]
	v_mfma_f32_16x16x32_bf16 v[104:107], v[176:179], v[194:197], v[104:107]
	v_mfma_f32_16x16x32_bf16 v[96:99], v[168:171], v[202:205], v[96:99]
	v_mfma_f32_16x16x32_bf16 v[88:91], v[176:179], v[202:205], v[88:91]
	v_mfma_f32_16x16x32_bf16 v[84:87], v[168:171], v[224:227], v[84:87]
	v_mfma_f32_16x16x32_bf16 v[76:79], v[176:179], v[224:227], v[76:79]
	v_mfma_f32_16x16x32_bf16 v[68:71], v[168:171], v[232:235], v[68:71]
	v_mfma_f32_16x16x32_bf16 v[64:67], v[176:179], v[232:235], v[64:67]
	v_mfma_f32_16x16x32_bf16 v[112:115], v[172:175], v[198:201], v[112:115]
	v_mfma_f32_16x16x32_bf16 v[104:107], v[180:183], v[198:201], v[104:107]
	v_mfma_f32_16x16x32_bf16 v[96:99], v[172:175], v[206:209], v[96:99]
	v_mfma_f32_16x16x32_bf16 v[88:91], v[180:183], v[206:209], v[88:91]
	v_mfma_f32_16x16x32_bf16 v[84:87], v[172:175], v[228:231], v[84:87]
	v_mfma_f32_16x16x32_bf16 v[76:79], v[180:183], v[228:231], v[76:79]
	v_mfma_f32_16x16x32_bf16 v[68:71], v[172:175], v[236:239], v[68:71]
	v_mfma_f32_16x16x32_bf16 v[64:67], v[180:183], v[236:239], v[64:67]
	s_barrier
	s_add_i32 s12, s28, s30
	v_lshl_add_u64 v[216:217], v[210:211], 0, v[132:133]
	s_mov_b32 m0, s12
	ds_read_b128 v[194:197], v149 offset:16384
	ds_read_b128 v[198:201], v149 offset:17408
	ds_read_b128 v[202:205], v149 offset:18432
	ds_read_b128 v[206:209], v149 offset:19456
	ds_read_b128 v[224:227], v149 offset:20480
	ds_read_b128 v[228:231], v149 offset:21504
	ds_read_b128 v[232:235], v149 offset:22528
	ds_read_b128 v[236:239], v149 offset:23552
	global_load_lds_dwordx4 v[216:217], off
	v_lshl_add_u64 v[218:219], v[210:211], 0, v[128:129]
	s_add_i32 m0, s12, 0x2000
	v_lshl_add_u64 v[220:221], v[210:211], 0, s[72:73]
	s_add_i32 s12, s29, s30
	global_load_lds_dwordx4 v[218:219], off
	v_lshl_add_u64 v[240:241], v[220:221], 0, v[132:133]
	s_mov_b32 m0, s12
	v_lshl_add_u64 v[220:221], v[220:221], 0, v[128:129]
	global_load_lds_dwordx4 v[240:241], off
	s_add_i32 m0, s12, 0x2000
	v_lshl_add_u64 v[240:241], s[16:17], 0, v[130:131]
	global_load_lds_dwordx4 v[220:221], off
	v_lshl_add_u64 v[220:221], s[16:17], 0, v[134:135]
	s_mov_b32 m0, s40
	s_nop 0
	global_load_lds_dwordx4 v[220:221], off
	s_mov_b32 m0, s41
	s_nop 0
	global_load_lds_dwordx4 v[240:241], off
	s_waitcnt vmcnt(8)
	s_waitcnt lgkmcnt(0)
	s_barrier
	s_waitcnt lgkmcnt(0)
	v_mfma_f32_16x16x32_bf16 v[60:63], v[152:155], v[194:197], v[60:63]
	v_mfma_f32_16x16x32_bf16 v[56:59], v[160:163], v[194:197], v[56:59]
	v_mfma_f32_16x16x32_bf16 v[52:55], v[152:155], v[202:205], v[52:55]
	v_mfma_f32_16x16x32_bf16 v[44:47], v[160:163], v[202:205], v[44:47]
	v_mfma_f32_16x16x32_bf16 v[36:39], v[152:155], v[224:227], v[36:39]
	v_mfma_f32_16x16x32_bf16 v[28:31], v[160:163], v[224:227], v[28:31]
	v_mfma_f32_16x16x32_bf16 v[20:23], v[152:155], v[232:235], v[20:23]
	v_mfma_f32_16x16x32_bf16 v[12:15], v[160:163], v[232:235], v[12:15]
	v_mfma_f32_16x16x32_bf16 v[60:63], v[156:159], v[198:201], v[60:63]
	v_mfma_f32_16x16x32_bf16 v[56:59], v[164:167], v[198:201], v[56:59]
	v_mfma_f32_16x16x32_bf16 v[52:55], v[156:159], v[206:209], v[52:55]
	v_mfma_f32_16x16x32_bf16 v[44:47], v[164:167], v[206:209], v[44:47]
	v_mfma_f32_16x16x32_bf16 v[36:39], v[156:159], v[228:231], v[36:39]
	v_mfma_f32_16x16x32_bf16 v[28:31], v[164:167], v[228:231], v[28:31]
	v_mfma_f32_16x16x32_bf16 v[20:23], v[156:159], v[236:239], v[20:23]
	v_mfma_f32_16x16x32_bf16 v[12:15], v[164:167], v[236:239], v[12:15]
	v_mfma_f32_16x16x32_bf16 v[48:51], v[168:171], v[194:197], v[48:51]
	v_mfma_f32_16x16x32_bf16 v[40:43], v[176:179], v[194:197], v[40:43]
	v_mfma_f32_16x16x32_bf16 v[32:35], v[168:171], v[202:205], v[32:35]
	v_mfma_f32_16x16x32_bf16 v[24:27], v[176:179], v[202:205], v[24:27]
	v_mfma_f32_16x16x32_bf16 v[16:19], v[168:171], v[224:227], v[16:19]
	v_mfma_f32_16x16x32_bf16 v[8:11], v[176:179], v[224:227], v[8:11]
	v_mfma_f32_16x16x32_bf16 v[4:7], v[168:171], v[232:235], v[4:7]
	v_mfma_f32_16x16x32_bf16 v[0:3], v[176:179], v[232:235], v[0:3]
	v_mfma_f32_16x16x32_bf16 v[48:51], v[172:175], v[198:201], v[48:51]
	v_mfma_f32_16x16x32_bf16 v[40:43], v[180:183], v[198:201], v[40:43]
	v_mfma_f32_16x16x32_bf16 v[32:35], v[172:175], v[206:209], v[32:35]
	v_mfma_f32_16x16x32_bf16 v[24:27], v[180:183], v[206:209], v[24:27]
	v_mfma_f32_16x16x32_bf16 v[16:19], v[172:175], v[228:231], v[16:19]
	v_mfma_f32_16x16x32_bf16 v[8:11], v[180:183], v[228:231], v[8:11]
	v_mfma_f32_16x16x32_bf16 v[4:7], v[172:175], v[236:239], v[4:7]
	v_mfma_f32_16x16x32_bf16 v[0:3], v[180:183], v[236:239], v[0:3]
	s_barrier
	s_add_i32 s28, 0, 0x18000
	s_add_i32 s29, 0, 0x1c000
	v_add_u32_e32 v164, s28, v147
	v_add_u32_e32 v180, s29, v147
	ds_read_b128 v[152:155], v164
	ds_read_b128 v[156:159], v164 offset:1024
	ds_read_b128 v[160:163], v164 offset:2048
	ds_read_b128 v[164:167], v164 offset:3072
	ds_read_b128 v[168:171], v180
	ds_read_b128 v[172:175], v180 offset:1024
	ds_read_b128 v[176:179], v180 offset:2048
	ds_read_b128 v[180:183], v180 offset:3072
	s_add_u32 s12, s16, 0xb0000
	s_addc_u32 s13, s17, 0
	s_mov_b32 m0, s42
	v_lshl_add_u64 v[242:243], s[12:13], 0, v[134:135]
	ds_read_b128 v[194:197], v149 offset:32768
	ds_read_b128 v[198:201], v149 offset:33792
	ds_read_b128 v[202:205], v149 offset:34816
	ds_read_b128 v[206:209], v149 offset:35840
	ds_read_b128 v[224:227], v149 offset:36864
	ds_read_b128 v[228:231], v149 offset:37888
	ds_read_b128 v[232:235], v149 offset:38912
	ds_read_b128 v[236:239], v149 offset:39936
	global_load_lds_dwordx4 v[242:243], off
	v_lshl_add_u64 v[242:243], s[12:13], 0, v[130:131]
	s_mov_b32 m0, s43
	s_nop 0
	global_load_lds_dwordx4 v[242:243], off
	s_waitcnt vmcnt(8)
	s_waitcnt lgkmcnt(0)
	s_barrier
	s_waitcnt lgkmcnt(0)
	v_mfma_f32_16x16x32_bf16 v[124:127], v[152:155], v[194:197], v[124:127]
	v_mfma_f32_16x16x32_bf16 v[120:123], v[160:163], v[194:197], v[120:123]
	v_mfma_f32_16x16x32_bf16 v[116:119], v[152:155], v[202:205], v[116:119]
	v_mfma_f32_16x16x32_bf16 v[108:111], v[160:163], v[202:205], v[108:111]
	v_mfma_f32_16x16x32_bf16 v[100:103], v[152:155], v[224:227], v[100:103]
	v_mfma_f32_16x16x32_bf16 v[92:95], v[160:163], v[224:227], v[92:95]
	v_mfma_f32_16x16x32_bf16 v[80:83], v[152:155], v[232:235], v[80:83]
	v_mfma_f32_16x16x32_bf16 v[72:75], v[160:163], v[232:235], v[72:75]
	v_mfma_f32_16x16x32_bf16 v[124:127], v[156:159], v[198:201], v[124:127]
	v_mfma_f32_16x16x32_bf16 v[120:123], v[164:167], v[198:201], v[120:123]
	v_mfma_f32_16x16x32_bf16 v[116:119], v[156:159], v[206:209], v[116:119]
	v_mfma_f32_16x16x32_bf16 v[108:111], v[164:167], v[206:209], v[108:111]
	v_mfma_f32_16x16x32_bf16 v[100:103], v[156:159], v[228:231], v[100:103]
	v_mfma_f32_16x16x32_bf16 v[92:95], v[164:167], v[228:231], v[92:95]
	v_mfma_f32_16x16x32_bf16 v[80:83], v[156:159], v[236:239], v[80:83]
	v_mfma_f32_16x16x32_bf16 v[72:75], v[164:167], v[236:239], v[72:75]
	v_mfma_f32_16x16x32_bf16 v[112:115], v[168:171], v[194:197], v[112:115]
	v_mfma_f32_16x16x32_bf16 v[104:107], v[176:179], v[194:197], v[104:107]
	v_mfma_f32_16x16x32_bf16 v[96:99], v[168:171], v[202:205], v[96:99]
	v_mfma_f32_16x16x32_bf16 v[88:91], v[176:179], v[202:205], v[88:91]
	v_mfma_f32_16x16x32_bf16 v[84:87], v[168:171], v[224:227], v[84:87]
	v_mfma_f32_16x16x32_bf16 v[76:79], v[176:179], v[224:227], v[76:79]
	v_mfma_f32_16x16x32_bf16 v[68:71], v[168:171], v[232:235], v[68:71]
	v_mfma_f32_16x16x32_bf16 v[64:67], v[176:179], v[232:235], v[64:67]
	v_mfma_f32_16x16x32_bf16 v[112:115], v[172:175], v[198:201], v[112:115]
	v_mfma_f32_16x16x32_bf16 v[104:107], v[180:183], v[198:201], v[104:107]
	v_mfma_f32_16x16x32_bf16 v[96:99], v[172:175], v[206:209], v[96:99]
	v_mfma_f32_16x16x32_bf16 v[88:91], v[180:183], v[206:209], v[88:91]
	v_mfma_f32_16x16x32_bf16 v[84:87], v[172:175], v[228:231], v[84:87]
	v_mfma_f32_16x16x32_bf16 v[76:79], v[180:183], v[228:231], v[76:79]
	v_mfma_f32_16x16x32_bf16 v[68:71], v[172:175], v[236:239], v[68:71]
	v_mfma_f32_16x16x32_bf16 v[64:67], v[180:183], v[236:239], v[64:67]
	s_barrier
	s_add_i32 s12, s28, s30
	v_lshl_add_u64 v[216:217], v[216:217], 0, s[68:69]
	s_mov_b32 m0, s12
	ds_read_b128 v[194:197], v149 offset:49152
	ds_read_b128 v[198:201], v149 offset:50176
	ds_read_b128 v[202:205], v149 offset:51200
	ds_read_b128 v[206:209], v149 offset:52224
	ds_read_b128 v[224:227], v149 offset:53248
	ds_read_b128 v[228:231], v149 offset:54272
	ds_read_b128 v[232:235], v149 offset:55296
	ds_read_b128 v[236:239], v149 offset:56320
	global_load_lds_dwordx4 v[216:217], off
	v_lshl_add_u64 v[216:217], v[218:219], 0, s[68:69]
	s_add_i32 m0, s12, 0x2000
	v_lshl_add_u64 v[210:211], v[210:211], 0, s[74:75]
	s_add_i32 s12, s29, s30
	global_load_lds_dwordx4 v[216:217], off
	v_lshl_add_u64 v[216:217], v[210:211], 0, v[132:133]
	s_mov_b32 m0, s12
	v_lshl_add_u64 v[210:211], v[210:211], 0, v[128:129]
	global_load_lds_dwordx4 v[216:217], off
	s_add_i32 m0, s12, 0x2000
	s_nop 0
	global_load_lds_dwordx4 v[210:211], off
	v_lshl_add_u64 v[210:211], v[220:221], 0, s[68:69]
	s_mov_b32 m0, s44
	s_nop 0
	global_load_lds_dwordx4 v[210:211], off
	v_lshl_add_u64 v[210:211], v[240:241], 0, s[68:69]
	s_mov_b32 m0, s45
	s_nop 0
	global_load_lds_dwordx4 v[210:211], off
	s_waitcnt vmcnt(8)
	s_waitcnt lgkmcnt(0)
	s_barrier
	s_waitcnt lgkmcnt(0)
	v_mfma_f32_16x16x32_bf16 v[60:63], v[152:155], v[194:197], v[60:63]
	v_mfma_f32_16x16x32_bf16 v[56:59], v[160:163], v[194:197], v[56:59]
	v_mfma_f32_16x16x32_bf16 v[52:55], v[152:155], v[202:205], v[52:55]
	v_mfma_f32_16x16x32_bf16 v[44:47], v[160:163], v[202:205], v[44:47]
	v_mfma_f32_16x16x32_bf16 v[36:39], v[152:155], v[224:227], v[36:39]
	v_mfma_f32_16x16x32_bf16 v[28:31], v[160:163], v[224:227], v[28:31]
	v_mfma_f32_16x16x32_bf16 v[20:23], v[152:155], v[232:235], v[20:23]
	v_mfma_f32_16x16x32_bf16 v[12:15], v[160:163], v[232:235], v[12:15]
	v_mfma_f32_16x16x32_bf16 v[60:63], v[156:159], v[198:201], v[60:63]
	v_mfma_f32_16x16x32_bf16 v[56:59], v[164:167], v[198:201], v[56:59]
	v_mfma_f32_16x16x32_bf16 v[52:55], v[156:159], v[206:209], v[52:55]
	v_mfma_f32_16x16x32_bf16 v[44:47], v[164:167], v[206:209], v[44:47]
	v_mfma_f32_16x16x32_bf16 v[36:39], v[156:159], v[228:231], v[36:39]
	v_mfma_f32_16x16x32_bf16 v[28:31], v[164:167], v[228:231], v[28:31]
	v_mfma_f32_16x16x32_bf16 v[20:23], v[156:159], v[236:239], v[20:23]
	v_mfma_f32_16x16x32_bf16 v[12:15], v[164:167], v[236:239], v[12:15]
	v_mfma_f32_16x16x32_bf16 v[48:51], v[168:171], v[194:197], v[48:51]
	v_mfma_f32_16x16x32_bf16 v[40:43], v[176:179], v[194:197], v[40:43]
	v_mfma_f32_16x16x32_bf16 v[32:35], v[168:171], v[202:205], v[32:35]
	v_mfma_f32_16x16x32_bf16 v[24:27], v[176:179], v[202:205], v[24:27]
	v_mfma_f32_16x16x32_bf16 v[16:19], v[168:171], v[224:227], v[16:19]
	v_mfma_f32_16x16x32_bf16 v[8:11], v[176:179], v[224:227], v[8:11]
	v_mfma_f32_16x16x32_bf16 v[4:7], v[168:171], v[232:235], v[4:7]
	v_mfma_f32_16x16x32_bf16 v[0:3], v[176:179], v[232:235], v[0:3]
	v_mfma_f32_16x16x32_bf16 v[48:51], v[172:175], v[198:201], v[48:51]
	v_mfma_f32_16x16x32_bf16 v[40:43], v[180:183], v[198:201], v[40:43]
	v_mfma_f32_16x16x32_bf16 v[32:35], v[172:175], v[206:209], v[32:35]
	v_mfma_f32_16x16x32_bf16 v[24:27], v[180:183], v[206:209], v[24:27]
	v_mfma_f32_16x16x32_bf16 v[16:19], v[172:175], v[228:231], v[16:19]
	v_mfma_f32_16x16x32_bf16 v[8:11], v[180:183], v[228:231], v[8:11]
	v_mfma_f32_16x16x32_bf16 v[4:7], v[172:175], v[236:239], v[4:7]
	v_mfma_f32_16x16x32_bf16 v[0:3], v[180:183], v[236:239], v[0:3]
	s_barrier
	s_add_i32 s59, s59, 2
	v_lshl_add_u64 v[144:145], v[144:145], 0, s[60:61]
	s_cmp_gt_u32 s59, 41
	s_mov_b64 s[12:13], s[14:15]
	s_cbranch_scc0 .LBB0_1491
	s_mov_b64 s[14:15], 0xb0000
	s_and_b64 vcc, exec, s[6:7]
	s_cbranch_vccz .LBB0_1494
	s_barrier

.LBB0_1587:
	s_add_u32 s28, s24, 0xfff80080
	s_addc_u32 s29, s25, -1
	s_add_i32 s48, 0, 0x10000
	s_cmp_eq_u32 s51, 28
	s_cselect_b32 s39, s9, s29
	s_cselect_b32 s38, s11, s28
	s_cselect_b32 s31, s45, s50
	s_cselect_b32 s30, s46, s47
	s_add_i32 s49, 0, 0x14000
	v_add_u32_e32 v154, s48, v139
	v_add_u32_e32 v170, s49, v139
	ds_read_b128 v[142:145], v154
	ds_read_b128 v[146:149], v154 offset:1024
	ds_read_b128 v[150:153], v154 offset:2048
	ds_read_b128 v[154:157], v154 offset:3072
	ds_read_b128 v[158:161], v170
	ds_read_b128 v[162:165], v170 offset:1024
	ds_read_b128 v[166:169], v170 offset:2048
	ds_read_b128 v[170:173], v170 offset:3072
	v_lshl_add_u64 v[182:183], s[24:25], 0, v[134:135]
	s_add_i32 m0, s20, 0xc000
	ds_read_b128 v[174:177], v141
	ds_read_b128 v[178:181], v141 offset:1024
	ds_read_b128 v[194:197], v141 offset:2048
	ds_read_b128 v[198:201], v141 offset:3072
	ds_read_b128 v[202:205], v141 offset:4096
	ds_read_b128 v[206:209], v141 offset:5120
	ds_read_b128 v[224:227], v141 offset:6144
	ds_read_b128 v[228:231], v141 offset:7168
	global_load_lds_dwordx4 v[182:183], off
	v_lshl_add_u64 v[182:183], s[24:25], 0, v[136:137]
	s_add_i32 m0, s20, 0xe000
	s_nop 0
	global_load_lds_dwordx4 v[182:183], off
	s_waitcnt vmcnt(8)
	s_waitcnt lgkmcnt(0)
	s_barrier
	s_waitcnt lgkmcnt(0)
	v_mfma_f32_16x16x32_bf16 v[124:127], v[142:145], v[174:177], v[124:127]
	v_mfma_f32_16x16x32_bf16 v[116:119], v[150:153], v[174:177], v[116:119]
	v_mfma_f32_16x16x32_bf16 v[108:111], v[142:145], v[194:197], v[108:111]
	v_mfma_f32_16x16x32_bf16 v[100:103], v[150:153], v[194:197], v[100:103]
	v_mfma_f32_16x16x32_bf16 v[92:95], v[142:145], v[202:205], v[92:95]
	v_mfma_f32_16x16x32_bf16 v[84:87], v[150:153], v[202:205], v[84:87]
	v_mfma_f32_16x16x32_bf16 v[76:79], v[142:145], v[224:227], v[76:79]
	v_mfma_f32_16x16x32_bf16 v[68:71], v[150:153], v[224:227], v[68:71]
	v_mfma_f32_16x16x32_bf16 v[124:127], v[146:149], v[178:181], v[124:127]
	v_mfma_f32_16x16x32_bf16 v[116:119], v[154:157], v[178:181], v[116:119]
	v_mfma_f32_16x16x32_bf16 v[108:111], v[146:149], v[198:201], v[108:111]
	v_mfma_f32_16x16x32_bf16 v[100:103], v[154:157], v[198:201], v[100:103]
	v_mfma_f32_16x16x32_bf16 v[92:95], v[146:149], v[206:209], v[92:95]
	v_mfma_f32_16x16x32_bf16 v[84:87], v[154:157], v[206:209], v[84:87]
	v_mfma_f32_16x16x32_bf16 v[76:79], v[146:149], v[228:231], v[76:79]
	v_mfma_f32_16x16x32_bf16 v[68:71], v[154:157], v[228:231], v[68:71]
	v_mfma_f32_16x16x32_bf16 v[120:123], v[158:161], v[174:177], v[120:123]
	v_mfma_f32_16x16x32_bf16 v[112:115], v[166:169], v[174:177], v[112:115]
	v_mfma_f32_16x16x32_bf16 v[104:107], v[158:161], v[194:197], v[104:107]
	v_mfma_f32_16x16x32_bf16 v[96:99], v[166:169], v[194:197], v[96:99]
	v_mfma_f32_16x16x32_bf16 v[88:91], v[158:161], v[202:205], v[88:91]
	v_mfma_f32_16x16x32_bf16 v[80:83], v[166:169], v[202:205], v[80:83]
	v_mfma_f32_16x16x32_bf16 v[72:75], v[158:161], v[224:227], v[72:75]
	v_mfma_f32_16x16x32_bf16 v[64:67], v[166:169], v[224:227], v[64:67]
	v_mfma_f32_16x16x32_bf16 v[120:123], v[162:165], v[178:181], v[120:123]
	v_mfma_f32_16x16x32_bf16 v[112:115], v[170:173], v[178:181], v[112:115]
	v_mfma_f32_16x16x32_bf16 v[104:107], v[162:165], v[198:201], v[104:107]
	v_mfma_f32_16x16x32_bf16 v[96:99], v[170:173], v[198:201], v[96:99]
	v_mfma_f32_16x16x32_bf16 v[88:91], v[162:165], v[206:209], v[88:91]
	v_mfma_f32_16x16x32_bf16 v[80:83], v[170:173], v[206:209], v[80:83]
	v_mfma_f32_16x16x32_bf16 v[72:75], v[162:165], v[228:231], v[72:75]
	v_mfma_f32_16x16x32_bf16 v[64:67], v[170:173], v[228:231], v[64:67]
	s_barrier
	s_add_i32 s28, s48, s4
	v_lshl_add_u64 v[182:183], s[30:31], 0, v[184:185]
	s_mov_b32 m0, s28
	ds_read_b128 v[174:177], v141 offset:16384
	ds_read_b128 v[178:181], v141 offset:17408
	ds_read_b128 v[194:197], v141 offset:18432
	ds_read_b128 v[198:201], v141 offset:19456
	ds_read_b128 v[202:205], v141 offset:20480
	ds_read_b128 v[206:209], v141 offset:21504
	ds_read_b128 v[224:227], v141 offset:22528
	ds_read_b128 v[228:231], v141 offset:23552
	global_load_lds_dwordx4 v[182:183], off
	s_add_i32 m0, s28, 0x2000
	s_add_u32 s28, s30, 0x80000
	v_lshl_add_u64 v[210:211], s[30:31], 0, v[128:129]
	s_addc_u32 s29, s31, 0
	s_add_i32 s48, s49, s4
	global_load_lds_dwordx4 v[210:211], off
	v_lshl_add_u64 v[216:217], s[28:29], 0, v[184:185]
	s_mov_b32 m0, s48
	v_lshl_add_u64 v[218:219], s[38:39], 0, v[130:131]
	global_load_lds_dwordx4 v[216:217], off
	v_lshl_add_u64 v[216:217], s[28:29], 0, v[128:129]
	s_add_i32 m0, s48, 0x2000
	s_nop 0
	global_load_lds_dwordx4 v[216:217], off
	v_lshl_add_u64 v[216:217], s[38:39], 0, v[132:133]
	s_mov_b32 m0, s20
	s_nop 0
	global_load_lds_dwordx4 v[216:217], off
	s_mov_b32 m0, s21
	s_nop 0
	global_load_lds_dwordx4 v[218:219], off
	s_waitcnt vmcnt(8)
	s_waitcnt lgkmcnt(0)
	s_barrier
	s_waitcnt lgkmcnt(0)
	v_mfma_f32_16x16x32_bf16 v[60:63], v[142:145], v[174:177], v[60:63]
	v_mfma_f32_16x16x32_bf16 v[52:55], v[150:153], v[174:177], v[52:55]
	v_mfma_f32_16x16x32_bf16 v[44:47], v[142:145], v[194:197], v[44:47]
	v_mfma_f32_16x16x32_bf16 v[36:39], v[150:153], v[194:197], v[36:39]
	v_mfma_f32_16x16x32_bf16 v[28:31], v[142:145], v[202:205], v[28:31]
	v_mfma_f32_16x16x32_bf16 v[20:23], v[150:153], v[202:205], v[20:23]
	v_mfma_f32_16x16x32_bf16 v[12:15], v[142:145], v[224:227], v[12:15]
	v_mfma_f32_16x16x32_bf16 v[4:7], v[150:153], v[224:227], v[4:7]
	v_mfma_f32_16x16x32_bf16 v[60:63], v[146:149], v[178:181], v[60:63]
	v_mfma_f32_16x16x32_bf16 v[52:55], v[154:157], v[178:181], v[52:55]
	v_mfma_f32_16x16x32_bf16 v[44:47], v[146:149], v[198:201], v[44:47]
	v_mfma_f32_16x16x32_bf16 v[36:39], v[154:157], v[198:201], v[36:39]
	v_mfma_f32_16x16x32_bf16 v[28:31], v[146:149], v[206:209], v[28:31]
	v_mfma_f32_16x16x32_bf16 v[20:23], v[154:157], v[206:209], v[20:23]
	v_mfma_f32_16x16x32_bf16 v[12:15], v[146:149], v[228:231], v[12:15]
	v_mfma_f32_16x16x32_bf16 v[4:7], v[154:157], v[228:231], v[4:7]
	v_mfma_f32_16x16x32_bf16 v[56:59], v[158:161], v[174:177], v[56:59]
	v_mfma_f32_16x16x32_bf16 v[48:51], v[166:169], v[174:177], v[48:51]
	v_mfma_f32_16x16x32_bf16 v[40:43], v[158:161], v[194:197], v[40:43]
	v_mfma_f32_16x16x32_bf16 v[32:35], v[166:169], v[194:197], v[32:35]
	v_mfma_f32_16x16x32_bf16 v[24:27], v[158:161], v[202:205], v[24:27]
	v_mfma_f32_16x16x32_bf16 v[16:19], v[166:169], v[202:205], v[16:19]
	v_mfma_f32_16x16x32_bf16 v[8:11], v[158:161], v[224:227], v[8:11]
	v_mfma_f32_16x16x32_bf16 v[0:3], v[166:169], v[224:227], v[0:3]
	v_mfma_f32_16x16x32_bf16 v[56:59], v[162:165], v[178:181], v[56:59]
	v_mfma_f32_16x16x32_bf16 v[48:51], v[170:173], v[178:181], v[48:51]
	v_mfma_f32_16x16x32_bf16 v[40:43], v[162:165], v[198:201], v[40:43]
	v_mfma_f32_16x16x32_bf16 v[32:35], v[170:173], v[198:201], v[32:35]
	v_mfma_f32_16x16x32_bf16 v[24:27], v[162:165], v[206:209], v[24:27]
	v_mfma_f32_16x16x32_bf16 v[16:19], v[170:173], v[206:209], v[16:19]
	v_mfma_f32_16x16x32_bf16 v[8:11], v[162:165], v[228:231], v[8:11]
	v_mfma_f32_16x16x32_bf16 v[0:3], v[170:173], v[228:231], v[0:3]
	s_barrier
	s_add_i32 s48, 0, 0x18000
	s_add_i32 s49, 0, 0x1c000
	v_add_u32_e32 v154, s48, v139
	v_add_u32_e32 v170, s49, v139
	ds_read_b128 v[142:145], v154
	ds_read_b128 v[146:149], v154 offset:1024
	ds_read_b128 v[150:153], v154 offset:2048
	ds_read_b128 v[154:157], v154 offset:3072
	ds_read_b128 v[158:161], v170
	ds_read_b128 v[162:165], v170 offset:1024
	ds_read_b128 v[166:169], v170 offset:2048
	ds_read_b128 v[170:173], v170 offset:3072
	s_add_u32 s28, s38, 0x80000
	s_addc_u32 s29, s39, 0
	s_mov_b32 m0, s26
	v_lshl_add_u64 v[232:233], s[28:29], 0, v[132:133]
	ds_read_b128 v[174:177], v141 offset:32768
	ds_read_b128 v[178:181], v141 offset:33792
	ds_read_b128 v[194:197], v141 offset:34816
	ds_read_b128 v[198:201], v141 offset:35840
	ds_read_b128 v[202:205], v141 offset:36864
	ds_read_b128 v[206:209], v141 offset:37888
	ds_read_b128 v[224:227], v141 offset:38912
	ds_read_b128 v[228:231], v141 offset:39936
	global_load_lds_dwordx4 v[232:233], off
	v_lshl_add_u64 v[232:233], s[28:29], 0, v[130:131]
	s_mov_b32 m0, s27
	s_nop 0
	global_load_lds_dwordx4 v[232:233], off
	s_waitcnt vmcnt(8)
	s_waitcnt lgkmcnt(0)
	s_barrier
	s_waitcnt lgkmcnt(0)
	v_mfma_f32_16x16x32_bf16 v[124:127], v[142:145], v[174:177], v[124:127]
	v_mfma_f32_16x16x32_bf16 v[116:119], v[150:153], v[174:177], v[116:119]
	v_mfma_f32_16x16x32_bf16 v[108:111], v[142:145], v[194:197], v[108:111]
	v_mfma_f32_16x16x32_bf16 v[100:103], v[150:153], v[194:197], v[100:103]
	v_mfma_f32_16x16x32_bf16 v[92:95], v[142:145], v[202:205], v[92:95]
	v_mfma_f32_16x16x32_bf16 v[84:87], v[150:153], v[202:205], v[84:87]
	v_mfma_f32_16x16x32_bf16 v[76:79], v[142:145], v[224:227], v[76:79]
	v_mfma_f32_16x16x32_bf16 v[68:71], v[150:153], v[224:227], v[68:71]
	v_mfma_f32_16x16x32_bf16 v[124:127], v[146:149], v[178:181], v[124:127]
	v_mfma_f32_16x16x32_bf16 v[116:119], v[154:157], v[178:181], v[116:119]
	v_mfma_f32_16x16x32_bf16 v[108:111], v[146:149], v[198:201], v[108:111]
	v_mfma_f32_16x16x32_bf16 v[100:103], v[154:157], v[198:201], v[100:103]
	v_mfma_f32_16x16x32_bf16 v[92:95], v[146:149], v[206:209], v[92:95]
	v_mfma_f32_16x16x32_bf16 v[84:87], v[154:157], v[206:209], v[84:87]
	v_mfma_f32_16x16x32_bf16 v[76:79], v[146:149], v[228:231], v[76:79]
	v_mfma_f32_16x16x32_bf16 v[68:71], v[154:157], v[228:231], v[68:71]
	v_mfma_f32_16x16x32_bf16 v[120:123], v[158:161], v[174:177], v[120:123]
	v_mfma_f32_16x16x32_bf16 v[112:115], v[166:169], v[174:177], v[112:115]
	v_mfma_f32_16x16x32_bf16 v[104:107], v[158:161], v[194:197], v[104:107]
	v_mfma_f32_16x16x32_bf16 v[96:99], v[166:169], v[194:197], v[96:99]
	v_mfma_f32_16x16x32_bf16 v[88:91], v[158:161], v[202:205], v[88:91]
	v_mfma_f32_16x16x32_bf16 v[80:83], v[166:169], v[202:205], v[80:83]
	v_mfma_f32_16x16x32_bf16 v[72:75], v[158:161], v[224:227], v[72:75]
	v_mfma_f32_16x16x32_bf16 v[64:67], v[166:169], v[224:227], v[64:67]
	v_mfma_f32_16x16x32_bf16 v[120:123], v[162:165], v[178:181], v[120:123]
	v_mfma_f32_16x16x32_bf16 v[112:115], v[170:173], v[178:181], v[112:115]
	v_mfma_f32_16x16x32_bf16 v[104:107], v[162:165], v[198:201], v[104:107]
	v_mfma_f32_16x16x32_bf16 v[96:99], v[170:173], v[198:201], v[96:99]
	v_mfma_f32_16x16x32_bf16 v[88:91], v[162:165], v[206:209], v[88:91]
	v_mfma_f32_16x16x32_bf16 v[80:83], v[170:173], v[206:209], v[80:83]
	v_mfma_f32_16x16x32_bf16 v[72:75], v[162:165], v[228:231], v[72:75]
	v_mfma_f32_16x16x32_bf16 v[64:67], v[170:173], v[228:231], v[64:67]
	s_barrier
	s_add_i32 s28, s48, s4
	v_lshl_add_u64 v[182:183], v[182:183], 0, s[68:69]
	s_mov_b32 m0, s28
	ds_read_b128 v[174:177], v141 offset:49152
	ds_read_b128 v[178:181], v141 offset:50176
	ds_read_b128 v[194:197], v141 offset:51200
	ds_read_b128 v[198:201], v141 offset:52224
	ds_read_b128 v[202:205], v141 offset:53248
	ds_read_b128 v[206:209], v141 offset:54272
	ds_read_b128 v[224:227], v141 offset:55296
	ds_read_b128 v[228:231], v141 offset:56320
	global_load_lds_dwordx4 v[182:183], off
	s_add_i32 m0, s28, 0x2000
	s_add_u32 s28, s30, 0x80080
	v_lshl_add_u64 v[182:183], v[210:211], 0, s[68:69]
	s_addc_u32 s29, s31, 0
	s_add_i32 s30, s49, s4
	global_load_lds_dwordx4 v[182:183], off
	v_lshl_add_u64 v[182:183], s[28:29], 0, v[184:185]
	s_mov_b32 m0, s30
	s_nop 0
	global_load_lds_dwordx4 v[182:183], off
	v_lshl_add_u64 v[182:183], s[28:29], 0, v[128:129]
	s_add_i32 m0, s30, 0x2000
	s_nop 0
	global_load_lds_dwordx4 v[182:183], off
	v_lshl_add_u64 v[182:183], v[216:217], 0, s[68:69]
	s_mov_b32 m0, s40
	s_nop 0
	global_load_lds_dwordx4 v[182:183], off
	v_lshl_add_u64 v[182:183], v[218:219], 0, s[68:69]
	s_mov_b32 m0, s41
	s_nop 0
	global_load_lds_dwordx4 v[182:183], off
	s_waitcnt vmcnt(8)
	s_waitcnt lgkmcnt(0)
	s_barrier
	s_waitcnt lgkmcnt(0)
	v_mfma_f32_16x16x32_bf16 v[60:63], v[142:145], v[174:177], v[60:63]
	v_mfma_f32_16x16x32_bf16 v[52:55], v[150:153], v[174:177], v[52:55]
	v_mfma_f32_16x16x32_bf16 v[44:47], v[142:145], v[194:197], v[44:47]
	v_mfma_f32_16x16x32_bf16 v[36:39], v[150:153], v[194:197], v[36:39]
	v_mfma_f32_16x16x32_bf16 v[28:31], v[142:145], v[202:205], v[28:31]
	v_mfma_f32_16x16x32_bf16 v[20:23], v[150:153], v[202:205], v[20:23]
	v_mfma_f32_16x16x32_bf16 v[12:15], v[142:145], v[224:227], v[12:15]
	v_mfma_f32_16x16x32_bf16 v[4:7], v[150:153], v[224:227], v[4:7]
	v_mfma_f32_16x16x32_bf16 v[60:63], v[146:149], v[178:181], v[60:63]
	v_mfma_f32_16x16x32_bf16 v[52:55], v[154:157], v[178:181], v[52:55]
	v_mfma_f32_16x16x32_bf16 v[44:47], v[146:149], v[198:201], v[44:47]
	v_mfma_f32_16x16x32_bf16 v[36:39], v[154:157], v[198:201], v[36:39]
	v_mfma_f32_16x16x32_bf16 v[28:31], v[146:149], v[206:209], v[28:31]
	v_mfma_f32_16x16x32_bf16 v[20:23], v[154:157], v[206:209], v[20:23]
	v_mfma_f32_16x16x32_bf16 v[12:15], v[146:149], v[228:231], v[12:15]
	v_mfma_f32_16x16x32_bf16 v[4:7], v[154:157], v[228:231], v[4:7]
	v_mfma_f32_16x16x32_bf16 v[56:59], v[158:161], v[174:177], v[56:59]
	v_mfma_f32_16x16x32_bf16 v[48:51], v[166:169], v[174:177], v[48:51]
	v_mfma_f32_16x16x32_bf16 v[40:43], v[158:161], v[194:197], v[40:43]
	v_mfma_f32_16x16x32_bf16 v[32:35], v[166:169], v[194:197], v[32:35]
	v_mfma_f32_16x16x32_bf16 v[24:27], v[158:161], v[202:205], v[24:27]
	v_mfma_f32_16x16x32_bf16 v[16:19], v[166:169], v[202:205], v[16:19]
	v_mfma_f32_16x16x32_bf16 v[8:11], v[158:161], v[224:227], v[8:11]
	v_mfma_f32_16x16x32_bf16 v[0:3], v[166:169], v[224:227], v[0:3]
	v_mfma_f32_16x16x32_bf16 v[56:59], v[162:165], v[178:181], v[56:59]
	v_mfma_f32_16x16x32_bf16 v[48:51], v[170:173], v[178:181], v[48:51]
	v_mfma_f32_16x16x32_bf16 v[40:43], v[162:165], v[198:201], v[40:43]
	v_mfma_f32_16x16x32_bf16 v[32:35], v[170:173], v[198:201], v[32:35]
	v_mfma_f32_16x16x32_bf16 v[24:27], v[162:165], v[206:209], v[24:27]
	v_mfma_f32_16x16x32_bf16 v[16:19], v[170:173], v[206:209], v[16:19]
	v_mfma_f32_16x16x32_bf16 v[8:11], v[162:165], v[228:231], v[8:11]
	v_mfma_f32_16x16x32_bf16 v[0:3], v[170:173], v[228:231], v[0:3]
	s_barrier
	s_add_i32 s51, s51, 2
	s_add_u32 s24, s24, 0x100
	s_addc_u32 s25, s25, 0
	s_add_u32 s47, s47, 0x100
	s_addc_u32 s50, s50, 0
	s_cmp_gt_u32 s51, 29
	s_cbranch_scc0 .LBB0_1587
	s_and_b64 vcc, exec, s[6:7]
	s_cbranch_vccz .LBB0_1590
	s_barrier

.LBB0_1661:
	s_add_u32 s24, s18, 0x100
	s_addc_u32 s25, s19, 0
	s_add_i32 s28, 0, 0x10000
	s_cmpk_eq_i32 s61, 0x54
	s_cselect_b32 s39, s51, s25
	s_cselect_b32 s38, s52, s24
	s_cselect_b32 s31, s53, s60
	s_cselect_b32 s30, s58, s59
	s_add_i32 s29, 0, 0x14000
	s_waitcnt vmcnt(0)
	v_add_u32_e32 v84, s28, v163
	v_add_u32_e32 v170, s29, v163
	ds_read_b128 v[64:67], v84
	ds_read_b128 v[68:71], v84 offset:1024
	ds_read_b128 v[80:83], v84 offset:2048
	ds_read_b128 v[84:87], v84 offset:3072
	ds_read_b128 v[154:157], v170
	ds_read_b128 v[158:161], v170 offset:1024
	ds_read_b128 v[166:169], v170 offset:2048
	ds_read_b128 v[170:173], v170 offset:3072
	v_lshl_add_u64 v[182:183], s[18:19], 0, v[150:151]
	s_add_i32 m0, s20, 0xc000
	ds_read_b128 v[174:177], v165
	ds_read_b128 v[178:181], v165 offset:1024
	ds_read_b128 v[194:197], v165 offset:2048
	ds_read_b128 v[198:201], v165 offset:3072
	ds_read_b128 v[202:205], v165 offset:4096
	ds_read_b128 v[206:209], v165 offset:5120
	ds_read_b128 v[224:227], v165 offset:6144
	ds_read_b128 v[228:231], v165 offset:7168
	global_load_lds_dwordx4 v[182:183], off
	v_lshl_add_u64 v[182:183], s[18:19], 0, v[152:153]
	s_add_i32 m0, s20, 0xe000
	s_nop 0
	global_load_lds_dwordx4 v[182:183], off
	s_waitcnt vmcnt(8)
	s_waitcnt lgkmcnt(0)
	s_barrier
	s_waitcnt lgkmcnt(0)
	v_mfma_f32_16x16x32_bf16 v[140:143], v[64:67], v[174:177], v[140:143]
	v_mfma_f32_16x16x32_bf16 v[136:139], v[80:83], v[174:177], v[136:139]
	v_mfma_f32_16x16x32_bf16 v[124:127], v[64:67], v[194:197], v[124:127]
	v_mfma_f32_16x16x32_bf16 v[120:123], v[80:83], v[194:197], v[120:123]
	v_mfma_f32_16x16x32_bf16 v[108:111], v[64:67], v[202:205], v[108:111]
	v_mfma_f32_16x16x32_bf16 v[104:107], v[80:83], v[202:205], v[104:107]
	v_mfma_f32_16x16x32_bf16 v[92:95], v[64:67], v[224:227], v[92:95]
	v_mfma_f32_16x16x32_bf16 v[88:91], v[80:83], v[224:227], v[88:91]
	v_mfma_f32_16x16x32_bf16 v[140:143], v[68:71], v[178:181], v[140:143]
	v_mfma_f32_16x16x32_bf16 v[136:139], v[84:87], v[178:181], v[136:139]
	v_mfma_f32_16x16x32_bf16 v[124:127], v[68:71], v[198:201], v[124:127]
	v_mfma_f32_16x16x32_bf16 v[120:123], v[84:87], v[198:201], v[120:123]
	v_mfma_f32_16x16x32_bf16 v[108:111], v[68:71], v[206:209], v[108:111]
	v_mfma_f32_16x16x32_bf16 v[104:107], v[84:87], v[206:209], v[104:107]
	v_mfma_f32_16x16x32_bf16 v[92:95], v[68:71], v[228:231], v[92:95]
	v_mfma_f32_16x16x32_bf16 v[88:91], v[84:87], v[228:231], v[88:91]
	v_mfma_f32_16x16x32_bf16 v[132:135], v[154:157], v[174:177], v[132:135]
	v_mfma_f32_16x16x32_bf16 v[128:131], v[166:169], v[174:177], v[128:131]
	v_mfma_f32_16x16x32_bf16 v[116:119], v[154:157], v[194:197], v[116:119]
	v_mfma_f32_16x16x32_bf16 v[112:115], v[166:169], v[194:197], v[112:115]
	v_mfma_f32_16x16x32_bf16 v[100:103], v[154:157], v[202:205], v[100:103]
	v_mfma_f32_16x16x32_bf16 v[96:99], v[166:169], v[202:205], v[96:99]
	v_mfma_f32_16x16x32_bf16 v[76:79], v[154:157], v[224:227], v[76:79]
	v_mfma_f32_16x16x32_bf16 v[72:75], v[166:169], v[224:227], v[72:75]
	v_mfma_f32_16x16x32_bf16 v[132:135], v[158:161], v[178:181], v[132:135]
	v_mfma_f32_16x16x32_bf16 v[128:131], v[170:173], v[178:181], v[128:131]
	v_mfma_f32_16x16x32_bf16 v[116:119], v[158:161], v[198:201], v[116:119]
	v_mfma_f32_16x16x32_bf16 v[112:115], v[170:173], v[198:201], v[112:115]
	v_mfma_f32_16x16x32_bf16 v[100:103], v[158:161], v[206:209], v[100:103]
	v_mfma_f32_16x16x32_bf16 v[96:99], v[170:173], v[206:209], v[96:99]
	v_mfma_f32_16x16x32_bf16 v[76:79], v[158:161], v[228:231], v[76:79]
	v_mfma_f32_16x16x32_bf16 v[72:75], v[170:173], v[228:231], v[72:75]
	s_barrier
	s_add_i32 s18, s28, s4
	v_lshl_add_u64 v[182:183], s[30:31], 0, v[184:185]
	s_mov_b32 m0, s18
	ds_read_b128 v[174:177], v165 offset:16384
	ds_read_b128 v[178:181], v165 offset:17408
	ds_read_b128 v[194:197], v165 offset:18432
	ds_read_b128 v[198:201], v165 offset:19456
	ds_read_b128 v[202:205], v165 offset:20480
	ds_read_b128 v[206:209], v165 offset:21504
	ds_read_b128 v[224:227], v165 offset:22528
	ds_read_b128 v[228:231], v165 offset:23552
	global_load_lds_dwordx4 v[182:183], off
	s_add_i32 m0, s18, 0x2000
	s_add_u32 s18, s30, 0x160000
	v_lshl_add_u64 v[210:211], s[30:31], 0, v[144:145]
	s_addc_u32 s19, s31, 0
	s_add_i32 s28, s29, s4
	global_load_lds_dwordx4 v[210:211], off
	v_lshl_add_u64 v[216:217], s[18:19], 0, v[184:185]
	s_mov_b32 m0, s28
	v_lshl_add_u64 v[218:219], s[38:39], 0, v[146:147]
	global_load_lds_dwordx4 v[216:217], off
	v_lshl_add_u64 v[216:217], s[18:19], 0, v[144:145]
	s_add_i32 m0, s28, 0x2000
	s_nop 0
	global_load_lds_dwordx4 v[216:217], off
	v_lshl_add_u64 v[216:217], s[38:39], 0, v[148:149]
	s_mov_b32 m0, s20
	s_nop 0
	global_load_lds_dwordx4 v[216:217], off
	s_mov_b32 m0, s21
	s_nop 0
	global_load_lds_dwordx4 v[218:219], off
	s_waitcnt vmcnt(8)
	s_waitcnt lgkmcnt(0)
	s_barrier
	s_waitcnt lgkmcnt(0)
	v_mfma_f32_16x16x32_bf16 v[60:63], v[64:67], v[174:177], v[60:63]
	v_mfma_f32_16x16x32_bf16 v[56:59], v[80:83], v[174:177], v[56:59]
	v_mfma_f32_16x16x32_bf16 v[44:47], v[64:67], v[194:197], v[44:47]
	v_mfma_f32_16x16x32_bf16 v[40:43], v[80:83], v[194:197], v[40:43]
	v_mfma_f32_16x16x32_bf16 v[28:31], v[64:67], v[202:205], v[28:31]
	v_mfma_f32_16x16x32_bf16 v[24:27], v[80:83], v[202:205], v[24:27]
	v_mfma_f32_16x16x32_bf16 v[12:15], v[64:67], v[224:227], v[12:15]
	v_mfma_f32_16x16x32_bf16 v[8:11], v[80:83], v[224:227], v[8:11]
	v_mfma_f32_16x16x32_bf16 v[60:63], v[68:71], v[178:181], v[60:63]
	v_mfma_f32_16x16x32_bf16 v[56:59], v[84:87], v[178:181], v[56:59]
	v_mfma_f32_16x16x32_bf16 v[44:47], v[68:71], v[198:201], v[44:47]
	v_mfma_f32_16x16x32_bf16 v[40:43], v[84:87], v[198:201], v[40:43]
	v_mfma_f32_16x16x32_bf16 v[28:31], v[68:71], v[206:209], v[28:31]
	v_mfma_f32_16x16x32_bf16 v[24:27], v[84:87], v[206:209], v[24:27]
	v_mfma_f32_16x16x32_bf16 v[12:15], v[68:71], v[228:231], v[12:15]
	v_mfma_f32_16x16x32_bf16 v[8:11], v[84:87], v[228:231], v[8:11]
	v_mfma_f32_16x16x32_bf16 v[52:55], v[154:157], v[174:177], v[52:55]
	v_mfma_f32_16x16x32_bf16 v[48:51], v[166:169], v[174:177], v[48:51]
	v_mfma_f32_16x16x32_bf16 v[36:39], v[154:157], v[194:197], v[36:39]
	v_mfma_f32_16x16x32_bf16 v[32:35], v[166:169], v[194:197], v[32:35]
	v_mfma_f32_16x16x32_bf16 v[20:23], v[154:157], v[202:205], v[20:23]
	v_mfma_f32_16x16x32_bf16 v[16:19], v[166:169], v[202:205], v[16:19]
	v_mfma_f32_16x16x32_bf16 v[4:7], v[154:157], v[224:227], v[4:7]
	v_mfma_f32_16x16x32_bf16 v[0:3], v[166:169], v[224:227], v[0:3]
	v_mfma_f32_16x16x32_bf16 v[52:55], v[158:161], v[178:181], v[52:55]
	v_mfma_f32_16x16x32_bf16 v[48:51], v[170:173], v[178:181], v[48:51]
	v_mfma_f32_16x16x32_bf16 v[36:39], v[158:161], v[198:201], v[36:39]
	v_mfma_f32_16x16x32_bf16 v[32:35], v[170:173], v[198:201], v[32:35]
	v_mfma_f32_16x16x32_bf16 v[20:23], v[158:161], v[206:209], v[20:23]
	v_mfma_f32_16x16x32_bf16 v[16:19], v[170:173], v[206:209], v[16:19]
	v_mfma_f32_16x16x32_bf16 v[4:7], v[158:161], v[228:231], v[4:7]
	v_mfma_f32_16x16x32_bf16 v[0:3], v[170:173], v[228:231], v[0:3]
	s_barrier
	s_add_i32 s28, 0, 0x18000
	s_add_i32 s29, 0, 0x1c000
	v_add_u32_e32 v84, s28, v163
	v_add_u32_e32 v170, s29, v163
	ds_read_b128 v[64:67], v84
	ds_read_b128 v[68:71], v84 offset:1024
	ds_read_b128 v[80:83], v84 offset:2048
	ds_read_b128 v[84:87], v84 offset:3072
	ds_read_b128 v[154:157], v170
	ds_read_b128 v[158:161], v170 offset:1024
	ds_read_b128 v[166:169], v170 offset:2048
	ds_read_b128 v[170:173], v170 offset:3072
	s_add_u32 s18, s38, 0x160000
	s_addc_u32 s19, s39, 0
	s_mov_b32 m0, s26
	v_lshl_add_u64 v[232:233], s[18:19], 0, v[148:149]
	ds_read_b128 v[174:177], v165 offset:32768
	ds_read_b128 v[178:181], v165 offset:33792
	ds_read_b128 v[194:197], v165 offset:34816
	ds_read_b128 v[198:201], v165 offset:35840
	ds_read_b128 v[202:205], v165 offset:36864
	ds_read_b128 v[206:209], v165 offset:37888
	ds_read_b128 v[224:227], v165 offset:38912
	ds_read_b128 v[228:231], v165 offset:39936
	global_load_lds_dwordx4 v[232:233], off
	v_lshl_add_u64 v[232:233], s[18:19], 0, v[146:147]
	s_mov_b32 m0, s27
	s_nop 0
	global_load_lds_dwordx4 v[232:233], off
	s_waitcnt vmcnt(8)
	s_waitcnt lgkmcnt(0)
	s_barrier
	s_waitcnt lgkmcnt(0)
	v_mfma_f32_16x16x32_bf16 v[140:143], v[64:67], v[174:177], v[140:143]
	v_mfma_f32_16x16x32_bf16 v[136:139], v[80:83], v[174:177], v[136:139]
	v_mfma_f32_16x16x32_bf16 v[124:127], v[64:67], v[194:197], v[124:127]
	v_mfma_f32_16x16x32_bf16 v[120:123], v[80:83], v[194:197], v[120:123]
	v_mfma_f32_16x16x32_bf16 v[108:111], v[64:67], v[202:205], v[108:111]
	v_mfma_f32_16x16x32_bf16 v[104:107], v[80:83], v[202:205], v[104:107]
	v_mfma_f32_16x16x32_bf16 v[92:95], v[64:67], v[224:227], v[92:95]
	v_mfma_f32_16x16x32_bf16 v[88:91], v[80:83], v[224:227], v[88:91]
	v_mfma_f32_16x16x32_bf16 v[140:143], v[68:71], v[178:181], v[140:143]
	v_mfma_f32_16x16x32_bf16 v[136:139], v[84:87], v[178:181], v[136:139]
	v_mfma_f32_16x16x32_bf16 v[124:127], v[68:71], v[198:201], v[124:127]
	v_mfma_f32_16x16x32_bf16 v[120:123], v[84:87], v[198:201], v[120:123]
	v_mfma_f32_16x16x32_bf16 v[108:111], v[68:71], v[206:209], v[108:111]
	v_mfma_f32_16x16x32_bf16 v[104:107], v[84:87], v[206:209], v[104:107]
	v_mfma_f32_16x16x32_bf16 v[92:95], v[68:71], v[228:231], v[92:95]
	v_mfma_f32_16x16x32_bf16 v[88:91], v[84:87], v[228:231], v[88:91]
	v_mfma_f32_16x16x32_bf16 v[132:135], v[154:157], v[174:177], v[132:135]
	v_mfma_f32_16x16x32_bf16 v[128:131], v[166:169], v[174:177], v[128:131]
	v_mfma_f32_16x16x32_bf16 v[116:119], v[154:157], v[194:197], v[116:119]
	v_mfma_f32_16x16x32_bf16 v[112:115], v[166:169], v[194:197], v[112:115]
	v_mfma_f32_16x16x32_bf16 v[100:103], v[154:157], v[202:205], v[100:103]
	v_mfma_f32_16x16x32_bf16 v[96:99], v[166:169], v[202:205], v[96:99]
	v_mfma_f32_16x16x32_bf16 v[76:79], v[154:157], v[224:227], v[76:79]
	v_mfma_f32_16x16x32_bf16 v[72:75], v[166:169], v[224:227], v[72:75]
	v_mfma_f32_16x16x32_bf16 v[132:135], v[158:161], v[178:181], v[132:135]
	v_mfma_f32_16x16x32_bf16 v[128:131], v[170:173], v[178:181], v[128:131]
	v_mfma_f32_16x16x32_bf16 v[116:119], v[158:161], v[198:201], v[116:119]
	v_mfma_f32_16x16x32_bf16 v[112:115], v[170:173], v[198:201], v[112:115]
	v_mfma_f32_16x16x32_bf16 v[100:103], v[158:161], v[206:209], v[100:103]
	v_mfma_f32_16x16x32_bf16 v[96:99], v[170:173], v[206:209], v[96:99]
	v_mfma_f32_16x16x32_bf16 v[76:79], v[158:161], v[228:231], v[76:79]
	v_mfma_f32_16x16x32_bf16 v[72:75], v[170:173], v[228:231], v[72:75]
	s_barrier
	s_add_i32 s18, s28, s4
	v_lshl_add_u64 v[182:183], v[182:183], 0, s[68:69]
	s_mov_b32 m0, s18
	ds_read_b128 v[174:177], v165 offset:49152
	ds_read_b128 v[178:181], v165 offset:50176
	ds_read_b128 v[194:197], v165 offset:51200
	ds_read_b128 v[198:201], v165 offset:52224
	ds_read_b128 v[202:205], v165 offset:53248
	ds_read_b128 v[206:209], v165 offset:54272
	ds_read_b128 v[224:227], v165 offset:55296
	ds_read_b128 v[228:231], v165 offset:56320
	global_load_lds_dwordx4 v[182:183], off
	s_add_i32 m0, s18, 0x2000
	s_add_u32 s18, s30, 0x160080
	v_lshl_add_u64 v[182:183], v[210:211], 0, s[68:69]
	s_addc_u32 s19, s31, 0
	s_add_i32 s28, s29, s4
	global_load_lds_dwordx4 v[182:183], off
	v_lshl_add_u64 v[182:183], s[18:19], 0, v[184:185]
	s_mov_b32 m0, s28
	s_nop 0
	global_load_lds_dwordx4 v[182:183], off
	v_lshl_add_u64 v[182:183], s[18:19], 0, v[144:145]
	s_add_i32 m0, s28, 0x2000
	s_nop 0
	global_load_lds_dwordx4 v[182:183], off
	v_lshl_add_u64 v[182:183], v[216:217], 0, s[68:69]
	s_mov_b32 m0, s42
	s_nop 0
	global_load_lds_dwordx4 v[182:183], off
	v_lshl_add_u64 v[182:183], v[218:219], 0, s[68:69]
	s_mov_b32 m0, s43
	s_nop 0
	global_load_lds_dwordx4 v[182:183], off
	s_waitcnt vmcnt(8)
	s_waitcnt lgkmcnt(0)
	s_barrier
	s_waitcnt lgkmcnt(0)
	v_mfma_f32_16x16x32_bf16 v[60:63], v[64:67], v[174:177], v[60:63]
	v_mfma_f32_16x16x32_bf16 v[56:59], v[80:83], v[174:177], v[56:59]
	v_mfma_f32_16x16x32_bf16 v[44:47], v[64:67], v[194:197], v[44:47]
	v_mfma_f32_16x16x32_bf16 v[40:43], v[80:83], v[194:197], v[40:43]
	v_mfma_f32_16x16x32_bf16 v[28:31], v[64:67], v[202:205], v[28:31]
	v_mfma_f32_16x16x32_bf16 v[24:27], v[80:83], v[202:205], v[24:27]
	v_mfma_f32_16x16x32_bf16 v[12:15], v[64:67], v[224:227], v[12:15]
	v_mfma_f32_16x16x32_bf16 v[8:11], v[80:83], v[224:227], v[8:11]
	v_mfma_f32_16x16x32_bf16 v[60:63], v[68:71], v[178:181], v[60:63]
	v_mfma_f32_16x16x32_bf16 v[56:59], v[84:87], v[178:181], v[56:59]
	v_mfma_f32_16x16x32_bf16 v[44:47], v[68:71], v[198:201], v[44:47]
	v_mfma_f32_16x16x32_bf16 v[40:43], v[84:87], v[198:201], v[40:43]
	v_mfma_f32_16x16x32_bf16 v[28:31], v[68:71], v[206:209], v[28:31]
	v_mfma_f32_16x16x32_bf16 v[24:27], v[84:87], v[206:209], v[24:27]
	v_mfma_f32_16x16x32_bf16 v[12:15], v[68:71], v[228:231], v[12:15]
	v_mfma_f32_16x16x32_bf16 v[8:11], v[84:87], v[228:231], v[8:11]
	v_mfma_f32_16x16x32_bf16 v[52:55], v[154:157], v[174:177], v[52:55]
	v_mfma_f32_16x16x32_bf16 v[48:51], v[166:169], v[174:177], v[48:51]
	v_mfma_f32_16x16x32_bf16 v[36:39], v[154:157], v[194:197], v[36:39]
	v_mfma_f32_16x16x32_bf16 v[32:35], v[166:169], v[194:197], v[32:35]
	v_mfma_f32_16x16x32_bf16 v[20:23], v[154:157], v[202:205], v[20:23]
	v_mfma_f32_16x16x32_bf16 v[16:19], v[166:169], v[202:205], v[16:19]
	v_mfma_f32_16x16x32_bf16 v[4:7], v[154:157], v[224:227], v[4:7]
	v_mfma_f32_16x16x32_bf16 v[0:3], v[166:169], v[224:227], v[0:3]
	v_mfma_f32_16x16x32_bf16 v[52:55], v[158:161], v[178:181], v[52:55]
	v_mfma_f32_16x16x32_bf16 v[48:51], v[170:173], v[178:181], v[48:51]
	v_mfma_f32_16x16x32_bf16 v[36:39], v[158:161], v[198:201], v[36:39]
	v_mfma_f32_16x16x32_bf16 v[32:35], v[170:173], v[198:201], v[32:35]
	v_mfma_f32_16x16x32_bf16 v[20:23], v[158:161], v[206:209], v[20:23]
	v_mfma_f32_16x16x32_bf16 v[16:19], v[170:173], v[206:209], v[16:19]
	v_mfma_f32_16x16x32_bf16 v[4:7], v[158:161], v[228:231], v[4:7]
	v_mfma_f32_16x16x32_bf16 v[0:3], v[170:173], v[228:231], v[0:3]
	s_barrier
	s_add_i32 s61, s61, 2
	s_add_u32 s59, s59, 0x100
	s_addc_u32 s60, s60, 0
	s_cmpk_gt_u32 s61, 0x55
	s_mov_b64 s[18:19], s[24:25]
	s_cbranch_scc0 .LBB0_1661
	s_and_b64 vcc, exec, s[8:9]
	s_cbranch_vccz .LBB0_1664
	s_barrier

.LBB0_1741:
	s_add_u32 s38, s36, 0x100
	s_addc_u32 s39, s37, 0
	s_add_i32 s28, 0, 0x10000
	s_cmp_eq_u32 s59, 4
	s_cselect_b32 s43, s11, s39
	s_cselect_b32 s42, s50, s38
	s_cselect_b32 s41, s51, s58
	s_cselect_b32 s40, s52, s53
	s_add_i32 s48, 0, 0x14000
	v_add_u32_e32 v124, s28, v172
	v_add_u32_e32 v170, s48, v172
	ds_read_b128 v[112:115], v124
	ds_read_b128 v[116:119], v124 offset:1024
	ds_read_b128 v[120:123], v124 offset:2048
	ds_read_b128 v[124:127], v124 offset:3072
	ds_read_b128 v[176:179], v170
	ds_read_b128 v[180:183], v170 offset:1024
	ds_read_b128 v[194:197], v170 offset:2048
	ds_read_b128 v[198:201], v170 offset:3072
	v_lshl_add_u64 v[170:171], s[36:37], 0, v[166:167]
	s_add_i32 m0, s20, 0xc000
	ds_read_b128 v[202:205], v174
	ds_read_b128 v[206:209], v174 offset:1024
	ds_read_b128 v[224:227], v174 offset:2048
	ds_read_b128 v[228:231], v174 offset:3072
	ds_read_b128 v[232:235], v174 offset:4096
	ds_read_b128 v[236:239], v174 offset:5120
	ds_read_b128 v[240:243], v174 offset:6144
	ds_read_b128 v[244:247], v174 offset:7168
	global_load_lds_dwordx4 v[170:171], off
	v_lshl_add_u64 v[170:171], s[36:37], 0, v[168:169]
	s_add_i32 m0, s20, 0xe000
	s_nop 0
	global_load_lds_dwordx4 v[170:171], off
	s_waitcnt vmcnt(8)
	s_waitcnt lgkmcnt(0)
	s_barrier
	s_waitcnt lgkmcnt(0)
	v_mfma_f32_16x16x32_bf16 v[140:143], v[112:115], v[202:205], v[140:143]
	v_mfma_f32_16x16x32_bf16 v[136:139], v[120:123], v[202:205], v[136:139]
	v_mfma_f32_16x16x32_bf16 v[108:111], v[112:115], v[224:227], v[108:111]
	v_mfma_f32_16x16x32_bf16 v[104:107], v[120:123], v[224:227], v[104:107]
	v_mfma_f32_16x16x32_bf16 v[92:95], v[112:115], v[232:235], v[92:95]
	v_mfma_f32_16x16x32_bf16 v[88:91], v[120:123], v[232:235], v[88:91]
	v_mfma_f32_16x16x32_bf16 v[76:79], v[112:115], v[240:243], v[76:79]
	v_mfma_f32_16x16x32_bf16 v[72:75], v[120:123], v[240:243], v[72:75]
	v_mfma_f32_16x16x32_bf16 v[140:143], v[116:119], v[206:209], v[140:143]
	v_mfma_f32_16x16x32_bf16 v[136:139], v[124:127], v[206:209], v[136:139]
	v_mfma_f32_16x16x32_bf16 v[108:111], v[116:119], v[228:231], v[108:111]
	v_mfma_f32_16x16x32_bf16 v[104:107], v[124:127], v[228:231], v[104:107]
	v_mfma_f32_16x16x32_bf16 v[92:95], v[116:119], v[236:239], v[92:95]
	v_mfma_f32_16x16x32_bf16 v[88:91], v[124:127], v[236:239], v[88:91]
	v_mfma_f32_16x16x32_bf16 v[76:79], v[116:119], v[244:247], v[76:79]
	v_mfma_f32_16x16x32_bf16 v[72:75], v[124:127], v[244:247], v[72:75]
	v_mfma_f32_16x16x32_bf16 v[132:135], v[176:179], v[202:205], v[132:135]
	v_mfma_f32_16x16x32_bf16 v[128:131], v[194:197], v[202:205], v[128:131]
	v_mfma_f32_16x16x32_bf16 v[100:103], v[176:179], v[224:227], v[100:103]
	v_mfma_f32_16x16x32_bf16 v[96:99], v[194:197], v[224:227], v[96:99]
	v_mfma_f32_16x16x32_bf16 v[84:87], v[176:179], v[232:235], v[84:87]
	v_mfma_f32_16x16x32_bf16 v[80:83], v[194:197], v[232:235], v[80:83]
	v_mfma_f32_16x16x32_bf16 v[68:71], v[176:179], v[240:243], v[68:71]
	v_mfma_f32_16x16x32_bf16 v[64:67], v[194:197], v[240:243], v[64:67]
	v_mfma_f32_16x16x32_bf16 v[132:135], v[180:183], v[206:209], v[132:135]
	v_mfma_f32_16x16x32_bf16 v[128:131], v[198:201], v[206:209], v[128:131]
	v_mfma_f32_16x16x32_bf16 v[100:103], v[180:183], v[228:231], v[100:103]
	v_mfma_f32_16x16x32_bf16 v[96:99], v[198:201], v[228:231], v[96:99]
	v_mfma_f32_16x16x32_bf16 v[84:87], v[180:183], v[236:239], v[84:87]
	v_mfma_f32_16x16x32_bf16 v[80:83], v[198:201], v[236:239], v[80:83]
	v_mfma_f32_16x16x32_bf16 v[68:71], v[180:183], v[244:247], v[68:71]
	v_mfma_f32_16x16x32_bf16 v[64:67], v[198:201], v[244:247], v[64:67]
	s_barrier
	s_add_i32 s28, s28, s4
	v_lshl_add_u64 v[170:171], s[40:41], 0, v[184:185]
	s_mov_b32 m0, s28
	ds_read_b128 v[202:205], v174 offset:16384
	ds_read_b128 v[206:209], v174 offset:17408
	ds_read_b128 v[224:227], v174 offset:18432
	ds_read_b128 v[228:231], v174 offset:19456
	ds_read_b128 v[232:235], v174 offset:20480
	ds_read_b128 v[236:239], v174 offset:21504
	ds_read_b128 v[240:243], v174 offset:22528
	ds_read_b128 v[244:247], v174 offset:23552
	global_load_lds_dwordx4 v[170:171], off
	s_add_i32 m0, s28, 0x2000
	s_add_u32 s28, s40, 0x160000
	v_lshl_add_u64 v[210:211], s[40:41], 0, v[144:145]
	s_addc_u32 s29, s41, 0
	s_add_i32 s36, s48, s4
	global_load_lds_dwordx4 v[210:211], off
	v_lshl_add_u64 v[216:217], s[28:29], 0, v[184:185]
	s_mov_b32 m0, s36
	v_lshl_add_u64 v[218:219], s[42:43], 0, v[146:147]
	global_load_lds_dwordx4 v[216:217], off
	v_lshl_add_u64 v[216:217], s[28:29], 0, v[144:145]
	s_add_i32 m0, s36, 0x2000
	s_nop 0
	global_load_lds_dwordx4 v[216:217], off
	v_lshl_add_u64 v[216:217], s[42:43], 0, v[148:149]
	s_mov_b32 m0, s20
	s_nop 0
	global_load_lds_dwordx4 v[216:217], off
	s_mov_b32 m0, s21
	s_nop 0
	global_load_lds_dwordx4 v[218:219], off
	s_waitcnt vmcnt(8)
	s_waitcnt lgkmcnt(0)
	s_barrier
	s_waitcnt lgkmcnt(0)
	v_mfma_f32_16x16x32_bf16 v[60:63], v[112:115], v[202:205], v[60:63]
	v_mfma_f32_16x16x32_bf16 v[56:59], v[120:123], v[202:205], v[56:59]
	v_mfma_f32_16x16x32_bf16 v[44:47], v[112:115], v[224:227], v[44:47]
	v_mfma_f32_16x16x32_bf16 v[40:43], v[120:123], v[224:227], v[40:43]
	v_mfma_f32_16x16x32_bf16 v[36:39], v[112:115], v[232:235], v[36:39]
	v_mfma_f32_16x16x32_bf16 v[28:31], v[120:123], v[232:235], v[28:31]
	v_mfma_f32_16x16x32_bf16 v[20:23], v[112:115], v[240:243], v[20:23]
	v_mfma_f32_16x16x32_bf16 v[12:15], v[120:123], v[240:243], v[12:15]
	v_mfma_f32_16x16x32_bf16 v[60:63], v[116:119], v[206:209], v[60:63]
	v_mfma_f32_16x16x32_bf16 v[56:59], v[124:127], v[206:209], v[56:59]
	v_mfma_f32_16x16x32_bf16 v[44:47], v[116:119], v[228:231], v[44:47]
	v_mfma_f32_16x16x32_bf16 v[40:43], v[124:127], v[228:231], v[40:43]
	v_mfma_f32_16x16x32_bf16 v[36:39], v[116:119], v[236:239], v[36:39]
	v_mfma_f32_16x16x32_bf16 v[28:31], v[124:127], v[236:239], v[28:31]
	v_mfma_f32_16x16x32_bf16 v[20:23], v[116:119], v[244:247], v[20:23]
	v_mfma_f32_16x16x32_bf16 v[12:15], v[124:127], v[244:247], v[12:15]
	v_mfma_f32_16x16x32_bf16 v[52:55], v[176:179], v[202:205], v[52:55]
	v_mfma_f32_16x16x32_bf16 v[48:51], v[194:197], v[202:205], v[48:51]
	v_mfma_f32_16x16x32_bf16 v[32:35], v[176:179], v[224:227], v[32:35]
	v_mfma_f32_16x16x32_bf16 v[24:27], v[194:197], v[224:227], v[24:27]
	v_mfma_f32_16x16x32_bf16 v[16:19], v[176:179], v[232:235], v[16:19]
	v_mfma_f32_16x16x32_bf16 v[8:11], v[194:197], v[232:235], v[8:11]
	v_mfma_f32_16x16x32_bf16 v[4:7], v[176:179], v[240:243], v[4:7]
	v_mfma_f32_16x16x32_bf16 v[0:3], v[194:197], v[240:243], v[0:3]
	v_mfma_f32_16x16x32_bf16 v[52:55], v[180:183], v[206:209], v[52:55]
	v_mfma_f32_16x16x32_bf16 v[48:51], v[198:201], v[206:209], v[48:51]
	v_mfma_f32_16x16x32_bf16 v[32:35], v[180:183], v[228:231], v[32:35]
	v_mfma_f32_16x16x32_bf16 v[24:27], v[198:201], v[228:231], v[24:27]
	v_mfma_f32_16x16x32_bf16 v[16:19], v[180:183], v[236:239], v[16:19]
	v_mfma_f32_16x16x32_bf16 v[8:11], v[198:201], v[236:239], v[8:11]
	v_mfma_f32_16x16x32_bf16 v[4:7], v[180:183], v[244:247], v[4:7]
	v_mfma_f32_16x16x32_bf16 v[0:3], v[198:201], v[244:247], v[0:3]
	s_barrier
	s_add_i32 s36, 0, 0x18000
	s_add_i32 s37, 0, 0x1c000
	v_add_u32_e32 v124, s36, v172
	v_add_u32_e32 v175, s37, v172
	ds_read_b128 v[112:115], v124
	ds_read_b128 v[116:119], v124 offset:1024
	ds_read_b128 v[120:123], v124 offset:2048
	ds_read_b128 v[124:127], v124 offset:3072
	ds_read_b128 v[176:179], v175
	ds_read_b128 v[180:183], v175 offset:1024
	ds_read_b128 v[194:197], v175 offset:2048
	ds_read_b128 v[198:201], v175 offset:3072
	s_add_u32 s28, s42, 0x160000
	s_addc_u32 s29, s43, 0
	s_mov_b32 m0, s26
	v_lshl_add_u64 v[220:221], s[28:29], 0, v[148:149]
	ds_read_b128 v[202:205], v174 offset:32768
	ds_read_b128 v[206:209], v174 offset:33792
	ds_read_b128 v[224:227], v174 offset:34816
	ds_read_b128 v[228:231], v174 offset:35840
	ds_read_b128 v[232:235], v174 offset:36864
	ds_read_b128 v[236:239], v174 offset:37888
	ds_read_b128 v[240:243], v174 offset:38912
	ds_read_b128 v[244:247], v174 offset:39936
	global_load_lds_dwordx4 v[220:221], off
	v_lshl_add_u64 v[220:221], s[28:29], 0, v[146:147]
	s_mov_b32 m0, s27
	s_nop 0
	global_load_lds_dwordx4 v[220:221], off
	s_waitcnt vmcnt(8)
	s_waitcnt lgkmcnt(0)
	s_barrier
	s_waitcnt lgkmcnt(0)
	v_mfma_f32_16x16x32_bf16 v[140:143], v[112:115], v[202:205], v[140:143]
	v_mfma_f32_16x16x32_bf16 v[136:139], v[120:123], v[202:205], v[136:139]
	v_mfma_f32_16x16x32_bf16 v[108:111], v[112:115], v[224:227], v[108:111]
	v_mfma_f32_16x16x32_bf16 v[104:107], v[120:123], v[224:227], v[104:107]
	v_mfma_f32_16x16x32_bf16 v[92:95], v[112:115], v[232:235], v[92:95]
	v_mfma_f32_16x16x32_bf16 v[88:91], v[120:123], v[232:235], v[88:91]
	v_mfma_f32_16x16x32_bf16 v[76:79], v[112:115], v[240:243], v[76:79]
	v_mfma_f32_16x16x32_bf16 v[72:75], v[120:123], v[240:243], v[72:75]
	v_mfma_f32_16x16x32_bf16 v[140:143], v[116:119], v[206:209], v[140:143]
	v_mfma_f32_16x16x32_bf16 v[136:139], v[124:127], v[206:209], v[136:139]
	v_mfma_f32_16x16x32_bf16 v[108:111], v[116:119], v[228:231], v[108:111]
	v_mfma_f32_16x16x32_bf16 v[104:107], v[124:127], v[228:231], v[104:107]
	v_mfma_f32_16x16x32_bf16 v[92:95], v[116:119], v[236:239], v[92:95]
	v_mfma_f32_16x16x32_bf16 v[88:91], v[124:127], v[236:239], v[88:91]
	v_mfma_f32_16x16x32_bf16 v[76:79], v[116:119], v[244:247], v[76:79]
	v_mfma_f32_16x16x32_bf16 v[72:75], v[124:127], v[244:247], v[72:75]
	v_mfma_f32_16x16x32_bf16 v[132:135], v[176:179], v[202:205], v[132:135]
	v_mfma_f32_16x16x32_bf16 v[128:131], v[194:197], v[202:205], v[128:131]
	v_mfma_f32_16x16x32_bf16 v[100:103], v[176:179], v[224:227], v[100:103]
	v_mfma_f32_16x16x32_bf16 v[96:99], v[194:197], v[224:227], v[96:99]
	v_mfma_f32_16x16x32_bf16 v[84:87], v[176:179], v[232:235], v[84:87]
	v_mfma_f32_16x16x32_bf16 v[80:83], v[194:197], v[232:235], v[80:83]
	v_mfma_f32_16x16x32_bf16 v[68:71], v[176:179], v[240:243], v[68:71]
	v_mfma_f32_16x16x32_bf16 v[64:67], v[194:197], v[240:243], v[64:67]
	v_mfma_f32_16x16x32_bf16 v[132:135], v[180:183], v[206:209], v[132:135]
	v_mfma_f32_16x16x32_bf16 v[128:131], v[198:201], v[206:209], v[128:131]
	v_mfma_f32_16x16x32_bf16 v[100:103], v[180:183], v[228:231], v[100:103]
	v_mfma_f32_16x16x32_bf16 v[96:99], v[198:201], v[228:231], v[96:99]
	v_mfma_f32_16x16x32_bf16 v[84:87], v[180:183], v[236:239], v[84:87]
	v_mfma_f32_16x16x32_bf16 v[80:83], v[198:201], v[236:239], v[80:83]
	v_mfma_f32_16x16x32_bf16 v[68:71], v[180:183], v[244:247], v[68:71]
	v_mfma_f32_16x16x32_bf16 v[64:67], v[198:201], v[244:247], v[64:67]
	s_barrier
	s_add_i32 s28, s36, s4
	v_lshl_add_u64 v[170:171], v[170:171], 0, s[68:69]
	s_mov_b32 m0, s28
	ds_read_b128 v[202:205], v174 offset:49152
	ds_read_b128 v[206:209], v174 offset:50176
	ds_read_b128 v[224:227], v174 offset:51200
	ds_read_b128 v[228:231], v174 offset:52224
	ds_read_b128 v[232:235], v174 offset:53248
	ds_read_b128 v[236:239], v174 offset:54272
	ds_read_b128 v[240:243], v174 offset:55296
	ds_read_b128 v[244:247], v174 offset:56320
	global_load_lds_dwordx4 v[170:171], off
	s_add_i32 m0, s28, 0x2000
	s_add_u32 s28, s40, 0x160080
	v_lshl_add_u64 v[170:171], v[210:211], 0, s[68:69]
	s_addc_u32 s29, s41, 0
	s_add_i32 s36, s37, s4
	global_load_lds_dwordx4 v[170:171], off
	v_lshl_add_u64 v[170:171], s[28:29], 0, v[184:185]
	s_mov_b32 m0, s36
	s_nop 0
	global_load_lds_dwordx4 v[170:171], off
	v_lshl_add_u64 v[170:171], s[28:29], 0, v[144:145]
	s_add_i32 m0, s36, 0x2000
	s_nop 0
	global_load_lds_dwordx4 v[170:171], off
	v_lshl_add_u64 v[170:171], v[216:217], 0, s[68:69]
	s_mov_b32 m0, s44
	s_nop 0
	global_load_lds_dwordx4 v[170:171], off
	v_lshl_add_u64 v[170:171], v[218:219], 0, s[68:69]
	s_mov_b32 m0, s45
	s_nop 0
	global_load_lds_dwordx4 v[170:171], off
	s_waitcnt vmcnt(8)
	s_waitcnt lgkmcnt(0)
	s_barrier
	s_waitcnt lgkmcnt(0)
	v_mfma_f32_16x16x32_bf16 v[60:63], v[112:115], v[202:205], v[60:63]
	v_mfma_f32_16x16x32_bf16 v[56:59], v[120:123], v[202:205], v[56:59]
	v_mfma_f32_16x16x32_bf16 v[44:47], v[112:115], v[224:227], v[44:47]
	v_mfma_f32_16x16x32_bf16 v[40:43], v[120:123], v[224:227], v[40:43]
	v_mfma_f32_16x16x32_bf16 v[36:39], v[112:115], v[232:235], v[36:39]
	v_mfma_f32_16x16x32_bf16 v[28:31], v[120:123], v[232:235], v[28:31]
	v_mfma_f32_16x16x32_bf16 v[20:23], v[112:115], v[240:243], v[20:23]
	v_mfma_f32_16x16x32_bf16 v[12:15], v[120:123], v[240:243], v[12:15]
	v_mfma_f32_16x16x32_bf16 v[60:63], v[116:119], v[206:209], v[60:63]
	v_mfma_f32_16x16x32_bf16 v[56:59], v[124:127], v[206:209], v[56:59]
	v_mfma_f32_16x16x32_bf16 v[44:47], v[116:119], v[228:231], v[44:47]
	v_mfma_f32_16x16x32_bf16 v[40:43], v[124:127], v[228:231], v[40:43]
	v_mfma_f32_16x16x32_bf16 v[36:39], v[116:119], v[236:239], v[36:39]
	v_mfma_f32_16x16x32_bf16 v[28:31], v[124:127], v[236:239], v[28:31]
	v_mfma_f32_16x16x32_bf16 v[20:23], v[116:119], v[244:247], v[20:23]
	v_mfma_f32_16x16x32_bf16 v[12:15], v[124:127], v[244:247], v[12:15]
	v_mfma_f32_16x16x32_bf16 v[52:55], v[176:179], v[202:205], v[52:55]
	v_mfma_f32_16x16x32_bf16 v[48:51], v[194:197], v[202:205], v[48:51]
	v_mfma_f32_16x16x32_bf16 v[32:35], v[176:179], v[224:227], v[32:35]
	v_mfma_f32_16x16x32_bf16 v[24:27], v[194:197], v[224:227], v[24:27]
	v_mfma_f32_16x16x32_bf16 v[16:19], v[176:179], v[232:235], v[16:19]
	v_mfma_f32_16x16x32_bf16 v[8:11], v[194:197], v[232:235], v[8:11]
	v_mfma_f32_16x16x32_bf16 v[4:7], v[176:179], v[240:243], v[4:7]
	v_mfma_f32_16x16x32_bf16 v[0:3], v[194:197], v[240:243], v[0:3]
	v_mfma_f32_16x16x32_bf16 v[52:55], v[180:183], v[206:209], v[52:55]
	v_mfma_f32_16x16x32_bf16 v[48:51], v[198:201], v[206:209], v[48:51]
	v_mfma_f32_16x16x32_bf16 v[32:35], v[180:183], v[228:231], v[32:35]
	v_mfma_f32_16x16x32_bf16 v[24:27], v[198:201], v[228:231], v[24:27]
	v_mfma_f32_16x16x32_bf16 v[16:19], v[180:183], v[236:239], v[16:19]
	v_mfma_f32_16x16x32_bf16 v[8:11], v[198:201], v[236:239], v[8:11]
	v_mfma_f32_16x16x32_bf16 v[4:7], v[180:183], v[244:247], v[4:7]
	v_mfma_f32_16x16x32_bf16 v[0:3], v[198:201], v[244:247], v[0:3]
	s_barrier
	s_add_i32 s59, s59, 2
	s_add_u32 s53, s53, 0x100
	s_addc_u32 s58, s58, 0
	s_cmp_gt_u32 s59, 5
	s_mov_b64 s[36:37], s[38:39]
	s_cbranch_scc0 .LBB0_1741
	s_and_b64 vcc, exec, s[8:9]
	s_cbranch_vccz .LBB0_1744
	s_barrier
